# speedup vs baseline: 1.0129x; 1.0129x over previous
.LBB7_27:
	ds_read_b128 v[128:131], v170
	ds_read_b128 v[132:135], v170 offset:1024
	ds_read_b128 v[136:139], v170 offset:2048
	ds_read_b128 v[140:143], v170 offset:3072
	s_add_u32 s30, s28, 0xfffd0080
	s_addc_u32 s31, s29, -1
	s_cmp_eq_u32 s73, 8
	s_cselect_b32 s35, s9, s31
	s_cselect_b32 s34, s8, s30
	s_cselect_b32 s31, s1, s72
	s_cselect_b32 s30, s0, s71
	s_add_i32 m0, s43, 0xc000
	ds_read_b128 v[158:161], v171
	ds_read_b128 v[176:179], v171 offset:1024
	ds_read_b128 v[180:183], v171 offset:2048
	ds_read_b128 v[184:187], v171 offset:3072
	ds_read_b128 v[188:191], v171 offset:4096
	ds_read_b128 v[192:195], v171 offset:5120
	ds_read_b128 v[196:199], v171 offset:6144
	ds_read_b128 v[200:203], v171 offset:7168
	global_load_lds_dwordx4 v152, s[28:29]
	s_add_i32 m0, s43, 0xe000
	s_nop 0
	global_load_lds_dwordx4 v154, s[28:29]
	s_waitcnt lgkmcnt(8)
	s_barrier
	s_waitcnt lgkmcnt(0)
	s_waitcnt lgkmcnt(0)
	v_mfma_f32_16x16x32_f16 v[124:127], v[128:131], v[158:161], v[124:127]
	v_mfma_f32_16x16x32_f16 v[120:123], v[136:139], v[158:161], v[120:123]
	v_mfma_f32_16x16x32_f16 v[108:111], v[128:131], v[180:183], v[108:111]
	v_mfma_f32_16x16x32_f16 v[104:107], v[136:139], v[180:183], v[104:107]
	v_mfma_f32_16x16x32_f16 v[96:99], v[128:131], v[188:191], v[96:99]
	v_mfma_f32_16x16x32_f16 v[88:91], v[136:139], v[188:191], v[88:91]
	v_mfma_f32_16x16x32_f16 v[80:83], v[128:131], v[196:199], v[80:83]
	v_mfma_f32_16x16x32_f16 v[72:75], v[136:139], v[196:199], v[72:75]
	v_mfma_f32_16x16x32_f16 v[124:127], v[132:135], v[176:179], v[124:127]
	v_mfma_f32_16x16x32_f16 v[120:123], v[140:143], v[176:179], v[120:123]
	v_mfma_f32_16x16x32_f16 v[108:111], v[132:135], v[184:187], v[108:111]
	v_mfma_f32_16x16x32_f16 v[104:107], v[140:143], v[184:187], v[104:107]
	v_mfma_f32_16x16x32_f16 v[96:99], v[132:135], v[192:195], v[96:99]
	v_mfma_f32_16x16x32_f16 v[88:91], v[140:143], v[192:195], v[88:91]
	v_mfma_f32_16x16x32_f16 v[80:83], v[132:135], v[200:203], v[80:83]
	v_mfma_f32_16x16x32_f16 v[72:75], v[140:143], v[200:203], v[72:75]
	s_barrier
	s_add_i32 s74, s65, s42
	s_add_u32 s78, s30, 0x80
	s_addc_u32 s79, s31, 0
	s_mov_b32 m0, s74
	ds_read_b128 v[204:207], v172
	ds_read_b128 v[208:211], v172 offset:1024
	ds_read_b128 v[212:215], v172 offset:2048
	ds_read_b128 v[216:219], v172 offset:3072
	global_load_lds_dwordx4 v146, s[30:31]
	s_add_i32 m0, s74, 0x2000
	s_nop 0
	global_load_lds_dwordx4 v150, s[30:31]
	s_barrier
	s_waitcnt lgkmcnt(0)
	s_waitcnt lgkmcnt(0)
	v_mfma_f32_16x16x32_f16 v[116:119], v[204:207], v[158:161], v[116:119]
	v_mfma_f32_16x16x32_f16 v[112:115], v[212:215], v[158:161], v[112:115]
	v_mfma_f32_16x16x32_f16 v[100:103], v[204:207], v[180:183], v[100:103]
	v_mfma_f32_16x16x32_f16 v[92:95], v[212:215], v[180:183], v[92:95]
	v_mfma_f32_16x16x32_f16 v[84:87], v[204:207], v[188:191], v[84:87]
	v_mfma_f32_16x16x32_f16 v[76:79], v[212:215], v[188:191], v[76:79]
	v_mfma_f32_16x16x32_f16 v[68:71], v[204:207], v[196:199], v[68:71]
	v_mfma_f32_16x16x32_f16 v[64:67], v[212:215], v[196:199], v[64:67]
	v_mfma_f32_16x16x32_f16 v[116:119], v[208:211], v[176:179], v[116:119]
	v_mfma_f32_16x16x32_f16 v[112:115], v[216:219], v[176:179], v[112:115]
	v_mfma_f32_16x16x32_f16 v[100:103], v[208:211], v[184:187], v[100:103]
	v_mfma_f32_16x16x32_f16 v[92:95], v[216:219], v[184:187], v[92:95]
	v_mfma_f32_16x16x32_f16 v[84:87], v[208:211], v[192:195], v[84:87]
	v_mfma_f32_16x16x32_f16 v[76:79], v[216:219], v[192:195], v[76:79]
	v_mfma_f32_16x16x32_f16 v[68:71], v[208:211], v[200:203], v[68:71]
	v_mfma_f32_16x16x32_f16 v[64:67], v[216:219], v[200:203], v[64:67]
	s_mov_b32 m0, s43
	s_add_u32 s80, s34, 0x80
	s_addc_u32 s81, s35, 0
	s_barrier
	ds_read_b128 v[158:161], v171 offset:16384
	ds_read_b128 v[176:179], v171 offset:17408
	ds_read_b128 v[180:183], v171 offset:18432
	ds_read_b128 v[184:187], v171 offset:19456
	ds_read_b128 v[188:191], v171 offset:20480
	ds_read_b128 v[192:195], v171 offset:21504
	ds_read_b128 v[196:199], v171 offset:22528
	ds_read_b128 v[200:203], v171 offset:23552
	global_load_lds_dwordx4 v144, s[34:35]
	s_mov_b32 m0, s44
	s_nop 0
	global_load_lds_dwordx4 v148, s[34:35]
	s_barrier
	s_waitcnt lgkmcnt(0)
	s_waitcnt lgkmcnt(0)
	v_mfma_f32_16x16x32_f16 v[60:63], v[128:131], v[158:161], v[60:63]
	v_mfma_f32_16x16x32_f16 v[56:59], v[136:139], v[158:161], v[56:59]
	v_mfma_f32_16x16x32_f16 v[48:51], v[128:131], v[180:183], v[48:51]
	v_mfma_f32_16x16x32_f16 v[40:43], v[136:139], v[180:183], v[40:43]
	v_mfma_f32_16x16x32_f16 v[32:35], v[128:131], v[188:191], v[32:35]
	v_mfma_f32_16x16x32_f16 v[24:27], v[136:139], v[188:191], v[24:27]
	v_mfma_f32_16x16x32_f16 v[16:19], v[128:131], v[196:199], v[16:19]
	v_mfma_f32_16x16x32_f16 v[8:11], v[136:139], v[196:199], v[8:11]
	v_mfma_f32_16x16x32_f16 v[60:63], v[132:135], v[176:179], v[60:63]
	v_mfma_f32_16x16x32_f16 v[56:59], v[140:143], v[176:179], v[56:59]
	v_mfma_f32_16x16x32_f16 v[48:51], v[132:135], v[184:187], v[48:51]
	v_mfma_f32_16x16x32_f16 v[40:43], v[140:143], v[184:187], v[40:43]
	v_mfma_f32_16x16x32_f16 v[32:35], v[132:135], v[192:195], v[32:35]
	v_mfma_f32_16x16x32_f16 v[24:27], v[140:143], v[192:195], v[24:27]
	v_mfma_f32_16x16x32_f16 v[16:19], v[132:135], v[200:203], v[16:19]
	v_mfma_f32_16x16x32_f16 v[8:11], v[140:143], v[200:203], v[8:11]
	s_barrier
	s_add_u32 s74, s30, 0xc000
	s_addc_u32 s75, s31, 0
	s_add_i32 s76, s66, s42
	s_mov_b32 m0, s76
	s_nop 0
	global_load_lds_dwordx4 v146, s[74:75]
	s_add_i32 m0, s76, 0x2000
	s_nop 0
	global_load_lds_dwordx4 v150, s[74:75]
	s_waitcnt vmcnt(6)
	s_barrier
	v_mfma_f32_16x16x32_f16 v[52:55], v[204:207], v[158:161], v[52:55]
	v_mfma_f32_16x16x32_f16 v[44:47], v[212:215], v[158:161], v[44:47]
	v_mfma_f32_16x16x32_f16 v[36:39], v[204:207], v[180:183], v[36:39]
	v_mfma_f32_16x16x32_f16 v[28:31], v[212:215], v[180:183], v[28:31]
	v_mfma_f32_16x16x32_f16 v[20:23], v[204:207], v[188:191], v[20:23]
	v_mfma_f32_16x16x32_f16 v[12:15], v[212:215], v[188:191], v[12:15]
	v_mfma_f32_16x16x32_f16 v[4:7], v[204:207], v[196:199], v[4:7]
	v_mfma_f32_16x16x32_f16 v[0:3], v[212:215], v[196:199], v[0:3]
	v_mfma_f32_16x16x32_f16 v[52:55], v[208:211], v[176:179], v[52:55]
	v_mfma_f32_16x16x32_f16 v[44:47], v[216:219], v[176:179], v[44:47]
	v_mfma_f32_16x16x32_f16 v[36:39], v[208:211], v[184:187], v[36:39]
	v_mfma_f32_16x16x32_f16 v[28:31], v[216:219], v[184:187], v[28:31]
	v_mfma_f32_16x16x32_f16 v[20:23], v[208:211], v[192:195], v[20:23]
	v_mfma_f32_16x16x32_f16 v[12:15], v[216:219], v[192:195], v[12:15]
	v_mfma_f32_16x16x32_f16 v[4:7], v[208:211], v[200:203], v[4:7]
	v_mfma_f32_16x16x32_f16 v[0:3], v[216:219], v[200:203], v[0:3]
	s_add_i32 s74, 0, 0x18000
	v_add_u32_e32 v140, s74, v166
	s_barrier
	ds_read_b128 v[128:131], v140
	ds_read_b128 v[132:135], v140 offset:1024
	ds_read_b128 v[136:139], v140 offset:2048
	ds_read_b128 v[140:143], v140 offset:3072
	s_add_u32 s34, s34, 0x30000
	s_addc_u32 s35, s35, 0
	s_mov_b32 m0, s45
	ds_read_b128 v[158:161], v171 offset:32768
	ds_read_b128 v[176:179], v171 offset:33792
	ds_read_b128 v[180:183], v171 offset:34816
	ds_read_b128 v[184:187], v171 offset:35840
	ds_read_b128 v[188:191], v171 offset:36864
	ds_read_b128 v[192:195], v171 offset:37888
	ds_read_b128 v[196:199], v171 offset:38912
	ds_read_b128 v[200:203], v171 offset:39936
	global_load_lds_dwordx4 v144, s[34:35]
	s_mov_b32 m0, s46
	s_nop 0
	global_load_lds_dwordx4 v148, s[34:35]
	s_waitcnt lgkmcnt(8)
	s_barrier
	s_waitcnt lgkmcnt(0)
	s_waitcnt lgkmcnt(0)
	v_mfma_f32_16x16x32_f16 v[124:127], v[128:131], v[158:161], v[124:127]
	v_mfma_f32_16x16x32_f16 v[120:123], v[136:139], v[158:161], v[120:123]
	v_mfma_f32_16x16x32_f16 v[108:111], v[128:131], v[180:183], v[108:111]
	v_mfma_f32_16x16x32_f16 v[104:107], v[136:139], v[180:183], v[104:107]
	v_mfma_f32_16x16x32_f16 v[96:99], v[128:131], v[188:191], v[96:99]
	v_mfma_f32_16x16x32_f16 v[88:91], v[136:139], v[188:191], v[88:91]
	v_mfma_f32_16x16x32_f16 v[80:83], v[128:131], v[196:199], v[80:83]
	v_mfma_f32_16x16x32_f16 v[72:75], v[136:139], v[196:199], v[72:75]
	v_mfma_f32_16x16x32_f16 v[124:127], v[132:135], v[176:179], v[124:127]
	v_mfma_f32_16x16x32_f16 v[120:123], v[140:143], v[176:179], v[120:123]
	v_mfma_f32_16x16x32_f16 v[108:111], v[132:135], v[184:187], v[108:111]
	v_mfma_f32_16x16x32_f16 v[104:107], v[140:143], v[184:187], v[104:107]
	v_mfma_f32_16x16x32_f16 v[96:99], v[132:135], v[192:195], v[96:99]
	v_mfma_f32_16x16x32_f16 v[88:91], v[140:143], v[192:195], v[88:91]
	v_mfma_f32_16x16x32_f16 v[80:83], v[132:135], v[200:203], v[80:83]
	v_mfma_f32_16x16x32_f16 v[72:75], v[140:143], v[200:203], v[72:75]
	s_barrier
	s_add_i32 s34, 0, 0x1c000
	s_add_i32 s35, s74, s42
	v_add_u32_e32 v175, s34, v166
	s_mov_b32 m0, s35
	ds_read_b128 v[204:207], v175
	ds_read_b128 v[208:211], v175 offset:1024
	ds_read_b128 v[212:215], v175 offset:2048
	ds_read_b128 v[216:219], v175 offset:3072
	global_load_lds_dwordx4 v146, s[78:79]
	s_add_i32 m0, s35, 0x2000
	s_nop 0
	global_load_lds_dwordx4 v150, s[78:79]
	s_barrier
	s_waitcnt lgkmcnt(0)
	s_waitcnt lgkmcnt(0)
	v_mfma_f32_16x16x32_f16 v[116:119], v[204:207], v[158:161], v[116:119]
	v_mfma_f32_16x16x32_f16 v[112:115], v[212:215], v[158:161], v[112:115]
	v_mfma_f32_16x16x32_f16 v[100:103], v[204:207], v[180:183], v[100:103]
	v_mfma_f32_16x16x32_f16 v[92:95], v[212:215], v[180:183], v[92:95]
	v_mfma_f32_16x16x32_f16 v[84:87], v[204:207], v[188:191], v[84:87]
	v_mfma_f32_16x16x32_f16 v[76:79], v[212:215], v[188:191], v[76:79]
	v_mfma_f32_16x16x32_f16 v[68:71], v[204:207], v[196:199], v[68:71]
	v_mfma_f32_16x16x32_f16 v[64:67], v[212:215], v[196:199], v[64:67]
	v_mfma_f32_16x16x32_f16 v[116:119], v[208:211], v[176:179], v[116:119]
	v_mfma_f32_16x16x32_f16 v[112:115], v[216:219], v[176:179], v[112:115]
	v_mfma_f32_16x16x32_f16 v[100:103], v[208:211], v[184:187], v[100:103]
	v_mfma_f32_16x16x32_f16 v[92:95], v[216:219], v[184:187], v[92:95]
	v_mfma_f32_16x16x32_f16 v[84:87], v[208:211], v[192:195], v[84:87]
	v_mfma_f32_16x16x32_f16 v[76:79], v[216:219], v[192:195], v[76:79]
	v_mfma_f32_16x16x32_f16 v[68:71], v[208:211], v[200:203], v[68:71]
	v_mfma_f32_16x16x32_f16 v[64:67], v[216:219], v[200:203], v[64:67]
	s_mov_b32 m0, s49
	s_barrier
	ds_read_b128 v[158:161], v171 offset:49152
	ds_read_b128 v[176:179], v171 offset:50176
	ds_read_b128 v[180:183], v171 offset:51200
	ds_read_b128 v[184:187], v171 offset:52224
	ds_read_b128 v[188:191], v171 offset:53248
	ds_read_b128 v[192:195], v171 offset:54272
	ds_read_b128 v[196:199], v171 offset:55296
	ds_read_b128 v[200:203], v171 offset:56320
	global_load_lds_dwordx4 v144, s[80:81]
	s_mov_b32 m0, s50
	s_nop 0
	global_load_lds_dwordx4 v148, s[80:81]
	s_barrier
	s_waitcnt lgkmcnt(0)
	s_waitcnt lgkmcnt(0)
	v_mfma_f32_16x16x32_f16 v[60:63], v[128:131], v[158:161], v[60:63]
	v_mfma_f32_16x16x32_f16 v[56:59], v[136:139], v[158:161], v[56:59]
	v_mfma_f32_16x16x32_f16 v[48:51], v[128:131], v[180:183], v[48:51]
	v_mfma_f32_16x16x32_f16 v[40:43], v[136:139], v[180:183], v[40:43]
	v_mfma_f32_16x16x32_f16 v[32:35], v[128:131], v[188:191], v[32:35]
	v_mfma_f32_16x16x32_f16 v[24:27], v[136:139], v[188:191], v[24:27]
	v_mfma_f32_16x16x32_f16 v[16:19], v[128:131], v[196:199], v[16:19]
	v_mfma_f32_16x16x32_f16 v[8:11], v[136:139], v[196:199], v[8:11]
	v_mfma_f32_16x16x32_f16 v[60:63], v[132:135], v[176:179], v[60:63]
	v_mfma_f32_16x16x32_f16 v[56:59], v[140:143], v[176:179], v[56:59]
	v_mfma_f32_16x16x32_f16 v[48:51], v[132:135], v[184:187], v[48:51]
	v_mfma_f32_16x16x32_f16 v[40:43], v[140:143], v[184:187], v[40:43]
	v_mfma_f32_16x16x32_f16 v[32:35], v[132:135], v[192:195], v[32:35]
	v_mfma_f32_16x16x32_f16 v[24:27], v[140:143], v[192:195], v[24:27]
	v_mfma_f32_16x16x32_f16 v[16:19], v[132:135], v[200:203], v[16:19]
	v_mfma_f32_16x16x32_f16 v[8:11], v[140:143], v[200:203], v[8:11]
	s_barrier
	s_add_u32 s30, s30, 0xc080
	s_addc_u32 s31, s31, 0
	s_add_i32 s34, s34, s42
	s_mov_b32 m0, s34
	s_nop 0
	global_load_lds_dwordx4 v146, s[30:31]
	s_add_i32 m0, s34, 0x2000
	s_nop 0
	global_load_lds_dwordx4 v150, s[30:31]
	s_waitcnt vmcnt(6)
	s_barrier
	v_mfma_f32_16x16x32_f16 v[52:55], v[204:207], v[158:161], v[52:55]
	v_mfma_f32_16x16x32_f16 v[44:47], v[212:215], v[158:161], v[44:47]
	v_mfma_f32_16x16x32_f16 v[36:39], v[204:207], v[180:183], v[36:39]
	v_mfma_f32_16x16x32_f16 v[28:31], v[212:215], v[180:183], v[28:31]
	v_mfma_f32_16x16x32_f16 v[20:23], v[204:207], v[188:191], v[20:23]
	v_mfma_f32_16x16x32_f16 v[12:15], v[212:215], v[188:191], v[12:15]
	v_mfma_f32_16x16x32_f16 v[4:7], v[204:207], v[196:199], v[4:7]
	v_mfma_f32_16x16x32_f16 v[0:3], v[212:215], v[196:199], v[0:3]
	v_mfma_f32_16x16x32_f16 v[52:55], v[208:211], v[176:179], v[52:55]
	v_mfma_f32_16x16x32_f16 v[44:47], v[216:219], v[176:179], v[44:47]
	v_mfma_f32_16x16x32_f16 v[36:39], v[208:211], v[184:187], v[36:39]
	v_mfma_f32_16x16x32_f16 v[28:31], v[216:219], v[184:187], v[28:31]
	v_mfma_f32_16x16x32_f16 v[20:23], v[208:211], v[192:195], v[20:23]
	v_mfma_f32_16x16x32_f16 v[12:15], v[216:219], v[192:195], v[12:15]
	v_mfma_f32_16x16x32_f16 v[4:7], v[208:211], v[200:203], v[4:7]
	v_mfma_f32_16x16x32_f16 v[0:3], v[216:219], v[200:203], v[0:3]
	s_add_i32 s73, s73, 2
	s_add_u32 s28, s28, 0x100
	s_addc_u32 s29, s29, 0
	s_add_u32 s71, s71, 0x100
	s_addc_u32 s72, s72, 0
	s_cmp_gt_u32 s73, 9
	s_barrier
	s_cbranch_scc0 .LBB7_27
	s_lshl_b32 s28, s70, 8
	s_add_i32 s28, s28, s48
	s_lshl_b32 s29, s67, 8
	s_or_b32 s29, s29, s51
	s_waitcnt vmcnt(6)
	v_pk_fma_f32 v[126:127], v[126:127], v[226:227], v[236:237] op_sel_hi:[1,0,1]
	v_pk_fma_f32 v[124:125], v[124:125], v[226:227], v[234:235] op_sel_hi:[1,0,1]
	v_pk_fma_f32 v[186:187], v[122:123], v[226:227], v[240:241] op_sel_hi:[1,0,1]
	v_pk_fma_f32 v[122:123], v[120:121], v[226:227], v[238:239] op_sel_hi:[1,0,1]
	v_cvt_pk_f16_f32 v120, v124, v125
	v_cvt_pk_f16_f32 v121, v126, v127
	v_cvt_pk_f16_f32 v122, v122, v123
	v_cvt_pk_f16_f32 v123, v186, v187
	ds_write_b128 v173, v[120:123]
	v_pk_fma_f32 v[118:119], v[118:119], v[226:227], v[244:245] op_sel_hi:[1,0,1]
	v_pk_fma_f32 v[116:117], v[116:117], v[226:227], v[242:243] op_sel_hi:[1,0,1]
	v_pk_fma_f32 v[120:121], v[114:115], v[226:227], v[248:249] op_sel_hi:[1,0,1]
	v_pk_fma_f32 v[114:115], v[112:113], v[226:227], v[246:247] op_sel_hi:[1,0,1]
	v_cvt_pk_f16_f32 v112, v116, v117
	v_cvt_pk_f16_f32 v113, v118, v119
	v_cvt_pk_f16_f32 v114, v114, v115
	v_cvt_pk_f16_f32 v115, v120, v121
	ds_write_b128 v173, v[112:115] offset:64
	v_or_b32_e32 v116, s28, v167
	ds_read_b128 v[112:115], v174
	v_mul_lo_u32 v116, v116, s10
	v_add_u32_e32 v120, s29, v116
	v_lshlrev_b32_e32 v121, 1, v120
	v_add_u32_e32 v122, v121, v168
	ds_read_b128 v[116:119], v174 offset:1152
	s_waitcnt lgkmcnt(0)
	buffer_store_dwordx4 v[112:115], v122, s[20:23], 0 offen nt
	v_pk_fma_f32 v[110:111], v[110:111], v[226:227], v[236:237] op_sel:[0,1,0]
	v_pk_fma_f32 v[108:109], v[108:109], v[226:227], v[234:235] op_sel:[0,1,0]
	v_pk_fma_f32 v[112:113], v[106:107], v[226:227], v[240:241] op_sel:[0,1,0]
	v_pk_fma_f32 v[106:107], v[104:105], v[226:227], v[238:239] op_sel:[0,1,0]
	v_cvt_pk_f16_f32 v104, v108, v109
	v_cvt_pk_f16_f32 v105, v110, v111
	v_cvt_pk_f16_f32 v106, v106, v107
	v_cvt_pk_f16_f32 v107, v112, v113
	ds_write_b128 v173, v[104:107]
	v_pk_fma_f32 v[102:103], v[102:103], v[226:227], v[244:245] op_sel:[0,1,0]
	v_pk_fma_f32 v[100:101], v[100:101], v[226:227], v[242:243] op_sel:[0,1,0]
	v_pk_fma_f32 v[104:105], v[94:95], v[226:227], v[248:249] op_sel:[0,1,0]
	v_pk_fma_f32 v[94:95], v[92:93], v[226:227], v[246:247] op_sel:[0,1,0]
	v_cvt_pk_f16_f32 v92, v100, v101
	v_cvt_pk_f16_f32 v93, v102, v103
	v_cvt_pk_f16_f32 v94, v94, v95
	v_cvt_pk_f16_f32 v95, v104, v105
	ds_write_b128 v173, v[92:95] offset:64
	ds_read_b128 v[92:95], v174
	ds_read_b128 v[100:103], v174 offset:1152
	v_add_u32_e32 v104, s55, v121
	v_add_u32_e32 v114, v121, v169
	v_add_u32_e32 v105, v104, v168
	buffer_store_dwordx4 v[116:119], v114, s[20:23], 0 offen nt
	s_waitcnt lgkmcnt(1)
	buffer_store_dwordx4 v[92:95], v105, s[20:23], 0 offen nt
	v_pk_fma_f32 v[86:87], v[86:87], v[228:229], v[244:245] op_sel_hi:[1,0,1]
	v_pk_fma_f32 v[84:85], v[84:85], v[228:229], v[242:243] op_sel_hi:[1,0,1]
	v_pk_fma_f32 v[92:93], v[98:99], v[228:229], v[236:237] op_sel_hi:[1,0,1]
	v_pk_fma_f32 v[94:95], v[96:97], v[228:229], v[234:235] op_sel_hi:[1,0,1]
	v_pk_fma_f32 v[96:97], v[90:91], v[228:229], v[240:241] op_sel_hi:[1,0,1]
	v_pk_fma_f32 v[90:91], v[88:89], v[228:229], v[238:239] op_sel_hi:[1,0,1]
	v_cvt_pk_f16_f32 v88, v94, v95
	v_cvt_pk_f16_f32 v89, v92, v93
	v_cvt_pk_f16_f32 v90, v90, v91
	v_cvt_pk_f16_f32 v91, v96, v97
	ds_write_b128 v173, v[88:91]
	v_pk_fma_f32 v[88:89], v[78:79], v[228:229], v[248:249] op_sel_hi:[1,0,1]
	v_pk_fma_f32 v[78:79], v[76:77], v[228:229], v[246:247] op_sel_hi:[1,0,1]
	v_cvt_pk_f16_f32 v76, v84, v85
	v_cvt_pk_f16_f32 v77, v86, v87
	v_cvt_pk_f16_f32 v78, v78, v79
	v_cvt_pk_f16_f32 v79, v88, v89
	ds_write_b128 v173, v[76:79] offset:64
	ds_read_b128 v[76:79], v174
	ds_read_b128 v[84:87], v174 offset:1152
	v_add_u32_e32 v88, s55, v104
	v_add_u32_e32 v105, v104, v169
	v_add_u32_e32 v89, v88, v168
	s_waitcnt lgkmcnt(4)
	buffer_store_dwordx4 v[100:103], v105, s[20:23], 0 offen nt
	s_waitcnt lgkmcnt(1)
	buffer_store_dwordx4 v[76:79], v89, s[20:23], 0 offen nt
	v_pk_fma_f32 v[70:71], v[70:71], v[228:229], v[244:245] op_sel:[0,1,0]
	v_pk_fma_f32 v[68:69], v[68:69], v[228:229], v[242:243] op_sel:[0,1,0]
	v_add_u32_e32 v76, v88, v169
	s_waitcnt lgkmcnt(0)
	buffer_store_dwordx4 v[84:87], v76, s[20:23], 0 offen nt
	v_pk_fma_f32 v[76:77], v[82:83], v[228:229], v[236:237] op_sel:[0,1,0]
	v_pk_fma_f32 v[78:79], v[80:81], v[228:229], v[234:235] op_sel:[0,1,0]
	v_pk_fma_f32 v[80:81], v[74:75], v[228:229], v[240:241] op_sel:[0,1,0]
	v_pk_fma_f32 v[74:75], v[72:73], v[228:229], v[238:239] op_sel:[0,1,0]
	v_cvt_pk_f16_f32 v72, v78, v79
	v_cvt_pk_f16_f32 v73, v76, v77
	v_cvt_pk_f16_f32 v74, v74, v75
	v_cvt_pk_f16_f32 v75, v80, v81
	ds_write_b128 v173, v[72:75]
	v_pk_fma_f32 v[72:73], v[66:67], v[228:229], v[248:249] op_sel:[0,1,0]
	v_pk_fma_f32 v[66:67], v[64:65], v[228:229], v[246:247] op_sel:[0,1,0]
	v_cvt_pk_f16_f32 v64, v68, v69
	v_cvt_pk_f16_f32 v65, v70, v71
	v_cvt_pk_f16_f32 v66, v66, v67
	v_cvt_pk_f16_f32 v67, v72, v73
	ds_write_b128 v173, v[64:67] offset:64
	ds_read_b128 v[64:67], v174
	ds_read_b128 v[68:71], v174 offset:1152
	v_add_u32_e32 v72, s56, v120
	v_lshlrev_b32_e32 v73, 1, v72
	v_add_u32_e32 v74, v73, v168
	s_waitcnt lgkmcnt(1)
	buffer_store_dwordx4 v[64:67], v74, s[20:23], 0 offen nt
	v_pk_fma_f32 v[62:63], v[62:63], v[230:231], v[236:237] op_sel_hi:[1,0,1]
	v_pk_fma_f32 v[60:61], v[60:61], v[230:231], v[234:235] op_sel_hi:[1,0,1]
	v_pk_fma_f32 v[64:65], v[58:59], v[230:231], v[240:241] op_sel_hi:[1,0,1]
	v_pk_fma_f32 v[58:59], v[56:57], v[230:231], v[238:239] op_sel_hi:[1,0,1]
	v_cvt_pk_f16_f32 v56, v60, v61
	v_cvt_pk_f16_f32 v57, v62, v63
	v_cvt_pk_f16_f32 v58, v58, v59
	v_cvt_pk_f16_f32 v59, v64, v65
	ds_write_b128 v173, v[56:59]
	v_pk_fma_f32 v[54:55], v[54:55], v[230:231], v[244:245] op_sel_hi:[1,0,1]
	v_pk_fma_f32 v[52:53], v[52:53], v[230:231], v[242:243] op_sel_hi:[1,0,1]
	v_pk_fma_f32 v[56:57], v[46:47], v[230:231], v[248:249] op_sel_hi:[1,0,1]
	v_pk_fma_f32 v[46:47], v[44:45], v[230:231], v[246:247] op_sel_hi:[1,0,1]
	v_cvt_pk_f16_f32 v44, v52, v53
	v_cvt_pk_f16_f32 v45, v54, v55
	v_cvt_pk_f16_f32 v46, v46, v47
	v_cvt_pk_f16_f32 v47, v56, v57
	ds_write_b128 v173, v[44:47] offset:64
	ds_read_b128 v[44:47], v174
	ds_read_b128 v[52:55], v174 offset:1152
	v_add_u32_e32 v56, s62, v88
	v_add_u32_e32 v66, v73, v169
	v_add_u32_e32 v57, v56, v168
	s_waitcnt lgkmcnt(4)
	buffer_store_dwordx4 v[68:71], v66, s[20:23], 0 offen nt
	s_waitcnt lgkmcnt(1)
	buffer_store_dwordx4 v[44:47], v57, s[20:23], 0 offen nt
	v_pk_fma_f32 v[38:39], v[38:39], v[230:231], v[244:245] op_sel:[0,1,0]
	v_pk_fma_f32 v[36:37], v[36:37], v[230:231], v[242:243] op_sel:[0,1,0]
	v_add_u32_e32 v44, v56, v169
	s_waitcnt lgkmcnt(0)
	buffer_store_dwordx4 v[52:55], v44, s[20:23], 0 offen nt
	v_pk_fma_f32 v[44:45], v[50:51], v[230:231], v[236:237] op_sel:[0,1,0]
	v_pk_fma_f32 v[46:47], v[48:49], v[230:231], v[234:235] op_sel:[0,1,0]
	v_pk_fma_f32 v[48:49], v[42:43], v[230:231], v[240:241] op_sel:[0,1,0]
	v_pk_fma_f32 v[42:43], v[40:41], v[230:231], v[238:239] op_sel:[0,1,0]
	v_cvt_pk_f16_f32 v40, v46, v47
	v_cvt_pk_f16_f32 v41, v44, v45
	v_cvt_pk_f16_f32 v42, v42, v43
	v_cvt_pk_f16_f32 v43, v48, v49
	ds_write_b128 v173, v[40:43]
	v_pk_fma_f32 v[40:41], v[30:31], v[230:231], v[248:249] op_sel:[0,1,0]
	v_pk_fma_f32 v[30:31], v[28:29], v[230:231], v[246:247] op_sel:[0,1,0]
	v_cvt_pk_f16_f32 v28, v36, v37
	v_cvt_pk_f16_f32 v29, v38, v39
	v_cvt_pk_f16_f32 v30, v30, v31
	v_cvt_pk_f16_f32 v31, v40, v41
	ds_write_b128 v173, v[28:31] offset:64
	ds_read_b128 v[28:31], v174
	ds_read_b128 v[36:39], v174 offset:1152
	v_add_u32_e32 v40, s63, v72
	v_lshlrev_b32_e32 v41, 1, v40
	v_add_u32_e32 v42, v41, v168
	s_waitcnt lgkmcnt(1)
	buffer_store_dwordx4 v[28:31], v42, s[20:23], 0 offen nt
	v_pk_fma_f32 v[22:23], v[22:23], v[232:233], v[244:245] op_sel_hi:[1,0,1]
	v_pk_fma_f32 v[20:21], v[20:21], v[232:233], v[242:243] op_sel_hi:[1,0,1]
	v_add_u32_e32 v28, v41, v169
	s_waitcnt lgkmcnt(0)
	buffer_store_dwordx4 v[36:39], v28, s[20:23], 0 offen nt
	v_pk_fma_f32 v[28:29], v[34:35], v[232:233], v[236:237] op_sel_hi:[1,0,1]
	v_pk_fma_f32 v[30:31], v[32:33], v[232:233], v[234:235] op_sel_hi:[1,0,1]
	v_pk_fma_f32 v[32:33], v[26:27], v[232:233], v[240:241] op_sel_hi:[1,0,1]
	v_pk_fma_f32 v[26:27], v[24:25], v[232:233], v[238:239] op_sel_hi:[1,0,1]
	v_cvt_pk_f16_f32 v24, v30, v31
	v_cvt_pk_f16_f32 v25, v28, v29
	v_cvt_pk_f16_f32 v26, v26, v27
	v_cvt_pk_f16_f32 v27, v32, v33
	ds_write_b128 v173, v[24:27]
	v_pk_fma_f32 v[24:25], v[14:15], v[232:233], v[248:249] op_sel_hi:[1,0,1]
	v_pk_fma_f32 v[14:15], v[12:13], v[232:233], v[246:247] op_sel_hi:[1,0,1]
	v_cvt_pk_f16_f32 v12, v20, v21
	v_cvt_pk_f16_f32 v13, v22, v23
	v_cvt_pk_f16_f32 v14, v14, v15
	v_cvt_pk_f16_f32 v15, v24, v25
	ds_write_b128 v173, v[12:15] offset:64
	ds_read_b128 v[12:15], v174
	ds_read_b128 v[20:23], v174 offset:1152
	v_add_u32_e32 v24, s64, v40
	v_lshlrev_b32_e32 v25, 1, v24
	v_add_u32_e32 v26, v25, v168
	s_waitcnt lgkmcnt(1)
	buffer_store_dwordx4 v[12:15], v26, s[20:23], 0 offen nt
	v_pk_fma_f32 v[6:7], v[6:7], v[232:233], v[244:245] op_sel:[0,1,0]
	v_pk_fma_f32 v[4:5], v[4:5], v[232:233], v[242:243] op_sel:[0,1,0]
	v_pk_fma_f32 v[12:13], v[18:19], v[232:233], v[236:237] op_sel:[0,1,0]
	v_pk_fma_f32 v[14:15], v[16:17], v[232:233], v[234:235] op_sel:[0,1,0]
	v_pk_fma_f32 v[16:17], v[10:11], v[232:233], v[240:241] op_sel:[0,1,0]
	v_pk_fma_f32 v[10:11], v[8:9], v[232:233], v[238:239] op_sel:[0,1,0]
	v_cvt_pk_f16_f32 v8, v14, v15
	v_cvt_pk_f16_f32 v9, v12, v13
	v_cvt_pk_f16_f32 v10, v10, v11
	v_cvt_pk_f16_f32 v11, v16, v17
	ds_write_b128 v173, v[8:11]
	v_pk_fma_f32 v[8:9], v[2:3], v[232:233], v[248:249] op_sel:[0,1,0]
	v_pk_fma_f32 v[2:3], v[0:1], v[232:233], v[246:247] op_sel:[0,1,0]
	v_cvt_pk_f16_f32 v0, v4, v5
	v_cvt_pk_f16_f32 v1, v6, v7
	v_cvt_pk_f16_f32 v2, v2, v3
	v_cvt_pk_f16_f32 v3, v8, v9
	ds_write_b128 v173, v[0:3] offset:64
	ds_read_b128 v[0:3], v174
	ds_read_b128 v[4:7], v174 offset:1152
	v_add_lshl_u32 v8, v24, s64, 1
	v_add_u32_e32 v25, v25, v169
	v_add_u32_e32 v9, v8, v168
	s_waitcnt lgkmcnt(4)
	buffer_store_dwordx4 v[20:23], v25, s[20:23], 0 offen nt
	s_waitcnt lgkmcnt(1)
	buffer_store_dwordx4 v[0:3], v9, s[20:23], 0 offen nt
	s_mov_b32 s67, s68
	s_mov_b32 s70, s69
	v_add_u32_e32 v0, v8, v169
	s_mov_b64 s[30:31], s[0:1]
	s_mov_b64 s[28:29], s[8:9]
	s_mov_b64 vcc, s[6:7]
	s_waitcnt lgkmcnt(0)
	buffer_store_dwordx4 v[4:7], v0, s[20:23], 0 offen nt
	s_cbranch_vccz .LBB7_12
	s_waitcnt vmcnt(0)
	s_cmpk_gt_u32 s36, 0xff
	s_cbranch_scc1 .LBB7_31
	s_barrier

.LBB7_32:
	s_endpgm
	s_endpgm
	s_endpgm
	s_endpgm
	s_endpgm
	s_endpgm
	s_endpgm
	s_endpgm
	s_endpgm
	s_endpgm
	s_endpgm
	s_endpgm
	s_endpgm
	s_endpgm
	s_endpgm
	s_endpgm
	s_endpgm
	s_endpgm
	s_endpgm
	s_endpgm
	s_endpgm
	s_endpgm
	s_endpgm
	s_endpgm
	s_endpgm
	s_endpgm
	s_endpgm
	s_endpgm
	s_endpgm
	s_endpgm
	s_endpgm

	.amdhsa_kernel _Z6k_gemmIN2pg6EpiLinILi0EEELi768EEvNS0_4GemmET_
		.amdhsa_group_segment_fixed_size 0
		.amdhsa_private_segment_fixed_size 0
		.amdhsa_kernarg_size 320
		.amdhsa_user_sgpr_count 2
		.amdhsa_user_sgpr_dispatch_ptr 0
		.amdhsa_user_sgpr_queue_ptr 0
		.amdhsa_user_sgpr_kernarg_segment_ptr 1
		.amdhsa_user_sgpr_dispatch_id 0
		.amdhsa_user_sgpr_kernarg_preload_length 0
		.amdhsa_user_sgpr_kernarg_preload_offset 0
		.amdhsa_user_sgpr_private_segment_size 0
		.amdhsa_uses_dynamic_stack 0
		.amdhsa_enable_private_segment 0
		.amdhsa_system_sgpr_workgroup_id_x 1
		.amdhsa_system_sgpr_workgroup_id_y 0
		.amdhsa_system_sgpr_workgroup_id_z 0
		.amdhsa_system_sgpr_workgroup_info 0
		.amdhsa_system_vgpr_workitem_id 0
		.amdhsa_next_free_vgpr 254
		.amdhsa_next_free_sgpr 82
		.amdhsa_accum_offset 256
		.amdhsa_reserve_vcc 1
		.amdhsa_float_round_mode_32 0
		.amdhsa_float_round_mode_16_64 0
		.amdhsa_float_denorm_mode_32 3
		.amdhsa_float_denorm_mode_16_64 3
		.amdhsa_dx10_clamp 1
		.amdhsa_ieee_mode 1
		.amdhsa_fp16_overflow 0
		.amdhsa_tg_split 0
		.amdhsa_exception_fp_ieee_invalid_op 0
		.amdhsa_exception_fp_denorm_src 0
		.amdhsa_exception_fp_ieee_div_zero 0
		.amdhsa_exception_fp_ieee_overflow 0
		.amdhsa_exception_fp_ieee_underflow 0
		.amdhsa_exception_fp_ieee_inexact 0
		.amdhsa_exception_int_div_zero 0
	.end_amdhsa_kernel

.LBB8_27:
	ds_read_b128 v[72:75], v231
	ds_read_b128 v[80:83], v231 offset:1024
	ds_read_b128 v[88:91], v231 offset:2048
	ds_read_b128 v[92:95], v231 offset:3072
	s_add_u32 s40, s38, 0xfffd0080
	s_addc_u32 s41, s39, -1
	s_cmp_eq_u32 s87, 8
	s_cselect_b32 s43, s9, s41
	s_cselect_b32 s42, s8, s40
	s_cselect_b32 s41, s1, s86
	s_cselect_b32 s40, s0, s85
	s_add_i32 m0, s51, 0xc000
	ds_read_b128 v[136:139], v232
	ds_read_b128 v[148:151], v232 offset:1024
	ds_read_b128 v[152:155], v232 offset:2048
	ds_read_b128 v[156:159], v232 offset:3072
	ds_read_b128 v[160:163], v232 offset:4096
	ds_read_b128 v[164:167], v232 offset:5120
	ds_read_b128 v[168:171], v232 offset:6144
	ds_read_b128 v[172:175], v232 offset:7168
	global_load_lds_dwordx4 v184, s[38:39]
	s_add_i32 m0, s51, 0xe000
	s_nop 0
	global_load_lds_dwordx4 v186, s[38:39]
	s_waitcnt lgkmcnt(8)
	s_barrier
	s_waitcnt lgkmcnt(0)
	s_waitcnt lgkmcnt(0)
	v_mfma_f32_16x16x32_f16 v[144:147], v[72:75], v[136:139], v[144:147]
	v_mfma_f32_16x16x32_f16 v[140:143], v[88:91], v[136:139], v[140:143]
	v_mfma_f32_16x16x32_f16 v[124:127], v[72:75], v[152:155], v[124:127]
	v_mfma_f32_16x16x32_f16 v[120:123], v[88:91], v[152:155], v[120:123]
	v_mfma_f32_16x16x32_f16 v[108:111], v[72:75], v[160:163], v[108:111]
	v_mfma_f32_16x16x32_f16 v[104:107], v[88:91], v[160:163], v[104:107]
	v_mfma_f32_16x16x32_f16 v[84:87], v[72:75], v[168:171], v[84:87]
	v_mfma_f32_16x16x32_f16 v[76:79], v[88:91], v[168:171], v[76:79]
	v_mfma_f32_16x16x32_f16 v[144:147], v[80:83], v[148:151], v[144:147]
	v_mfma_f32_16x16x32_f16 v[140:143], v[92:95], v[148:151], v[140:143]
	v_mfma_f32_16x16x32_f16 v[124:127], v[80:83], v[156:159], v[124:127]
	v_mfma_f32_16x16x32_f16 v[120:123], v[92:95], v[156:159], v[120:123]
	v_mfma_f32_16x16x32_f16 v[108:111], v[80:83], v[164:167], v[108:111]
	v_mfma_f32_16x16x32_f16 v[104:107], v[92:95], v[164:167], v[104:107]
	v_mfma_f32_16x16x32_f16 v[84:87], v[80:83], v[172:175], v[84:87]
	v_mfma_f32_16x16x32_f16 v[76:79], v[92:95], v[172:175], v[76:79]
	s_barrier
	s_add_i32 s88, s70, s50
	s_add_u32 s92, s40, 0x80
	s_addc_u32 s93, s41, 0
	s_mov_b32 m0, s88
	ds_read_b128 v[190:193], v233
	ds_read_b128 v[194:197], v233 offset:1024
	ds_read_b128 v[198:201], v233 offset:2048
	ds_read_b128 v[202:205], v233 offset:3072
	global_load_lds_dwordx4 v178, s[40:41]
	s_add_i32 m0, s88, 0x2000
	s_nop 0
	global_load_lds_dwordx4 v182, s[40:41]
	s_barrier
	s_waitcnt lgkmcnt(0)
	s_waitcnt lgkmcnt(0)
	v_mfma_f32_16x16x32_f16 v[132:135], v[190:193], v[136:139], v[132:135]
	v_mfma_f32_16x16x32_f16 v[128:131], v[198:201], v[136:139], v[128:131]
	v_mfma_f32_16x16x32_f16 v[116:119], v[190:193], v[152:155], v[116:119]
	v_mfma_f32_16x16x32_f16 v[112:115], v[198:201], v[152:155], v[112:115]
	v_mfma_f32_16x16x32_f16 v[100:103], v[190:193], v[160:163], v[100:103]
	v_mfma_f32_16x16x32_f16 v[96:99], v[198:201], v[160:163], v[96:99]
	v_mfma_f32_16x16x32_f16 v[68:71], v[190:193], v[168:171], v[68:71]
	v_mfma_f32_16x16x32_f16 v[64:67], v[198:201], v[168:171], v[64:67]
	v_mfma_f32_16x16x32_f16 v[132:135], v[194:197], v[148:151], v[132:135]
	v_mfma_f32_16x16x32_f16 v[128:131], v[202:205], v[148:151], v[128:131]
	v_mfma_f32_16x16x32_f16 v[116:119], v[194:197], v[156:159], v[116:119]
	v_mfma_f32_16x16x32_f16 v[112:115], v[202:205], v[156:159], v[112:115]
	v_mfma_f32_16x16x32_f16 v[100:103], v[194:197], v[164:167], v[100:103]
	v_mfma_f32_16x16x32_f16 v[96:99], v[202:205], v[164:167], v[96:99]
	v_mfma_f32_16x16x32_f16 v[68:71], v[194:197], v[172:175], v[68:71]
	v_mfma_f32_16x16x32_f16 v[64:67], v[202:205], v[172:175], v[64:67]
	s_mov_b32 m0, s51
	s_add_u32 s94, s42, 0x80
	s_addc_u32 s95, s43, 0
	s_barrier
	ds_read_b128 v[136:139], v232 offset:16384
	ds_read_b128 v[148:151], v232 offset:17408
	ds_read_b128 v[152:155], v232 offset:18432
	ds_read_b128 v[156:159], v232 offset:19456
	ds_read_b128 v[160:163], v232 offset:20480
	ds_read_b128 v[164:167], v232 offset:21504
	ds_read_b128 v[168:171], v232 offset:22528
	ds_read_b128 v[172:175], v232 offset:23552
	global_load_lds_dwordx4 v176, s[42:43]
	s_mov_b32 m0, s52
	s_nop 0
	global_load_lds_dwordx4 v180, s[42:43]
	s_barrier
	s_waitcnt lgkmcnt(0)
	s_waitcnt lgkmcnt(0)
	v_mfma_f32_16x16x32_f16 v[60:63], v[72:75], v[136:139], v[60:63]
	v_mfma_f32_16x16x32_f16 v[56:59], v[88:91], v[136:139], v[56:59]
	v_mfma_f32_16x16x32_f16 v[44:47], v[72:75], v[152:155], v[44:47]
	v_mfma_f32_16x16x32_f16 v[40:43], v[88:91], v[152:155], v[40:43]
	v_mfma_f32_16x16x32_f16 v[28:31], v[72:75], v[160:163], v[28:31]
	v_mfma_f32_16x16x32_f16 v[24:27], v[88:91], v[160:163], v[24:27]
	v_mfma_f32_16x16x32_f16 v[12:15], v[72:75], v[168:171], v[12:15]
	v_mfma_f32_16x16x32_f16 v[8:11], v[88:91], v[168:171], v[8:11]
	v_mfma_f32_16x16x32_f16 v[60:63], v[80:83], v[148:151], v[60:63]
	v_mfma_f32_16x16x32_f16 v[56:59], v[92:95], v[148:151], v[56:59]
	v_mfma_f32_16x16x32_f16 v[44:47], v[80:83], v[156:159], v[44:47]
	v_mfma_f32_16x16x32_f16 v[40:43], v[92:95], v[156:159], v[40:43]
	v_mfma_f32_16x16x32_f16 v[28:31], v[80:83], v[164:167], v[28:31]
	v_mfma_f32_16x16x32_f16 v[24:27], v[92:95], v[164:167], v[24:27]
	v_mfma_f32_16x16x32_f16 v[12:15], v[80:83], v[172:175], v[12:15]
	v_mfma_f32_16x16x32_f16 v[8:11], v[92:95], v[172:175], v[8:11]
	s_barrier
	s_add_u32 s88, s40, 0xc000
	s_addc_u32 s89, s41, 0
	s_add_i32 s90, s71, s50
	s_mov_b32 m0, s90
	s_nop 0
	global_load_lds_dwordx4 v178, s[88:89]
	s_add_i32 m0, s90, 0x2000
	s_nop 0
	global_load_lds_dwordx4 v182, s[88:89]
	s_waitcnt vmcnt(6)
	s_barrier
	v_mfma_f32_16x16x32_f16 v[52:55], v[190:193], v[136:139], v[52:55]
	v_mfma_f32_16x16x32_f16 v[48:51], v[198:201], v[136:139], v[48:51]
	v_mfma_f32_16x16x32_f16 v[36:39], v[190:193], v[152:155], v[36:39]
	v_mfma_f32_16x16x32_f16 v[32:35], v[198:201], v[152:155], v[32:35]
	v_mfma_f32_16x16x32_f16 v[20:23], v[190:193], v[160:163], v[20:23]
	v_mfma_f32_16x16x32_f16 v[16:19], v[198:201], v[160:163], v[16:19]
	v_mfma_f32_16x16x32_f16 v[4:7], v[190:193], v[168:171], v[4:7]
	v_mfma_f32_16x16x32_f16 v[0:3], v[198:201], v[168:171], v[0:3]
	v_mfma_f32_16x16x32_f16 v[52:55], v[194:197], v[148:151], v[52:55]
	v_mfma_f32_16x16x32_f16 v[48:51], v[202:205], v[148:151], v[48:51]
	v_mfma_f32_16x16x32_f16 v[36:39], v[194:197], v[156:159], v[36:39]
	v_mfma_f32_16x16x32_f16 v[32:35], v[202:205], v[156:159], v[32:35]
	v_mfma_f32_16x16x32_f16 v[20:23], v[194:197], v[164:167], v[20:23]
	v_mfma_f32_16x16x32_f16 v[16:19], v[202:205], v[164:167], v[16:19]
	v_mfma_f32_16x16x32_f16 v[4:7], v[194:197], v[172:175], v[4:7]
	v_mfma_f32_16x16x32_f16 v[0:3], v[202:205], v[172:175], v[0:3]
	s_add_i32 s88, 0, 0x18000
	v_add_u32_e32 v92, s88, v228
	s_barrier
	ds_read_b128 v[72:75], v92
	ds_read_b128 v[80:83], v92 offset:1024
	ds_read_b128 v[88:91], v92 offset:2048
	ds_read_b128 v[92:95], v92 offset:3072
	s_add_u32 s42, s42, 0x30000
	s_addc_u32 s43, s43, 0
	s_mov_b32 m0, s53
	ds_read_b128 v[136:139], v232 offset:32768
	ds_read_b128 v[148:151], v232 offset:33792
	ds_read_b128 v[152:155], v232 offset:34816
	ds_read_b128 v[156:159], v232 offset:35840
	ds_read_b128 v[160:163], v232 offset:36864
	ds_read_b128 v[164:167], v232 offset:37888
	ds_read_b128 v[168:171], v232 offset:38912
	ds_read_b128 v[172:175], v232 offset:39936
	global_load_lds_dwordx4 v176, s[42:43]
	s_mov_b32 m0, s54
	s_nop 0
	global_load_lds_dwordx4 v180, s[42:43]
	s_waitcnt lgkmcnt(8)
	s_barrier
	s_waitcnt lgkmcnt(0)
	s_waitcnt lgkmcnt(0)
	v_mfma_f32_16x16x32_f16 v[144:147], v[72:75], v[136:139], v[144:147]
	v_mfma_f32_16x16x32_f16 v[140:143], v[88:91], v[136:139], v[140:143]
	v_mfma_f32_16x16x32_f16 v[124:127], v[72:75], v[152:155], v[124:127]
	v_mfma_f32_16x16x32_f16 v[120:123], v[88:91], v[152:155], v[120:123]
	v_mfma_f32_16x16x32_f16 v[108:111], v[72:75], v[160:163], v[108:111]
	v_mfma_f32_16x16x32_f16 v[104:107], v[88:91], v[160:163], v[104:107]
	v_mfma_f32_16x16x32_f16 v[84:87], v[72:75], v[168:171], v[84:87]
	v_mfma_f32_16x16x32_f16 v[76:79], v[88:91], v[168:171], v[76:79]
	v_mfma_f32_16x16x32_f16 v[144:147], v[80:83], v[148:151], v[144:147]
	v_mfma_f32_16x16x32_f16 v[140:143], v[92:95], v[148:151], v[140:143]
	v_mfma_f32_16x16x32_f16 v[124:127], v[80:83], v[156:159], v[124:127]
	v_mfma_f32_16x16x32_f16 v[120:123], v[92:95], v[156:159], v[120:123]
	v_mfma_f32_16x16x32_f16 v[108:111], v[80:83], v[164:167], v[108:111]
	v_mfma_f32_16x16x32_f16 v[104:107], v[92:95], v[164:167], v[104:107]
	v_mfma_f32_16x16x32_f16 v[84:87], v[80:83], v[172:175], v[84:87]
	v_mfma_f32_16x16x32_f16 v[76:79], v[92:95], v[172:175], v[76:79]
	s_barrier
	s_add_i32 s42, 0, 0x1c000
	s_add_i32 s43, s88, s50
	v_add_u32_e32 v202, s42, v228
	s_mov_b32 m0, s43
	ds_read_b128 v[190:193], v202
	ds_read_b128 v[194:197], v202 offset:1024
	ds_read_b128 v[198:201], v202 offset:2048
	ds_read_b128 v[202:205], v202 offset:3072
	global_load_lds_dwordx4 v178, s[92:93]
	s_add_i32 m0, s43, 0x2000
	s_nop 0
	global_load_lds_dwordx4 v182, s[92:93]
	s_barrier
	s_waitcnt lgkmcnt(0)
	s_waitcnt lgkmcnt(0)
	v_mfma_f32_16x16x32_f16 v[132:135], v[190:193], v[136:139], v[132:135]
	v_mfma_f32_16x16x32_f16 v[128:131], v[198:201], v[136:139], v[128:131]
	v_mfma_f32_16x16x32_f16 v[116:119], v[190:193], v[152:155], v[116:119]
	v_mfma_f32_16x16x32_f16 v[112:115], v[198:201], v[152:155], v[112:115]
	v_mfma_f32_16x16x32_f16 v[100:103], v[190:193], v[160:163], v[100:103]
	v_mfma_f32_16x16x32_f16 v[96:99], v[198:201], v[160:163], v[96:99]
	v_mfma_f32_16x16x32_f16 v[68:71], v[190:193], v[168:171], v[68:71]
	v_mfma_f32_16x16x32_f16 v[64:67], v[198:201], v[168:171], v[64:67]
	v_mfma_f32_16x16x32_f16 v[132:135], v[194:197], v[148:151], v[132:135]
	v_mfma_f32_16x16x32_f16 v[128:131], v[202:205], v[148:151], v[128:131]
	v_mfma_f32_16x16x32_f16 v[116:119], v[194:197], v[156:159], v[116:119]
	v_mfma_f32_16x16x32_f16 v[112:115], v[202:205], v[156:159], v[112:115]
	v_mfma_f32_16x16x32_f16 v[100:103], v[194:197], v[164:167], v[100:103]
	v_mfma_f32_16x16x32_f16 v[96:99], v[202:205], v[164:167], v[96:99]
	v_mfma_f32_16x16x32_f16 v[68:71], v[194:197], v[172:175], v[68:71]
	v_mfma_f32_16x16x32_f16 v[64:67], v[202:205], v[172:175], v[64:67]
	s_mov_b32 m0, s59
	s_barrier
	ds_read_b128 v[136:139], v232 offset:49152
	ds_read_b128 v[148:151], v232 offset:50176
	ds_read_b128 v[152:155], v232 offset:51200
	ds_read_b128 v[156:159], v232 offset:52224
	ds_read_b128 v[160:163], v232 offset:53248
	ds_read_b128 v[164:167], v232 offset:54272
	ds_read_b128 v[168:171], v232 offset:55296
	ds_read_b128 v[172:175], v232 offset:56320
	global_load_lds_dwordx4 v176, s[94:95]
	s_mov_b32 m0, s60
	s_nop 0
	global_load_lds_dwordx4 v180, s[94:95]
	s_barrier
	s_waitcnt lgkmcnt(0)
	s_waitcnt lgkmcnt(0)
	v_mfma_f32_16x16x32_f16 v[60:63], v[72:75], v[136:139], v[60:63]
	v_mfma_f32_16x16x32_f16 v[56:59], v[88:91], v[136:139], v[56:59]
	v_mfma_f32_16x16x32_f16 v[44:47], v[72:75], v[152:155], v[44:47]
	v_mfma_f32_16x16x32_f16 v[40:43], v[88:91], v[152:155], v[40:43]
	v_mfma_f32_16x16x32_f16 v[28:31], v[72:75], v[160:163], v[28:31]
	v_mfma_f32_16x16x32_f16 v[24:27], v[88:91], v[160:163], v[24:27]
	v_mfma_f32_16x16x32_f16 v[12:15], v[72:75], v[168:171], v[12:15]
	v_mfma_f32_16x16x32_f16 v[8:11], v[88:91], v[168:171], v[8:11]
	v_mfma_f32_16x16x32_f16 v[60:63], v[80:83], v[148:151], v[60:63]
	v_mfma_f32_16x16x32_f16 v[56:59], v[92:95], v[148:151], v[56:59]
	v_mfma_f32_16x16x32_f16 v[44:47], v[80:83], v[156:159], v[44:47]
	v_mfma_f32_16x16x32_f16 v[40:43], v[92:95], v[156:159], v[40:43]
	v_mfma_f32_16x16x32_f16 v[28:31], v[80:83], v[164:167], v[28:31]
	v_mfma_f32_16x16x32_f16 v[24:27], v[92:95], v[164:167], v[24:27]
	v_mfma_f32_16x16x32_f16 v[12:15], v[80:83], v[172:175], v[12:15]
	v_mfma_f32_16x16x32_f16 v[8:11], v[92:95], v[172:175], v[8:11]
	s_barrier
	s_add_u32 s40, s40, 0xc080
	s_addc_u32 s41, s41, 0
	s_add_i32 s42, s42, s50
	s_mov_b32 m0, s42
	s_nop 0
	global_load_lds_dwordx4 v178, s[40:41]
	s_add_i32 m0, s42, 0x2000
	s_nop 0
	global_load_lds_dwordx4 v182, s[40:41]
	s_waitcnt vmcnt(6)
	s_barrier
	v_mfma_f32_16x16x32_f16 v[52:55], v[190:193], v[136:139], v[52:55]
	v_mfma_f32_16x16x32_f16 v[48:51], v[198:201], v[136:139], v[48:51]
	v_mfma_f32_16x16x32_f16 v[36:39], v[190:193], v[152:155], v[36:39]
	v_mfma_f32_16x16x32_f16 v[32:35], v[198:201], v[152:155], v[32:35]
	v_mfma_f32_16x16x32_f16 v[20:23], v[190:193], v[160:163], v[20:23]
	v_mfma_f32_16x16x32_f16 v[16:19], v[198:201], v[160:163], v[16:19]
	v_mfma_f32_16x16x32_f16 v[4:7], v[190:193], v[168:171], v[4:7]
	v_mfma_f32_16x16x32_f16 v[0:3], v[198:201], v[168:171], v[0:3]
	v_mfma_f32_16x16x32_f16 v[52:55], v[194:197], v[148:151], v[52:55]
	v_mfma_f32_16x16x32_f16 v[48:51], v[202:205], v[148:151], v[48:51]
	v_mfma_f32_16x16x32_f16 v[36:39], v[194:197], v[156:159], v[36:39]
	v_mfma_f32_16x16x32_f16 v[32:35], v[202:205], v[156:159], v[32:35]
	v_mfma_f32_16x16x32_f16 v[20:23], v[194:197], v[164:167], v[20:23]
	v_mfma_f32_16x16x32_f16 v[16:19], v[202:205], v[164:167], v[16:19]
	v_mfma_f32_16x16x32_f16 v[4:7], v[194:197], v[172:175], v[4:7]
	v_mfma_f32_16x16x32_f16 v[0:3], v[202:205], v[172:175], v[0:3]
	s_add_i32 s87, s87, 2
	s_add_u32 s38, s38, 0x100
	s_addc_u32 s39, s39, 0
	s_add_u32 s85, s85, 0x100
	s_addc_u32 s86, s86, 0
	s_cmp_gt_u32 s87, 9
	s_barrier
	s_cbranch_scc0 .LBB8_27
	s_lshl_b32 s92, s84, 8
	s_add_i32 s92, s92, s58
	s_lshl_b32 s93, s83, 8
	s_or_b32 s93, s93, s61
	v_lshlrev_b32_e32 v237, 2, v226
	s_lshl_b32 s96, s93, 2
	s_add_u32 s94, s16, s96
	s_addc_u32 s95, s17, 0
	global_load_dwordx4 v[72:75], v237, s[94:95] offset:0
	global_load_dwordx4 v[80:83], v237, s[94:95] offset:16
	global_load_dwordx4 v[88:91], v237, s[94:95] offset:128
	global_load_dwordx4 v[92:95], v237, s[94:95] offset:144
	s_add_u32 s94, s18, s96
	s_addc_u32 s95, s19, 0
	global_load_dwordx4 v[136:139], v237, s[94:95] offset:0
	global_load_dwordx4 v[148:151], v237, s[94:95] offset:16
	global_load_dwordx4 v[152:155], v237, s[94:95] offset:128
	global_load_dwordx4 v[156:159], v237, s[94:95] offset:144
	s_add_u32 s94, s14, s96
	s_addc_u32 s95, s15, 0
	global_load_dwordx4 v[160:163], v237, s[94:95] offset:0
	global_load_dwordx4 v[164:167], v237, s[94:95] offset:16
	global_load_dwordx4 v[168:171], v237, s[94:95] offset:128
	global_load_dwordx4 v[172:175], v237, s[94:95] offset:144
	v_lshlrev_b32_e32 v190, 3, v227
	s_lshl_b32 s96, s92, 3
	s_add_u32 s94, s12, s96
	s_addc_u32 s95, s13, 0
	global_load_dwordx2 v[238:239], v190, s[94:95] offset:0
	global_load_dwordx2 v[192:193], v190, s[94:95] offset:128
	global_load_dwordx2 v[194:195], v190, s[94:95] offset:256
	global_load_dwordx2 v[196:197], v190, s[94:95] offset:384
	global_load_dwordx2 v[198:199], v190, s[94:95] offset:1024
	global_load_dwordx2 v[200:201], v190, s[94:95] offset:1152
	global_load_dwordx2 v[202:203], v190, s[94:95] offset:1280
	global_load_dwordx2 v[204:205], v190, s[94:95] offset:1408
	v_mul_u32_u24_e32 v191, 0x600, v227
	v_lshl_add_u32 v191, v226, 1, v191
	s_mul_i32 s96, s92, 0x600
	s_lshl_b32 s97, s93, 1
	s_add_u32 s96, s96, s97
	s_add_u32 s98, s10, s96
	s_addc_u32 s99, s11, 0
	s_add_u32 s94, s98, 0x0
	s_addc_u32 s95, s99, 0
	global_load_dwordx4 v[208:211], v191, s[94:95] offset:0 nt
	global_load_dwordx4 v[212:215], v191, s[94:95] offset:64 nt
	s_add_u32 s94, s98, 0x6000
	s_addc_u32 s95, s99, 0
	global_load_dwordx4 v[216:219], v191, s[94:95] offset:0 nt
	global_load_dwordx4 v[220:223], v191, s[94:95] offset:64 nt
	v_add_u32_e32 v224, s92, v229
	v_mul_u32_u24_e32 v224, 0x600, v224
	s_lshl_b32 s97, s93, 1
	v_add3_u32 v224, v224, v230, s97
	s_lshl_b32 s96, s83, 2
	s_lshr_b32 s97, s61, 6
	s_add_u32 s96, s96, s97
	s_lshl_b32 s96, s96, 19
	s_lshl_b32 s97, s92, 3
	s_add_u32 s96, s96, s97
	s_add_u32 s100, s28, s96
	s_addc_u32 s101, s29, 0
	s_waitcnt vmcnt(19)
	v_pk_add_f32 v[72:73], v[72:73], v[136:137]
	v_pk_add_f32 v[74:75], v[74:75], v[138:139]
	s_waitcnt vmcnt(18)
	v_pk_add_f32 v[80:81], v[80:81], v[148:149]
	v_pk_add_f32 v[82:83], v[82:83], v[150:151]
	s_waitcnt vmcnt(17)
	v_pk_add_f32 v[88:89], v[88:89], v[152:153]
	v_pk_add_f32 v[90:91], v[90:91], v[154:155]
	s_waitcnt vmcnt(16)
	v_pk_add_f32 v[92:93], v[92:93], v[156:157]
	v_pk_add_f32 v[94:95], v[94:95], v[158:159]
	v_pk_add_f32 v[144:145], v[144:145], v[72:73]
	v_pk_add_f32 v[146:147], v[146:147], v[74:75]
	v_pk_add_f32 v[124:125], v[124:125], v[72:73]
	v_pk_add_f32 v[126:127], v[126:127], v[74:75]
	v_pk_add_f32 v[108:109], v[108:109], v[72:73]
	v_pk_add_f32 v[110:111], v[110:111], v[74:75]
	v_pk_add_f32 v[84:85], v[84:85], v[72:73]
	v_pk_add_f32 v[86:87], v[86:87], v[74:75]
	v_pk_add_f32 v[60:61], v[60:61], v[72:73]
	v_pk_add_f32 v[62:63], v[62:63], v[74:75]
	v_pk_add_f32 v[44:45], v[44:45], v[72:73]
	v_pk_add_f32 v[46:47], v[46:47], v[74:75]
	v_pk_add_f32 v[28:29], v[28:29], v[72:73]
	v_pk_add_f32 v[30:31], v[30:31], v[74:75]
	v_pk_add_f32 v[12:13], v[12:13], v[72:73]
	v_pk_add_f32 v[14:15], v[14:15], v[74:75]
	v_pk_add_f32 v[140:141], v[140:141], v[80:81]
	v_pk_add_f32 v[142:143], v[142:143], v[82:83]
	v_pk_add_f32 v[120:121], v[120:121], v[80:81]
	v_pk_add_f32 v[122:123], v[122:123], v[82:83]
	v_pk_add_f32 v[104:105], v[104:105], v[80:81]
	v_pk_add_f32 v[106:107], v[106:107], v[82:83]
	v_pk_add_f32 v[76:77], v[76:77], v[80:81]
	v_pk_add_f32 v[78:79], v[78:79], v[82:83]
	v_pk_add_f32 v[56:57], v[56:57], v[80:81]
	v_pk_add_f32 v[58:59], v[58:59], v[82:83]
	v_pk_add_f32 v[40:41], v[40:41], v[80:81]
	v_pk_add_f32 v[42:43], v[42:43], v[82:83]
	v_pk_add_f32 v[24:25], v[24:25], v[80:81]
	v_pk_add_f32 v[26:27], v[26:27], v[82:83]
	v_pk_add_f32 v[8:9], v[8:9], v[80:81]
	v_pk_add_f32 v[10:11], v[10:11], v[82:83]
	v_pk_add_f32 v[132:133], v[132:133], v[88:89]
	v_pk_add_f32 v[134:135], v[134:135], v[90:91]
	v_pk_add_f32 v[116:117], v[116:117], v[88:89]
	v_pk_add_f32 v[118:119], v[118:119], v[90:91]
	v_pk_add_f32 v[100:101], v[100:101], v[88:89]
	v_pk_add_f32 v[102:103], v[102:103], v[90:91]
	v_pk_add_f32 v[68:69], v[68:69], v[88:89]
	v_pk_add_f32 v[70:71], v[70:71], v[90:91]
	v_pk_add_f32 v[52:53], v[52:53], v[88:89]
	v_pk_add_f32 v[54:55], v[54:55], v[90:91]
	v_pk_add_f32 v[36:37], v[36:37], v[88:89]
	v_pk_add_f32 v[38:39], v[38:39], v[90:91]
	v_pk_add_f32 v[20:21], v[20:21], v[88:89]
	v_pk_add_f32 v[22:23], v[22:23], v[90:91]
	v_pk_add_f32 v[4:5], v[4:5], v[88:89]
	v_pk_add_f32 v[6:7], v[6:7], v[90:91]
	v_pk_add_f32 v[128:129], v[128:129], v[92:93]
	v_pk_add_f32 v[130:131], v[130:131], v[94:95]
	v_pk_add_f32 v[112:113], v[112:113], v[92:93]
	v_pk_add_f32 v[114:115], v[114:115], v[94:95]
	v_pk_add_f32 v[96:97], v[96:97], v[92:93]
	v_pk_add_f32 v[98:99], v[98:99], v[94:95]
	v_pk_add_f32 v[64:65], v[64:65], v[92:93]
	v_pk_add_f32 v[66:67], v[66:67], v[94:95]
	v_pk_add_f32 v[48:49], v[48:49], v[92:93]
	v_pk_add_f32 v[50:51], v[50:51], v[94:95]
	v_pk_add_f32 v[32:33], v[32:33], v[92:93]
	v_pk_add_f32 v[34:35], v[34:35], v[94:95]
	v_pk_add_f32 v[16:17], v[16:17], v[92:93]
	v_pk_add_f32 v[18:19], v[18:19], v[94:95]
	v_pk_add_f32 v[0:1], v[0:1], v[92:93]
	v_pk_add_f32 v[2:3], v[2:3], v[94:95]
	s_add_u32 s94, s98, 0xc000
	s_addc_u32 s95, s99, 0
	global_load_dwordx4 v[240:243], v191, s[94:95] offset:0 nt
	global_load_dwordx4 v[244:247], v191, s[94:95] offset:64 nt
	s_add_u32 s94, s98, 0x12000
	s_addc_u32 s95, s99, 0
	global_load_dwordx4 v[248:251], v191, s[94:95] offset:0 nt
	global_load_dwordx4 v[252:255], v191, s[94:95] offset:64 nt
	s_add_u32 s94, s98, 0x30000
	s_addc_u32 s95, s99, 0
	global_load_dwordx4 v[136:139], v191, s[94:95] offset:0 nt
	global_load_dwordx4 v[148:151], v191, s[94:95] offset:64 nt
	s_add_u32 s94, s98, 0x36000
	s_addc_u32 s95, s99, 0
	global_load_dwordx4 v[152:155], v191, s[94:95] offset:0 nt
	global_load_dwordx4 v[156:159], v191, s[94:95] offset:64 nt
	s_waitcnt vmcnt(19)
	s_waitcnt vmcnt(11)
	v_cvt_f32_f16_e32 v72, v208
	v_cvt_f32_f16_sdwa v73, v208 dst_sel:DWORD dst_unused:UNUSED_PAD src0_sel:WORD_1
	v_cvt_f32_f16_e32 v74, v209
	v_cvt_f32_f16_sdwa v75, v209 dst_sel:DWORD dst_unused:UNUSED_PAD src0_sel:WORD_1
	v_cvt_f32_f16_e32 v80, v210
	v_cvt_f32_f16_sdwa v81, v210 dst_sel:DWORD dst_unused:UNUSED_PAD src0_sel:WORD_1
	v_cvt_f32_f16_e32 v82, v211
	v_cvt_f32_f16_sdwa v83, v211 dst_sel:DWORD dst_unused:UNUSED_PAD src0_sel:WORD_1
	v_sub_f32_e32 v72, v72, v238
	v_sub_f32_e32 v73, v73, v238
	v_sub_f32_e32 v74, v74, v238
	v_sub_f32_e32 v75, v75, v238
	v_sub_f32_e32 v80, v80, v238
	v_sub_f32_e32 v81, v81, v238
	v_sub_f32_e32 v82, v82, v238
	v_sub_f32_e32 v83, v83, v238
	v_pk_mul_f32 v[72:73], v[238:239], v[72:73] op_sel:[1,0]
	v_pk_mul_f32 v[74:75], v[238:239], v[74:75] op_sel:[1,0]
	v_pk_mul_f32 v[80:81], v[238:239], v[80:81] op_sel:[1,0]
	v_pk_mul_f32 v[82:83], v[238:239], v[82:83] op_sel:[1,0]
	v_pk_fma_f32 v[144:145], v[72:73], v[160:161], v[144:145]
	v_pk_fma_f32 v[146:147], v[74:75], v[162:163], v[146:147]
	v_pk_fma_f32 v[140:141], v[80:81], v[164:165], v[140:141]
	v_pk_fma_f32 v[142:143], v[82:83], v[166:167], v[142:143]
	v_cvt_pk_f16_f32 v144, v144, v145
	v_cvt_pk_f16_f32 v145, v146, v147
	v_cvt_pk_f16_f32 v146, v140, v141
	v_cvt_pk_f16_f32 v147, v142, v143
	ds_write_b128 v235, v[144:147]
	v_fma_mix_f32 v206, v144, 1.0, 0 op_sel_hi:[1,0,0]
	v_fma_mix_f32 v207, v144, v144, 0 op_sel_hi:[1,1,0]
	v_fma_mix_f32 v206, v144, 1.0, v206 op_sel:[1,0,0] op_sel_hi:[1,0,0]
	v_fma_mix_f32 v207, v144, v144, v207 op_sel:[1,1,0] op_sel_hi:[1,1,0]
	v_fma_mix_f32 v206, v145, 1.0, v206 op_sel_hi:[1,0,0]
	v_fma_mix_f32 v207, v145, v145, v207 op_sel_hi:[1,1,0]
	v_fma_mix_f32 v206, v145, 1.0, v206 op_sel:[1,0,0] op_sel_hi:[1,0,0]
	v_fma_mix_f32 v207, v145, v145, v207 op_sel:[1,1,0] op_sel_hi:[1,1,0]
	v_fma_mix_f32 v206, v146, 1.0, v206 op_sel_hi:[1,0,0]
	v_fma_mix_f32 v207, v146, v146, v207 op_sel_hi:[1,1,0]
	v_fma_mix_f32 v206, v146, 1.0, v206 op_sel:[1,0,0] op_sel_hi:[1,0,0]
	v_fma_mix_f32 v207, v146, v146, v207 op_sel:[1,1,0] op_sel_hi:[1,1,0]
	v_fma_mix_f32 v206, v147, 1.0, v206 op_sel_hi:[1,0,0]
	v_fma_mix_f32 v207, v147, v147, v207 op_sel_hi:[1,1,0]
	v_fma_mix_f32 v206, v147, 1.0, v206 op_sel:[1,0,0] op_sel_hi:[1,0,0]
	v_fma_mix_f32 v207, v147, v147, v207 op_sel:[1,1,0] op_sel_hi:[1,1,0]
	s_waitcnt vmcnt(10)
	v_cvt_f32_f16_e32 v72, v212
	v_cvt_f32_f16_sdwa v73, v212 dst_sel:DWORD dst_unused:UNUSED_PAD src0_sel:WORD_1
	v_cvt_f32_f16_e32 v74, v213
	v_cvt_f32_f16_sdwa v75, v213 dst_sel:DWORD dst_unused:UNUSED_PAD src0_sel:WORD_1
	v_cvt_f32_f16_e32 v80, v214
	v_cvt_f32_f16_sdwa v81, v214 dst_sel:DWORD dst_unused:UNUSED_PAD src0_sel:WORD_1
	v_cvt_f32_f16_e32 v82, v215
	v_cvt_f32_f16_sdwa v83, v215 dst_sel:DWORD dst_unused:UNUSED_PAD src0_sel:WORD_1
	v_sub_f32_e32 v72, v72, v238
	v_sub_f32_e32 v73, v73, v238
	v_sub_f32_e32 v74, v74, v238
	v_sub_f32_e32 v75, v75, v238
	v_sub_f32_e32 v80, v80, v238
	v_sub_f32_e32 v81, v81, v238
	v_sub_f32_e32 v82, v82, v238
	v_sub_f32_e32 v83, v83, v238
	v_pk_mul_f32 v[72:73], v[238:239], v[72:73] op_sel:[1,0]
	v_pk_mul_f32 v[74:75], v[238:239], v[74:75] op_sel:[1,0]
	v_pk_mul_f32 v[80:81], v[238:239], v[80:81] op_sel:[1,0]
	v_pk_mul_f32 v[82:83], v[238:239], v[82:83] op_sel:[1,0]
	v_pk_fma_f32 v[132:133], v[72:73], v[168:169], v[132:133]
	v_pk_fma_f32 v[134:135], v[74:75], v[170:171], v[134:135]
	v_pk_fma_f32 v[128:129], v[80:81], v[172:173], v[128:129]
	v_pk_fma_f32 v[130:131], v[82:83], v[174:175], v[130:131]
	v_cvt_pk_f16_f32 v132, v132, v133
	v_cvt_pk_f16_f32 v133, v134, v135
	v_cvt_pk_f16_f32 v134, v128, v129
	v_cvt_pk_f16_f32 v135, v130, v131
	ds_write_b128 v235, v[132:135] offset:64
	v_fma_mix_f32 v206, v132, 1.0, v206 op_sel_hi:[1,0,0]
	v_fma_mix_f32 v207, v132, v132, v207 op_sel_hi:[1,1,0]
	v_fma_mix_f32 v206, v132, 1.0, v206 op_sel:[1,0,0] op_sel_hi:[1,0,0]
	v_fma_mix_f32 v207, v132, v132, v207 op_sel:[1,1,0] op_sel_hi:[1,1,0]
	v_fma_mix_f32 v206, v133, 1.0, v206 op_sel_hi:[1,0,0]
	v_fma_mix_f32 v207, v133, v133, v207 op_sel_hi:[1,1,0]
	v_fma_mix_f32 v206, v133, 1.0, v206 op_sel:[1,0,0] op_sel_hi:[1,0,0]
	v_fma_mix_f32 v207, v133, v133, v207 op_sel:[1,1,0] op_sel_hi:[1,1,0]
	v_fma_mix_f32 v206, v134, 1.0, v206 op_sel_hi:[1,0,0]
	v_fma_mix_f32 v207, v134, v134, v207 op_sel_hi:[1,1,0]
	v_fma_mix_f32 v206, v134, 1.0, v206 op_sel:[1,0,0] op_sel_hi:[1,0,0]
	v_fma_mix_f32 v207, v134, v134, v207 op_sel:[1,1,0] op_sel_hi:[1,1,0]
	v_fma_mix_f32 v206, v135, 1.0, v206 op_sel_hi:[1,0,0]
	v_fma_mix_f32 v207, v135, v135, v207 op_sel_hi:[1,1,0]
	v_fma_mix_f32 v206, v135, 1.0, v206 op_sel:[1,0,0] op_sel_hi:[1,0,0]
	v_fma_mix_f32 v207, v135, v135, v207 op_sel:[1,1,0] op_sel_hi:[1,1,0]
	ds_read_b128 v[88:91], v236
	ds_read_b128 v[92:95], v236 offset:1152
	s_waitcnt vmcnt(9)
	v_cvt_f32_f16_e32 v72, v216
	v_cvt_f32_f16_sdwa v73, v216 dst_sel:DWORD dst_unused:UNUSED_PAD src0_sel:WORD_1
	v_cvt_f32_f16_e32 v74, v217
	v_cvt_f32_f16_sdwa v75, v217 dst_sel:DWORD dst_unused:UNUSED_PAD src0_sel:WORD_1
	v_cvt_f32_f16_e32 v80, v218
	v_cvt_f32_f16_sdwa v81, v218 dst_sel:DWORD dst_unused:UNUSED_PAD src0_sel:WORD_1
	v_cvt_f32_f16_e32 v82, v219
	v_cvt_f32_f16_sdwa v83, v219 dst_sel:DWORD dst_unused:UNUSED_PAD src0_sel:WORD_1
	v_sub_f32_e32 v72, v72, v192
	v_sub_f32_e32 v73, v73, v192
	v_sub_f32_e32 v74, v74, v192
	v_sub_f32_e32 v75, v75, v192
	v_sub_f32_e32 v80, v80, v192
	v_sub_f32_e32 v81, v81, v192
	v_sub_f32_e32 v82, v82, v192
	v_sub_f32_e32 v83, v83, v192
	v_pk_mul_f32 v[72:73], v[192:193], v[72:73] op_sel:[1,0]
	v_pk_mul_f32 v[74:75], v[192:193], v[74:75] op_sel:[1,0]
	v_pk_mul_f32 v[80:81], v[192:193], v[80:81] op_sel:[1,0]
	v_pk_mul_f32 v[82:83], v[192:193], v[82:83] op_sel:[1,0]
	v_pk_fma_f32 v[124:125], v[72:73], v[160:161], v[124:125]
	v_pk_fma_f32 v[126:127], v[74:75], v[162:163], v[126:127]
	v_pk_fma_f32 v[120:121], v[80:81], v[164:165], v[120:121]
	v_pk_fma_f32 v[122:123], v[82:83], v[166:167], v[122:123]
	v_cvt_pk_f16_f32 v124, v124, v125
	v_cvt_pk_f16_f32 v125, v126, v127
	v_cvt_pk_f16_f32 v126, v120, v121
	v_cvt_pk_f16_f32 v127, v122, v123
	s_waitcnt lgkmcnt(0)
	buffer_store_dwordx4 v[88:91], v224, s[24:27], 0 offen nt
	v_add_u32_e32 v82, 0x3000, v224
	buffer_store_dwordx4 v[92:95], v82, s[24:27], 0 offen nt
	ds_write_b128 v235, v[124:127]
	v_fma_mix_f32 v140, v124, 1.0, 0 op_sel_hi:[1,0,0]
	v_fma_mix_f32 v141, v124, v124, 0 op_sel_hi:[1,1,0]
	v_fma_mix_f32 v140, v124, 1.0, v140 op_sel:[1,0,0] op_sel_hi:[1,0,0]
	v_fma_mix_f32 v141, v124, v124, v141 op_sel:[1,1,0] op_sel_hi:[1,1,0]
	v_fma_mix_f32 v140, v125, 1.0, v140 op_sel_hi:[1,0,0]
	v_fma_mix_f32 v141, v125, v125, v141 op_sel_hi:[1,1,0]
	v_fma_mix_f32 v140, v125, 1.0, v140 op_sel:[1,0,0] op_sel_hi:[1,0,0]
	v_fma_mix_f32 v141, v125, v125, v141 op_sel:[1,1,0] op_sel_hi:[1,1,0]
	v_fma_mix_f32 v140, v126, 1.0, v140 op_sel_hi:[1,0,0]
	v_fma_mix_f32 v141, v126, v126, v141 op_sel_hi:[1,1,0]
	v_fma_mix_f32 v140, v126, 1.0, v140 op_sel:[1,0,0] op_sel_hi:[1,0,0]
	v_fma_mix_f32 v141, v126, v126, v141 op_sel:[1,1,0] op_sel_hi:[1,1,0]
	v_fma_mix_f32 v140, v127, 1.0, v140 op_sel_hi:[1,0,0]
	v_fma_mix_f32 v141, v127, v127, v141 op_sel_hi:[1,1,0]
	v_fma_mix_f32 v140, v127, 1.0, v140 op_sel:[1,0,0] op_sel_hi:[1,0,0]
	v_fma_mix_f32 v141, v127, v127, v141 op_sel:[1,1,0] op_sel_hi:[1,1,0]
	s_waitcnt vmcnt(10)
	v_cvt_f32_f16_e32 v72, v220
	v_cvt_f32_f16_sdwa v73, v220 dst_sel:DWORD dst_unused:UNUSED_PAD src0_sel:WORD_1
	v_cvt_f32_f16_e32 v74, v221
	v_cvt_f32_f16_sdwa v75, v221 dst_sel:DWORD dst_unused:UNUSED_PAD src0_sel:WORD_1
	v_cvt_f32_f16_e32 v80, v222
	v_cvt_f32_f16_sdwa v81, v222 dst_sel:DWORD dst_unused:UNUSED_PAD src0_sel:WORD_1
	v_cvt_f32_f16_e32 v82, v223
	v_cvt_f32_f16_sdwa v83, v223 dst_sel:DWORD dst_unused:UNUSED_PAD src0_sel:WORD_1
	v_sub_f32_e32 v72, v72, v192
	v_sub_f32_e32 v73, v73, v192
	v_sub_f32_e32 v74, v74, v192
	v_sub_f32_e32 v75, v75, v192
	v_sub_f32_e32 v80, v80, v192
	v_sub_f32_e32 v81, v81, v192
	v_sub_f32_e32 v82, v82, v192
	v_sub_f32_e32 v83, v83, v192
	v_pk_mul_f32 v[72:73], v[192:193], v[72:73] op_sel:[1,0]
	v_pk_mul_f32 v[74:75], v[192:193], v[74:75] op_sel:[1,0]
	v_pk_mul_f32 v[80:81], v[192:193], v[80:81] op_sel:[1,0]
	v_pk_mul_f32 v[82:83], v[192:193], v[82:83] op_sel:[1,0]
	v_pk_fma_f32 v[116:117], v[72:73], v[168:169], v[116:117]
	v_pk_fma_f32 v[118:119], v[74:75], v[170:171], v[118:119]
	v_pk_fma_f32 v[112:113], v[80:81], v[172:173], v[112:113]
	v_pk_fma_f32 v[114:115], v[82:83], v[174:175], v[114:115]
	v_cvt_pk_f16_f32 v116, v116, v117
	v_cvt_pk_f16_f32 v117, v118, v119
	v_cvt_pk_f16_f32 v118, v112, v113
	v_cvt_pk_f16_f32 v119, v114, v115
	ds_write_b128 v235, v[116:119] offset:64
	v_fma_mix_f32 v140, v116, 1.0, v140 op_sel_hi:[1,0,0]
	v_fma_mix_f32 v141, v116, v116, v141 op_sel_hi:[1,1,0]
	v_fma_mix_f32 v140, v116, 1.0, v140 op_sel:[1,0,0] op_sel_hi:[1,0,0]
	v_fma_mix_f32 v141, v116, v116, v141 op_sel:[1,1,0] op_sel_hi:[1,1,0]
	v_fma_mix_f32 v140, v117, 1.0, v140 op_sel_hi:[1,0,0]
	v_fma_mix_f32 v141, v117, v117, v141 op_sel_hi:[1,1,0]
	v_fma_mix_f32 v140, v117, 1.0, v140 op_sel:[1,0,0] op_sel_hi:[1,0,0]
	v_fma_mix_f32 v141, v117, v117, v141 op_sel:[1,1,0] op_sel_hi:[1,1,0]
	v_fma_mix_f32 v140, v118, 1.0, v140 op_sel_hi:[1,0,0]
	v_fma_mix_f32 v141, v118, v118, v141 op_sel_hi:[1,1,0]
	v_fma_mix_f32 v140, v118, 1.0, v140 op_sel:[1,0,0] op_sel_hi:[1,0,0]
	v_fma_mix_f32 v141, v118, v118, v141 op_sel:[1,1,0] op_sel_hi:[1,1,0]
	v_fma_mix_f32 v140, v119, 1.0, v140 op_sel_hi:[1,0,0]
	v_fma_mix_f32 v141, v119, v119, v141 op_sel_hi:[1,1,0]
	v_fma_mix_f32 v140, v119, 1.0, v140 op_sel:[1,0,0] op_sel_hi:[1,0,0]
	v_fma_mix_f32 v141, v119, v119, v141 op_sel:[1,1,0] op_sel_hi:[1,1,0]
	ds_read_b128 v[208:211], v236
	ds_read_b128 v[128:131], v236 offset:1152
	s_add_u32 s94, s98, 0x3c000
	s_addc_u32 s95, s99, 0
	global_load_dwordx4 v[212:215], v191, s[94:95] offset:0 nt
	global_load_dwordx4 v[144:147], v191, s[94:95] offset:64 nt
	s_add_u32 s94, s98, 0x42000
	s_addc_u32 s95, s99, 0
	global_load_dwordx4 v[132:135], v191, s[94:95] offset:0 nt
	global_load_dwordx4 v[88:91], v191, s[94:95] offset:64 nt
	s_waitcnt vmcnt(13)
	v_cvt_f32_f16_e32 v72, v240
	v_cvt_f32_f16_sdwa v73, v240 dst_sel:DWORD dst_unused:UNUSED_PAD src0_sel:WORD_1
	v_cvt_f32_f16_e32 v74, v241
	v_cvt_f32_f16_sdwa v75, v241 dst_sel:DWORD dst_unused:UNUSED_PAD src0_sel:WORD_1
	v_cvt_f32_f16_e32 v80, v242
	v_cvt_f32_f16_sdwa v81, v242 dst_sel:DWORD dst_unused:UNUSED_PAD src0_sel:WORD_1
	v_cvt_f32_f16_e32 v82, v243
	v_cvt_f32_f16_sdwa v83, v243 dst_sel:DWORD dst_unused:UNUSED_PAD src0_sel:WORD_1
	v_sub_f32_e32 v72, v72, v194
	v_sub_f32_e32 v73, v73, v194
	v_sub_f32_e32 v74, v74, v194
	v_sub_f32_e32 v75, v75, v194
	v_sub_f32_e32 v80, v80, v194
	v_sub_f32_e32 v81, v81, v194
	v_sub_f32_e32 v82, v82, v194
	v_sub_f32_e32 v83, v83, v194
	v_pk_mul_f32 v[72:73], v[194:195], v[72:73] op_sel:[1,0]
	v_pk_mul_f32 v[74:75], v[194:195], v[74:75] op_sel:[1,0]
	v_pk_mul_f32 v[80:81], v[194:195], v[80:81] op_sel:[1,0]
	v_pk_mul_f32 v[82:83], v[194:195], v[82:83] op_sel:[1,0]
	v_pk_fma_f32 v[108:109], v[72:73], v[160:161], v[108:109]
	v_pk_fma_f32 v[110:111], v[74:75], v[162:163], v[110:111]
	v_pk_fma_f32 v[104:105], v[80:81], v[164:165], v[104:105]
	v_pk_fma_f32 v[106:107], v[82:83], v[166:167], v[106:107]
	v_cvt_pk_f16_f32 v108, v108, v109
	v_cvt_pk_f16_f32 v109, v110, v111
	v_cvt_pk_f16_f32 v110, v104, v105
	v_cvt_pk_f16_f32 v111, v106, v107
	s_waitcnt lgkmcnt(0)
	v_add_u32_e32 v83, 0x6000, v224
	buffer_store_dwordx4 v[208:211], v83, s[24:27], 0 offen nt
	v_add_u32_e32 v82, 0x9000, v224
	buffer_store_dwordx4 v[128:131], v82, s[24:27], 0 offen nt
	ds_write_b128 v235, v[108:111]
	v_fma_mix_f32 v142, v108, 1.0, 0 op_sel_hi:[1,0,0]
	v_fma_mix_f32 v143, v108, v108, 0 op_sel_hi:[1,1,0]
	v_fma_mix_f32 v142, v108, 1.0, v142 op_sel:[1,0,0] op_sel_hi:[1,0,0]
	v_fma_mix_f32 v143, v108, v108, v143 op_sel:[1,1,0] op_sel_hi:[1,1,0]
	v_fma_mix_f32 v142, v109, 1.0, v142 op_sel_hi:[1,0,0]
	v_fma_mix_f32 v143, v109, v109, v143 op_sel_hi:[1,1,0]
	v_fma_mix_f32 v142, v109, 1.0, v142 op_sel:[1,0,0] op_sel_hi:[1,0,0]
	v_fma_mix_f32 v143, v109, v109, v143 op_sel:[1,1,0] op_sel_hi:[1,1,0]
	v_fma_mix_f32 v142, v110, 1.0, v142 op_sel_hi:[1,0,0]
	v_fma_mix_f32 v143, v110, v110, v143 op_sel_hi:[1,1,0]
	v_fma_mix_f32 v142, v110, 1.0, v142 op_sel:[1,0,0] op_sel_hi:[1,0,0]
	v_fma_mix_f32 v143, v110, v110, v143 op_sel:[1,1,0] op_sel_hi:[1,1,0]
	v_fma_mix_f32 v142, v111, 1.0, v142 op_sel_hi:[1,0,0]
	v_fma_mix_f32 v143, v111, v111, v143 op_sel_hi:[1,1,0]
	v_fma_mix_f32 v142, v111, 1.0, v142 op_sel:[1,0,0] op_sel_hi:[1,0,0]
	v_fma_mix_f32 v143, v111, v111, v143 op_sel:[1,1,0] op_sel_hi:[1,1,0]
	s_waitcnt vmcnt(14)
	v_cvt_f32_f16_e32 v72, v244
	v_cvt_f32_f16_sdwa v73, v244 dst_sel:DWORD dst_unused:UNUSED_PAD src0_sel:WORD_1
	v_cvt_f32_f16_e32 v74, v245
	v_cvt_f32_f16_sdwa v75, v245 dst_sel:DWORD dst_unused:UNUSED_PAD src0_sel:WORD_1
	v_cvt_f32_f16_e32 v80, v246
	v_cvt_f32_f16_sdwa v81, v246 dst_sel:DWORD dst_unused:UNUSED_PAD src0_sel:WORD_1
	v_cvt_f32_f16_e32 v82, v247
	v_cvt_f32_f16_sdwa v83, v247 dst_sel:DWORD dst_unused:UNUSED_PAD src0_sel:WORD_1
	v_sub_f32_e32 v72, v72, v194
	v_sub_f32_e32 v73, v73, v194
	v_sub_f32_e32 v74, v74, v194
	v_sub_f32_e32 v75, v75, v194
	v_sub_f32_e32 v80, v80, v194
	v_sub_f32_e32 v81, v81, v194
	v_sub_f32_e32 v82, v82, v194
	v_sub_f32_e32 v83, v83, v194
	v_pk_mul_f32 v[72:73], v[194:195], v[72:73] op_sel:[1,0]
	v_pk_mul_f32 v[74:75], v[194:195], v[74:75] op_sel:[1,0]
	v_pk_mul_f32 v[80:81], v[194:195], v[80:81] op_sel:[1,0]
	v_pk_mul_f32 v[82:83], v[194:195], v[82:83] op_sel:[1,0]
	v_pk_fma_f32 v[100:101], v[72:73], v[168:169], v[100:101]
	v_pk_fma_f32 v[102:103], v[74:75], v[170:171], v[102:103]
	v_pk_fma_f32 v[96:97], v[80:81], v[172:173], v[96:97]
	v_pk_fma_f32 v[98:99], v[82:83], v[174:175], v[98:99]
	v_cvt_pk_f16_f32 v100, v100, v101
	v_cvt_pk_f16_f32 v101, v102, v103
	v_cvt_pk_f16_f32 v102, v96, v97
	v_cvt_pk_f16_f32 v103, v98, v99
	ds_write_b128 v235, v[100:103] offset:64
	v_fma_mix_f32 v142, v100, 1.0, v142 op_sel_hi:[1,0,0]
	v_fma_mix_f32 v143, v100, v100, v143 op_sel_hi:[1,1,0]
	v_fma_mix_f32 v142, v100, 1.0, v142 op_sel:[1,0,0] op_sel_hi:[1,0,0]
	v_fma_mix_f32 v143, v100, v100, v143 op_sel:[1,1,0] op_sel_hi:[1,1,0]
	v_fma_mix_f32 v142, v101, 1.0, v142 op_sel_hi:[1,0,0]
	v_fma_mix_f32 v143, v101, v101, v143 op_sel_hi:[1,1,0]
	v_fma_mix_f32 v142, v101, 1.0, v142 op_sel:[1,0,0] op_sel_hi:[1,0,0]
	v_fma_mix_f32 v143, v101, v101, v143 op_sel:[1,1,0] op_sel_hi:[1,1,0]
	v_fma_mix_f32 v142, v102, 1.0, v142 op_sel_hi:[1,0,0]
	v_fma_mix_f32 v143, v102, v102, v143 op_sel_hi:[1,1,0]
	v_fma_mix_f32 v142, v102, 1.0, v142 op_sel:[1,0,0] op_sel_hi:[1,0,0]
	v_fma_mix_f32 v143, v102, v102, v143 op_sel:[1,1,0] op_sel_hi:[1,1,0]
	v_fma_mix_f32 v142, v103, 1.0, v142 op_sel_hi:[1,0,0]
	v_fma_mix_f32 v143, v103, v103, v143 op_sel_hi:[1,1,0]
	v_fma_mix_f32 v142, v103, 1.0, v142 op_sel:[1,0,0] op_sel_hi:[1,0,0]
	v_fma_mix_f32 v143, v103, v103, v143 op_sel:[1,1,0] op_sel_hi:[1,1,0]
	ds_read_b128 v[92:95], v236
	ds_read_b128 v[120:123], v236 offset:1152
	s_waitcnt vmcnt(13)
	v_cvt_f32_f16_e32 v72, v248
	v_cvt_f32_f16_sdwa v73, v248 dst_sel:DWORD dst_unused:UNUSED_PAD src0_sel:WORD_1
	v_cvt_f32_f16_e32 v74, v249
	v_cvt_f32_f16_sdwa v75, v249 dst_sel:DWORD dst_unused:UNUSED_PAD src0_sel:WORD_1
	v_cvt_f32_f16_e32 v80, v250
	v_cvt_f32_f16_sdwa v81, v250 dst_sel:DWORD dst_unused:UNUSED_PAD src0_sel:WORD_1
	v_cvt_f32_f16_e32 v82, v251
	v_cvt_f32_f16_sdwa v83, v251 dst_sel:DWORD dst_unused:UNUSED_PAD src0_sel:WORD_1
	v_sub_f32_e32 v72, v72, v196
	v_sub_f32_e32 v73, v73, v196
	v_sub_f32_e32 v74, v74, v196
	v_sub_f32_e32 v75, v75, v196
	v_sub_f32_e32 v80, v80, v196
	v_sub_f32_e32 v81, v81, v196
	v_sub_f32_e32 v82, v82, v196
	v_sub_f32_e32 v83, v83, v196
	v_pk_mul_f32 v[72:73], v[196:197], v[72:73] op_sel:[1,0]
	v_pk_mul_f32 v[74:75], v[196:197], v[74:75] op_sel:[1,0]
	v_pk_mul_f32 v[80:81], v[196:197], v[80:81] op_sel:[1,0]
	v_pk_mul_f32 v[82:83], v[196:197], v[82:83] op_sel:[1,0]
	v_pk_fma_f32 v[84:85], v[72:73], v[160:161], v[84:85]
	v_pk_fma_f32 v[86:87], v[74:75], v[162:163], v[86:87]
	v_pk_fma_f32 v[76:77], v[80:81], v[164:165], v[76:77]
	v_pk_fma_f32 v[78:79], v[82:83], v[166:167], v[78:79]
	v_cvt_pk_f16_f32 v84, v84, v85
	v_cvt_pk_f16_f32 v85, v86, v87
	v_cvt_pk_f16_f32 v86, v76, v77
	v_cvt_pk_f16_f32 v87, v78, v79
	s_waitcnt lgkmcnt(0)
	v_add_u32_e32 v83, 0xc000, v224
	buffer_store_dwordx4 v[92:95], v83, s[24:27], 0 offen nt
	v_add_u32_e32 v82, 0xf000, v224
	buffer_store_dwordx4 v[120:123], v82, s[24:27], 0 offen nt
	ds_write_b128 v235, v[84:87]
	v_fma_mix_f32 v216, v84, 1.0, 0 op_sel_hi:[1,0,0]
	v_fma_mix_f32 v217, v84, v84, 0 op_sel_hi:[1,1,0]
	v_fma_mix_f32 v216, v84, 1.0, v216 op_sel:[1,0,0] op_sel_hi:[1,0,0]
	v_fma_mix_f32 v217, v84, v84, v217 op_sel:[1,1,0] op_sel_hi:[1,1,0]
	v_fma_mix_f32 v216, v85, 1.0, v216 op_sel_hi:[1,0,0]
	v_fma_mix_f32 v217, v85, v85, v217 op_sel_hi:[1,1,0]
	v_fma_mix_f32 v216, v85, 1.0, v216 op_sel:[1,0,0] op_sel_hi:[1,0,0]
	v_fma_mix_f32 v217, v85, v85, v217 op_sel:[1,1,0] op_sel_hi:[1,1,0]
	v_fma_mix_f32 v216, v86, 1.0, v216 op_sel_hi:[1,0,0]
	v_fma_mix_f32 v217, v86, v86, v217 op_sel_hi:[1,1,0]
	v_fma_mix_f32 v216, v86, 1.0, v216 op_sel:[1,0,0] op_sel_hi:[1,0,0]
	v_fma_mix_f32 v217, v86, v86, v217 op_sel:[1,1,0] op_sel_hi:[1,1,0]
	v_fma_mix_f32 v216, v87, 1.0, v216 op_sel_hi:[1,0,0]
	v_fma_mix_f32 v217, v87, v87, v217 op_sel_hi:[1,1,0]
	v_fma_mix_f32 v216, v87, 1.0, v216 op_sel:[1,0,0] op_sel_hi:[1,0,0]
	v_fma_mix_f32 v217, v87, v87, v217 op_sel:[1,1,0] op_sel_hi:[1,1,0]
	s_waitcnt vmcnt(14)
	v_cvt_f32_f16_e32 v72, v252
	v_cvt_f32_f16_sdwa v73, v252 dst_sel:DWORD dst_unused:UNUSED_PAD src0_sel:WORD_1
	v_cvt_f32_f16_e32 v74, v253
	v_cvt_f32_f16_sdwa v75, v253 dst_sel:DWORD dst_unused:UNUSED_PAD src0_sel:WORD_1
	v_cvt_f32_f16_e32 v80, v254
	v_cvt_f32_f16_sdwa v81, v254 dst_sel:DWORD dst_unused:UNUSED_PAD src0_sel:WORD_1
	v_cvt_f32_f16_e32 v82, v255
	v_cvt_f32_f16_sdwa v83, v255 dst_sel:DWORD dst_unused:UNUSED_PAD src0_sel:WORD_1
	v_sub_f32_e32 v72, v72, v196
	v_sub_f32_e32 v73, v73, v196
	v_sub_f32_e32 v74, v74, v196
	v_sub_f32_e32 v75, v75, v196
	v_sub_f32_e32 v80, v80, v196
	v_sub_f32_e32 v81, v81, v196
	v_sub_f32_e32 v82, v82, v196
	v_sub_f32_e32 v83, v83, v196
	v_pk_mul_f32 v[72:73], v[196:197], v[72:73] op_sel:[1,0]
	v_pk_mul_f32 v[74:75], v[196:197], v[74:75] op_sel:[1,0]
	v_pk_mul_f32 v[80:81], v[196:197], v[80:81] op_sel:[1,0]
	v_pk_mul_f32 v[82:83], v[196:197], v[82:83] op_sel:[1,0]
	v_pk_fma_f32 v[68:69], v[72:73], v[168:169], v[68:69]
	v_pk_fma_f32 v[70:71], v[74:75], v[170:171], v[70:71]
	v_pk_fma_f32 v[64:65], v[80:81], v[172:173], v[64:65]
	v_pk_fma_f32 v[66:67], v[82:83], v[174:175], v[66:67]
	v_cvt_pk_f16_f32 v68, v68, v69
	v_cvt_pk_f16_f32 v69, v70, v71
	v_cvt_pk_f16_f32 v70, v64, v65
	v_cvt_pk_f16_f32 v71, v66, v67
	ds_write_b128 v235, v[68:71] offset:64
	v_fma_mix_f32 v216, v68, 1.0, v216 op_sel_hi:[1,0,0]
	v_fma_mix_f32 v217, v68, v68, v217 op_sel_hi:[1,1,0]
	v_fma_mix_f32 v216, v68, 1.0, v216 op_sel:[1,0,0] op_sel_hi:[1,0,0]
	v_fma_mix_f32 v217, v68, v68, v217 op_sel:[1,1,0] op_sel_hi:[1,1,0]
	v_fma_mix_f32 v216, v69, 1.0, v216 op_sel_hi:[1,0,0]
	v_fma_mix_f32 v217, v69, v69, v217 op_sel_hi:[1,1,0]
	v_fma_mix_f32 v216, v69, 1.0, v216 op_sel:[1,0,0] op_sel_hi:[1,0,0]
	v_fma_mix_f32 v217, v69, v69, v217 op_sel:[1,1,0] op_sel_hi:[1,1,0]
	v_fma_mix_f32 v216, v70, 1.0, v216 op_sel_hi:[1,0,0]
	v_fma_mix_f32 v217, v70, v70, v217 op_sel_hi:[1,1,0]
	v_fma_mix_f32 v216, v70, 1.0, v216 op_sel:[1,0,0] op_sel_hi:[1,0,0]
	v_fma_mix_f32 v217, v70, v70, v217 op_sel:[1,1,0] op_sel_hi:[1,1,0]
	v_fma_mix_f32 v216, v71, 1.0, v216 op_sel_hi:[1,0,0]
	v_fma_mix_f32 v217, v71, v71, v217 op_sel_hi:[1,1,0]
	v_fma_mix_f32 v216, v71, 1.0, v216 op_sel:[1,0,0] op_sel_hi:[1,0,0]
	v_fma_mix_f32 v217, v71, v71, v217 op_sel:[1,1,0] op_sel_hi:[1,1,0]
	ds_read_b128 v[112:115], v236
	ds_read_b128 v[220:223], v236 offset:1152
	s_waitcnt vmcnt(13)
	v_cvt_f32_f16_e32 v72, v136
	v_cvt_f32_f16_sdwa v73, v136 dst_sel:DWORD dst_unused:UNUSED_PAD src0_sel:WORD_1
	v_cvt_f32_f16_e32 v74, v137
	v_cvt_f32_f16_sdwa v75, v137 dst_sel:DWORD dst_unused:UNUSED_PAD src0_sel:WORD_1
	v_cvt_f32_f16_e32 v80, v138
	v_cvt_f32_f16_sdwa v81, v138 dst_sel:DWORD dst_unused:UNUSED_PAD src0_sel:WORD_1
	v_cvt_f32_f16_e32 v82, v139
	v_cvt_f32_f16_sdwa v83, v139 dst_sel:DWORD dst_unused:UNUSED_PAD src0_sel:WORD_1
	v_sub_f32_e32 v72, v72, v198
	v_sub_f32_e32 v73, v73, v198
	v_sub_f32_e32 v74, v74, v198
	v_sub_f32_e32 v75, v75, v198
	v_sub_f32_e32 v80, v80, v198
	v_sub_f32_e32 v81, v81, v198
	v_sub_f32_e32 v82, v82, v198
	v_sub_f32_e32 v83, v83, v198
	v_pk_mul_f32 v[72:73], v[198:199], v[72:73] op_sel:[1,0]
	v_pk_mul_f32 v[74:75], v[198:199], v[74:75] op_sel:[1,0]
	v_pk_mul_f32 v[80:81], v[198:199], v[80:81] op_sel:[1,0]
	v_pk_mul_f32 v[82:83], v[198:199], v[82:83] op_sel:[1,0]
	v_pk_fma_f32 v[60:61], v[72:73], v[160:161], v[60:61]
	v_pk_fma_f32 v[62:63], v[74:75], v[162:163], v[62:63]
	v_pk_fma_f32 v[56:57], v[80:81], v[164:165], v[56:57]
	v_pk_fma_f32 v[58:59], v[82:83], v[166:167], v[58:59]
	v_cvt_pk_f16_f32 v60, v60, v61
	v_cvt_pk_f16_f32 v61, v62, v63
	v_cvt_pk_f16_f32 v62, v56, v57
	v_cvt_pk_f16_f32 v63, v58, v59
	s_waitcnt lgkmcnt(0)
	v_add_u32_e32 v83, 0x12000, v224
	buffer_store_dwordx4 v[112:115], v83, s[24:27], 0 offen nt
	v_add_u32_e32 v82, 0x15000, v224
	buffer_store_dwordx4 v[220:223], v82, s[24:27], 0 offen nt
	ds_write_b128 v235, v[60:63]
	v_fma_mix_f32 v218, v60, 1.0, 0 op_sel_hi:[1,0,0]
	v_fma_mix_f32 v219, v60, v60, 0 op_sel_hi:[1,1,0]
	v_fma_mix_f32 v218, v60, 1.0, v218 op_sel:[1,0,0] op_sel_hi:[1,0,0]
	v_fma_mix_f32 v219, v60, v60, v219 op_sel:[1,1,0] op_sel_hi:[1,1,0]
	v_fma_mix_f32 v218, v61, 1.0, v218 op_sel_hi:[1,0,0]
	v_fma_mix_f32 v219, v61, v61, v219 op_sel_hi:[1,1,0]
	v_fma_mix_f32 v218, v61, 1.0, v218 op_sel:[1,0,0] op_sel_hi:[1,0,0]
	v_fma_mix_f32 v219, v61, v61, v219 op_sel:[1,1,0] op_sel_hi:[1,1,0]
	v_fma_mix_f32 v218, v62, 1.0, v218 op_sel_hi:[1,0,0]
	v_fma_mix_f32 v219, v62, v62, v219 op_sel_hi:[1,1,0]
	v_fma_mix_f32 v218, v62, 1.0, v218 op_sel:[1,0,0] op_sel_hi:[1,0,0]
	v_fma_mix_f32 v219, v62, v62, v219 op_sel:[1,1,0] op_sel_hi:[1,1,0]
	v_fma_mix_f32 v218, v63, 1.0, v218 op_sel_hi:[1,0,0]
	v_fma_mix_f32 v219, v63, v63, v219 op_sel_hi:[1,1,0]
	v_fma_mix_f32 v218, v63, 1.0, v218 op_sel:[1,0,0] op_sel_hi:[1,0,0]
	v_fma_mix_f32 v219, v63, v63, v219 op_sel:[1,1,0] op_sel_hi:[1,1,0]
	s_waitcnt vmcnt(14)
	v_cvt_f32_f16_e32 v72, v148
	v_cvt_f32_f16_sdwa v73, v148 dst_sel:DWORD dst_unused:UNUSED_PAD src0_sel:WORD_1
	v_cvt_f32_f16_e32 v74, v149
	v_cvt_f32_f16_sdwa v75, v149 dst_sel:DWORD dst_unused:UNUSED_PAD src0_sel:WORD_1
	v_cvt_f32_f16_e32 v80, v150
	v_cvt_f32_f16_sdwa v81, v150 dst_sel:DWORD dst_unused:UNUSED_PAD src0_sel:WORD_1
	v_cvt_f32_f16_e32 v82, v151
	v_cvt_f32_f16_sdwa v83, v151 dst_sel:DWORD dst_unused:UNUSED_PAD src0_sel:WORD_1
	v_sub_f32_e32 v72, v72, v198
	v_sub_f32_e32 v73, v73, v198
	v_sub_f32_e32 v74, v74, v198
	v_sub_f32_e32 v75, v75, v198
	v_sub_f32_e32 v80, v80, v198
	v_sub_f32_e32 v81, v81, v198
	v_sub_f32_e32 v82, v82, v198
	v_sub_f32_e32 v83, v83, v198
	v_pk_mul_f32 v[72:73], v[198:199], v[72:73] op_sel:[1,0]
	v_pk_mul_f32 v[74:75], v[198:199], v[74:75] op_sel:[1,0]
	v_pk_mul_f32 v[80:81], v[198:199], v[80:81] op_sel:[1,0]
	v_pk_mul_f32 v[82:83], v[198:199], v[82:83] op_sel:[1,0]
	v_pk_fma_f32 v[52:53], v[72:73], v[168:169], v[52:53]
	v_pk_fma_f32 v[54:55], v[74:75], v[170:171], v[54:55]
	v_pk_fma_f32 v[48:49], v[80:81], v[172:173], v[48:49]
	v_pk_fma_f32 v[50:51], v[82:83], v[174:175], v[50:51]
	v_cvt_pk_f16_f32 v52, v52, v53
	v_cvt_pk_f16_f32 v53, v54, v55
	v_cvt_pk_f16_f32 v54, v48, v49
	v_cvt_pk_f16_f32 v55, v50, v51
	ds_write_b128 v235, v[52:55] offset:64
	v_fma_mix_f32 v218, v52, 1.0, v218 op_sel_hi:[1,0,0]
	v_fma_mix_f32 v219, v52, v52, v219 op_sel_hi:[1,1,0]
	v_fma_mix_f32 v218, v52, 1.0, v218 op_sel:[1,0,0] op_sel_hi:[1,0,0]
	v_fma_mix_f32 v219, v52, v52, v219 op_sel:[1,1,0] op_sel_hi:[1,1,0]
	v_fma_mix_f32 v218, v53, 1.0, v218 op_sel_hi:[1,0,0]
	v_fma_mix_f32 v219, v53, v53, v219 op_sel_hi:[1,1,0]
	v_fma_mix_f32 v218, v53, 1.0, v218 op_sel:[1,0,0] op_sel_hi:[1,0,0]
	v_fma_mix_f32 v219, v53, v53, v219 op_sel:[1,1,0] op_sel_hi:[1,1,0]
	v_fma_mix_f32 v218, v54, 1.0, v218 op_sel_hi:[1,0,0]
	v_fma_mix_f32 v219, v54, v54, v219 op_sel_hi:[1,1,0]
	v_fma_mix_f32 v218, v54, 1.0, v218 op_sel:[1,0,0] op_sel_hi:[1,0,0]
	v_fma_mix_f32 v219, v54, v54, v219 op_sel:[1,1,0] op_sel_hi:[1,1,0]
	v_fma_mix_f32 v218, v55, 1.0, v218 op_sel_hi:[1,0,0]
	v_fma_mix_f32 v219, v55, v55, v219 op_sel_hi:[1,1,0]
	v_fma_mix_f32 v218, v55, 1.0, v218 op_sel:[1,0,0] op_sel_hi:[1,0,0]
	v_fma_mix_f32 v219, v55, v55, v219 op_sel:[1,1,0] op_sel_hi:[1,1,0]
	ds_read_b128 v[124:127], v236
	ds_read_b128 v[116:119], v236 offset:1152
	s_waitcnt vmcnt(13)
	v_cvt_f32_f16_e32 v72, v152
	v_cvt_f32_f16_sdwa v73, v152 dst_sel:DWORD dst_unused:UNUSED_PAD src0_sel:WORD_1
	v_cvt_f32_f16_e32 v74, v153
	v_cvt_f32_f16_sdwa v75, v153 dst_sel:DWORD dst_unused:UNUSED_PAD src0_sel:WORD_1
	v_cvt_f32_f16_e32 v80, v154
	v_cvt_f32_f16_sdwa v81, v154 dst_sel:DWORD dst_unused:UNUSED_PAD src0_sel:WORD_1
	v_cvt_f32_f16_e32 v82, v155
	v_cvt_f32_f16_sdwa v83, v155 dst_sel:DWORD dst_unused:UNUSED_PAD src0_sel:WORD_1
	v_sub_f32_e32 v72, v72, v200
	v_sub_f32_e32 v73, v73, v200
	v_sub_f32_e32 v74, v74, v200
	v_sub_f32_e32 v75, v75, v200
	v_sub_f32_e32 v80, v80, v200
	v_sub_f32_e32 v81, v81, v200
	v_sub_f32_e32 v82, v82, v200
	v_sub_f32_e32 v83, v83, v200
	v_pk_mul_f32 v[72:73], v[200:201], v[72:73] op_sel:[1,0]
	v_pk_mul_f32 v[74:75], v[200:201], v[74:75] op_sel:[1,0]
	v_pk_mul_f32 v[80:81], v[200:201], v[80:81] op_sel:[1,0]
	v_pk_mul_f32 v[82:83], v[200:201], v[82:83] op_sel:[1,0]
	v_pk_fma_f32 v[44:45], v[72:73], v[160:161], v[44:45]
	v_pk_fma_f32 v[46:47], v[74:75], v[162:163], v[46:47]
	v_pk_fma_f32 v[40:41], v[80:81], v[164:165], v[40:41]
	v_pk_fma_f32 v[42:43], v[82:83], v[166:167], v[42:43]
	v_cvt_pk_f16_f32 v44, v44, v45
	v_cvt_pk_f16_f32 v45, v46, v47
	v_cvt_pk_f16_f32 v46, v40, v41
	v_cvt_pk_f16_f32 v47, v42, v43
	s_waitcnt lgkmcnt(0)
	v_add_u32_e32 v83, 0x30000, v224
	buffer_store_dwordx4 v[124:127], v83, s[24:27], 0 offen nt
	v_add_u32_e32 v82, 0x33000, v224
	buffer_store_dwordx4 v[116:119], v82, s[24:27], 0 offen nt
	ds_write_b128 v235, v[44:47]
	v_fma_mix_f32 v208, v44, 1.0, 0 op_sel_hi:[1,0,0]
	v_fma_mix_f32 v209, v44, v44, 0 op_sel_hi:[1,1,0]
	v_fma_mix_f32 v208, v44, 1.0, v208 op_sel:[1,0,0] op_sel_hi:[1,0,0]
	v_fma_mix_f32 v209, v44, v44, v209 op_sel:[1,1,0] op_sel_hi:[1,1,0]
	v_fma_mix_f32 v208, v45, 1.0, v208 op_sel_hi:[1,0,0]
	v_fma_mix_f32 v209, v45, v45, v209 op_sel_hi:[1,1,0]
	v_fma_mix_f32 v208, v45, 1.0, v208 op_sel:[1,0,0] op_sel_hi:[1,0,0]
	v_fma_mix_f32 v209, v45, v45, v209 op_sel:[1,1,0] op_sel_hi:[1,1,0]
	v_fma_mix_f32 v208, v46, 1.0, v208 op_sel_hi:[1,0,0]
	v_fma_mix_f32 v209, v46, v46, v209 op_sel_hi:[1,1,0]
	v_fma_mix_f32 v208, v46, 1.0, v208 op_sel:[1,0,0] op_sel_hi:[1,0,0]
	v_fma_mix_f32 v209, v46, v46, v209 op_sel:[1,1,0] op_sel_hi:[1,1,0]
	v_fma_mix_f32 v208, v47, 1.0, v208 op_sel_hi:[1,0,0]
	v_fma_mix_f32 v209, v47, v47, v209 op_sel_hi:[1,1,0]
	v_fma_mix_f32 v208, v47, 1.0, v208 op_sel:[1,0,0] op_sel_hi:[1,0,0]
	v_fma_mix_f32 v209, v47, v47, v209 op_sel:[1,1,0] op_sel_hi:[1,1,0]
	s_waitcnt vmcnt(14)
	v_cvt_f32_f16_e32 v72, v156
	v_cvt_f32_f16_sdwa v73, v156 dst_sel:DWORD dst_unused:UNUSED_PAD src0_sel:WORD_1
	v_cvt_f32_f16_e32 v74, v157
	v_cvt_f32_f16_sdwa v75, v157 dst_sel:DWORD dst_unused:UNUSED_PAD src0_sel:WORD_1
	v_cvt_f32_f16_e32 v80, v158
	v_cvt_f32_f16_sdwa v81, v158 dst_sel:DWORD dst_unused:UNUSED_PAD src0_sel:WORD_1
	v_cvt_f32_f16_e32 v82, v159
	v_cvt_f32_f16_sdwa v83, v159 dst_sel:DWORD dst_unused:UNUSED_PAD src0_sel:WORD_1
	v_sub_f32_e32 v72, v72, v200
	v_sub_f32_e32 v73, v73, v200
	v_sub_f32_e32 v74, v74, v200
	v_sub_f32_e32 v75, v75, v200
	v_sub_f32_e32 v80, v80, v200
	v_sub_f32_e32 v81, v81, v200
	v_sub_f32_e32 v82, v82, v200
	v_sub_f32_e32 v83, v83, v200
	v_pk_mul_f32 v[72:73], v[200:201], v[72:73] op_sel:[1,0]
	v_pk_mul_f32 v[74:75], v[200:201], v[74:75] op_sel:[1,0]
	v_pk_mul_f32 v[80:81], v[200:201], v[80:81] op_sel:[1,0]
	v_pk_mul_f32 v[82:83], v[200:201], v[82:83] op_sel:[1,0]
	v_pk_fma_f32 v[36:37], v[72:73], v[168:169], v[36:37]
	v_pk_fma_f32 v[38:39], v[74:75], v[170:171], v[38:39]
	v_pk_fma_f32 v[32:33], v[80:81], v[172:173], v[32:33]
	v_pk_fma_f32 v[34:35], v[82:83], v[174:175], v[34:35]
	v_cvt_pk_f16_f32 v36, v36, v37
	v_cvt_pk_f16_f32 v37, v38, v39
	v_cvt_pk_f16_f32 v38, v32, v33
	v_cvt_pk_f16_f32 v39, v34, v35
	ds_write_b128 v235, v[36:39] offset:64
	v_fma_mix_f32 v208, v36, 1.0, v208 op_sel_hi:[1,0,0]
	v_fma_mix_f32 v209, v36, v36, v209 op_sel_hi:[1,1,0]
	v_fma_mix_f32 v208, v36, 1.0, v208 op_sel:[1,0,0] op_sel_hi:[1,0,0]
	v_fma_mix_f32 v209, v36, v36, v209 op_sel:[1,1,0] op_sel_hi:[1,1,0]
	v_fma_mix_f32 v208, v37, 1.0, v208 op_sel_hi:[1,0,0]
	v_fma_mix_f32 v209, v37, v37, v209 op_sel_hi:[1,1,0]
	v_fma_mix_f32 v208, v37, 1.0, v208 op_sel:[1,0,0] op_sel_hi:[1,0,0]
	v_fma_mix_f32 v209, v37, v37, v209 op_sel:[1,1,0] op_sel_hi:[1,1,0]
	v_fma_mix_f32 v208, v38, 1.0, v208 op_sel_hi:[1,0,0]
	v_fma_mix_f32 v209, v38, v38, v209 op_sel_hi:[1,1,0]
	v_fma_mix_f32 v208, v38, 1.0, v208 op_sel:[1,0,0] op_sel_hi:[1,0,0]
	v_fma_mix_f32 v209, v38, v38, v209 op_sel:[1,1,0] op_sel_hi:[1,1,0]
	v_fma_mix_f32 v208, v39, 1.0, v208 op_sel_hi:[1,0,0]
	v_fma_mix_f32 v209, v39, v39, v209 op_sel_hi:[1,1,0]
	v_fma_mix_f32 v208, v39, 1.0, v208 op_sel:[1,0,0] op_sel_hi:[1,0,0]
	v_fma_mix_f32 v209, v39, v39, v209 op_sel:[1,1,0] op_sel_hi:[1,1,0]
	ds_read_b128 v[128:131], v236
	ds_read_b128 v[104:107], v236 offset:1152
	s_waitcnt vmcnt(11)
	v_cvt_f32_f16_e32 v72, v212
	v_cvt_f32_f16_sdwa v73, v212 dst_sel:DWORD dst_unused:UNUSED_PAD src0_sel:WORD_1
	v_cvt_f32_f16_e32 v74, v213
	v_cvt_f32_f16_sdwa v75, v213 dst_sel:DWORD dst_unused:UNUSED_PAD src0_sel:WORD_1
	v_cvt_f32_f16_e32 v80, v214
	v_cvt_f32_f16_sdwa v81, v214 dst_sel:DWORD dst_unused:UNUSED_PAD src0_sel:WORD_1
	v_cvt_f32_f16_e32 v82, v215
	v_cvt_f32_f16_sdwa v83, v215 dst_sel:DWORD dst_unused:UNUSED_PAD src0_sel:WORD_1
	v_sub_f32_e32 v72, v72, v202
	v_sub_f32_e32 v73, v73, v202
	v_sub_f32_e32 v74, v74, v202
	v_sub_f32_e32 v75, v75, v202
	v_sub_f32_e32 v80, v80, v202
	v_sub_f32_e32 v81, v81, v202
	v_sub_f32_e32 v82, v82, v202
	v_sub_f32_e32 v83, v83, v202
	v_pk_mul_f32 v[72:73], v[202:203], v[72:73] op_sel:[1,0]
	v_pk_mul_f32 v[74:75], v[202:203], v[74:75] op_sel:[1,0]
	v_pk_mul_f32 v[80:81], v[202:203], v[80:81] op_sel:[1,0]
	v_pk_mul_f32 v[82:83], v[202:203], v[82:83] op_sel:[1,0]
	v_pk_fma_f32 v[28:29], v[72:73], v[160:161], v[28:29]
	v_pk_fma_f32 v[30:31], v[74:75], v[162:163], v[30:31]
	v_pk_fma_f32 v[24:25], v[80:81], v[164:165], v[24:25]
	v_pk_fma_f32 v[26:27], v[82:83], v[166:167], v[26:27]
	v_cvt_pk_f16_f32 v28, v28, v29
	v_cvt_pk_f16_f32 v29, v30, v31
	v_cvt_pk_f16_f32 v30, v24, v25
	v_cvt_pk_f16_f32 v31, v26, v27
	s_waitcnt lgkmcnt(0)
	v_add_u32_e32 v83, 0x36000, v224
	buffer_store_dwordx4 v[128:131], v83, s[24:27], 0 offen nt
	v_add_u32_e32 v82, 0x39000, v224
	buffer_store_dwordx4 v[104:107], v82, s[24:27], 0 offen nt
	ds_write_b128 v235, v[28:31]
	v_fma_mix_f32 v210, v28, 1.0, 0 op_sel_hi:[1,0,0]
	v_fma_mix_f32 v211, v28, v28, 0 op_sel_hi:[1,1,0]
	v_fma_mix_f32 v210, v28, 1.0, v210 op_sel:[1,0,0] op_sel_hi:[1,0,0]
	v_fma_mix_f32 v211, v28, v28, v211 op_sel:[1,1,0] op_sel_hi:[1,1,0]
	v_fma_mix_f32 v210, v29, 1.0, v210 op_sel_hi:[1,0,0]
	v_fma_mix_f32 v211, v29, v29, v211 op_sel_hi:[1,1,0]
	v_fma_mix_f32 v210, v29, 1.0, v210 op_sel:[1,0,0] op_sel_hi:[1,0,0]
	v_fma_mix_f32 v211, v29, v29, v211 op_sel:[1,1,0] op_sel_hi:[1,1,0]
	v_fma_mix_f32 v210, v30, 1.0, v210 op_sel_hi:[1,0,0]
	v_fma_mix_f32 v211, v30, v30, v211 op_sel_hi:[1,1,0]
	v_fma_mix_f32 v210, v30, 1.0, v210 op_sel:[1,0,0] op_sel_hi:[1,0,0]
	v_fma_mix_f32 v211, v30, v30, v211 op_sel:[1,1,0] op_sel_hi:[1,1,0]
	v_fma_mix_f32 v210, v31, 1.0, v210 op_sel_hi:[1,0,0]
	v_fma_mix_f32 v211, v31, v31, v211 op_sel_hi:[1,1,0]
	v_fma_mix_f32 v210, v31, 1.0, v210 op_sel:[1,0,0] op_sel_hi:[1,0,0]
	v_fma_mix_f32 v211, v31, v31, v211 op_sel:[1,1,0] op_sel_hi:[1,1,0]
	s_waitcnt vmcnt(12)
	v_cvt_f32_f16_e32 v72, v144
	v_cvt_f32_f16_sdwa v73, v144 dst_sel:DWORD dst_unused:UNUSED_PAD src0_sel:WORD_1
	v_cvt_f32_f16_e32 v74, v145
	v_cvt_f32_f16_sdwa v75, v145 dst_sel:DWORD dst_unused:UNUSED_PAD src0_sel:WORD_1
	v_cvt_f32_f16_e32 v80, v146
	v_cvt_f32_f16_sdwa v81, v146 dst_sel:DWORD dst_unused:UNUSED_PAD src0_sel:WORD_1
	v_cvt_f32_f16_e32 v82, v147
	v_cvt_f32_f16_sdwa v83, v147 dst_sel:DWORD dst_unused:UNUSED_PAD src0_sel:WORD_1
	v_sub_f32_e32 v72, v72, v202
	v_sub_f32_e32 v73, v73, v202
	v_sub_f32_e32 v74, v74, v202
	v_sub_f32_e32 v75, v75, v202
	v_sub_f32_e32 v80, v80, v202
	v_sub_f32_e32 v81, v81, v202
	v_sub_f32_e32 v82, v82, v202
	v_sub_f32_e32 v83, v83, v202
	v_pk_mul_f32 v[72:73], v[202:203], v[72:73] op_sel:[1,0]
	v_pk_mul_f32 v[74:75], v[202:203], v[74:75] op_sel:[1,0]
	v_pk_mul_f32 v[80:81], v[202:203], v[80:81] op_sel:[1,0]
	v_pk_mul_f32 v[82:83], v[202:203], v[82:83] op_sel:[1,0]
	v_pk_fma_f32 v[20:21], v[72:73], v[168:169], v[20:21]
	v_pk_fma_f32 v[22:23], v[74:75], v[170:171], v[22:23]
	v_pk_fma_f32 v[16:17], v[80:81], v[172:173], v[16:17]
	v_pk_fma_f32 v[18:19], v[82:83], v[174:175], v[18:19]
	v_cvt_pk_f16_f32 v20, v20, v21
	v_cvt_pk_f16_f32 v21, v22, v23
	v_cvt_pk_f16_f32 v22, v16, v17
	v_cvt_pk_f16_f32 v23, v18, v19
	ds_write_b128 v235, v[20:23] offset:64
	v_fma_mix_f32 v210, v20, 1.0, v210 op_sel_hi:[1,0,0]
	v_fma_mix_f32 v211, v20, v20, v211 op_sel_hi:[1,1,0]
	v_fma_mix_f32 v210, v20, 1.0, v210 op_sel:[1,0,0] op_sel_hi:[1,0,0]
	v_fma_mix_f32 v211, v20, v20, v211 op_sel:[1,1,0] op_sel_hi:[1,1,0]
	v_fma_mix_f32 v210, v21, 1.0, v210 op_sel_hi:[1,0,0]
	v_fma_mix_f32 v211, v21, v21, v211 op_sel_hi:[1,1,0]
	v_fma_mix_f32 v210, v21, 1.0, v210 op_sel:[1,0,0] op_sel_hi:[1,0,0]
	v_fma_mix_f32 v211, v21, v21, v211 op_sel:[1,1,0] op_sel_hi:[1,1,0]
	v_fma_mix_f32 v210, v22, 1.0, v210 op_sel_hi:[1,0,0]
	v_fma_mix_f32 v211, v22, v22, v211 op_sel_hi:[1,1,0]
	v_fma_mix_f32 v210, v22, 1.0, v210 op_sel:[1,0,0] op_sel_hi:[1,0,0]
	v_fma_mix_f32 v211, v22, v22, v211 op_sel:[1,1,0] op_sel_hi:[1,1,0]
	v_fma_mix_f32 v210, v23, 1.0, v210 op_sel_hi:[1,0,0]
	v_fma_mix_f32 v211, v23, v23, v211 op_sel_hi:[1,1,0]
	v_fma_mix_f32 v210, v23, 1.0, v210 op_sel:[1,0,0] op_sel_hi:[1,0,0]
	v_fma_mix_f32 v211, v23, v23, v211 op_sel:[1,1,0] op_sel_hi:[1,1,0]
	ds_read_b128 v[240:243], v236
	ds_read_b128 v[96:99], v236 offset:1152
	s_waitcnt vmcnt(11)
	v_cvt_f32_f16_e32 v72, v132
	v_cvt_f32_f16_sdwa v73, v132 dst_sel:DWORD dst_unused:UNUSED_PAD src0_sel:WORD_1
	v_cvt_f32_f16_e32 v74, v133
	v_cvt_f32_f16_sdwa v75, v133 dst_sel:DWORD dst_unused:UNUSED_PAD src0_sel:WORD_1
	v_cvt_f32_f16_e32 v80, v134
	v_cvt_f32_f16_sdwa v81, v134 dst_sel:DWORD dst_unused:UNUSED_PAD src0_sel:WORD_1
	v_cvt_f32_f16_e32 v82, v135
	v_cvt_f32_f16_sdwa v83, v135 dst_sel:DWORD dst_unused:UNUSED_PAD src0_sel:WORD_1
	v_sub_f32_e32 v72, v72, v204
	v_sub_f32_e32 v73, v73, v204
	v_sub_f32_e32 v74, v74, v204
	v_sub_f32_e32 v75, v75, v204
	v_sub_f32_e32 v80, v80, v204
	v_sub_f32_e32 v81, v81, v204
	v_sub_f32_e32 v82, v82, v204
	v_sub_f32_e32 v83, v83, v204
	v_pk_mul_f32 v[72:73], v[204:205], v[72:73] op_sel:[1,0]
	v_pk_mul_f32 v[74:75], v[204:205], v[74:75] op_sel:[1,0]
	v_pk_mul_f32 v[80:81], v[204:205], v[80:81] op_sel:[1,0]
	v_pk_mul_f32 v[82:83], v[204:205], v[82:83] op_sel:[1,0]
	v_pk_fma_f32 v[12:13], v[72:73], v[160:161], v[12:13]
	v_pk_fma_f32 v[14:15], v[74:75], v[162:163], v[14:15]
	v_pk_fma_f32 v[8:9], v[80:81], v[164:165], v[8:9]
	v_pk_fma_f32 v[10:11], v[82:83], v[166:167], v[10:11]
	v_cvt_pk_f16_f32 v12, v12, v13
	v_cvt_pk_f16_f32 v13, v14, v15
	v_cvt_pk_f16_f32 v14, v8, v9
	v_cvt_pk_f16_f32 v15, v10, v11
	s_waitcnt lgkmcnt(0)
	v_add_u32_e32 v83, 0x3c000, v224
	buffer_store_dwordx4 v[240:243], v83, s[24:27], 0 offen nt
	v_add_u32_e32 v82, 0x3f000, v224
	buffer_store_dwordx4 v[96:99], v82, s[24:27], 0 offen nt
	ds_write_b128 v235, v[12:15]
	v_fma_mix_f32 v244, v12, 1.0, 0 op_sel_hi:[1,0,0]
	v_fma_mix_f32 v245, v12, v12, 0 op_sel_hi:[1,1,0]
	v_fma_mix_f32 v244, v12, 1.0, v244 op_sel:[1,0,0] op_sel_hi:[1,0,0]
	v_fma_mix_f32 v245, v12, v12, v245 op_sel:[1,1,0] op_sel_hi:[1,1,0]
	v_fma_mix_f32 v244, v13, 1.0, v244 op_sel_hi:[1,0,0]
	v_fma_mix_f32 v245, v13, v13, v245 op_sel_hi:[1,1,0]
	v_fma_mix_f32 v244, v13, 1.0, v244 op_sel:[1,0,0] op_sel_hi:[1,0,0]
	v_fma_mix_f32 v245, v13, v13, v245 op_sel:[1,1,0] op_sel_hi:[1,1,0]
	v_fma_mix_f32 v244, v14, 1.0, v244 op_sel_hi:[1,0,0]
	v_fma_mix_f32 v245, v14, v14, v245 op_sel_hi:[1,1,0]
	v_fma_mix_f32 v244, v14, 1.0, v244 op_sel:[1,0,0] op_sel_hi:[1,0,0]
	v_fma_mix_f32 v245, v14, v14, v245 op_sel:[1,1,0] op_sel_hi:[1,1,0]
	v_fma_mix_f32 v244, v15, 1.0, v244 op_sel_hi:[1,0,0]
	v_fma_mix_f32 v245, v15, v15, v245 op_sel_hi:[1,1,0]
	v_fma_mix_f32 v244, v15, 1.0, v244 op_sel:[1,0,0] op_sel_hi:[1,0,0]
	v_fma_mix_f32 v245, v15, v15, v245 op_sel:[1,1,0] op_sel_hi:[1,1,0]
	s_waitcnt vmcnt(12)
	v_cvt_f32_f16_e32 v72, v88
	v_cvt_f32_f16_sdwa v73, v88 dst_sel:DWORD dst_unused:UNUSED_PAD src0_sel:WORD_1
	v_cvt_f32_f16_e32 v74, v89
	v_cvt_f32_f16_sdwa v75, v89 dst_sel:DWORD dst_unused:UNUSED_PAD src0_sel:WORD_1
	v_cvt_f32_f16_e32 v80, v90
	v_cvt_f32_f16_sdwa v81, v90 dst_sel:DWORD dst_unused:UNUSED_PAD src0_sel:WORD_1
	v_cvt_f32_f16_e32 v82, v91
	v_cvt_f32_f16_sdwa v83, v91 dst_sel:DWORD dst_unused:UNUSED_PAD src0_sel:WORD_1
	v_sub_f32_e32 v72, v72, v204
	v_sub_f32_e32 v73, v73, v204
	v_sub_f32_e32 v74, v74, v204
	v_sub_f32_e32 v75, v75, v204
	v_sub_f32_e32 v80, v80, v204
	v_sub_f32_e32 v81, v81, v204
	v_sub_f32_e32 v82, v82, v204
	v_sub_f32_e32 v83, v83, v204
	v_pk_mul_f32 v[72:73], v[204:205], v[72:73] op_sel:[1,0]
	v_pk_mul_f32 v[74:75], v[204:205], v[74:75] op_sel:[1,0]
	v_pk_mul_f32 v[80:81], v[204:205], v[80:81] op_sel:[1,0]
	v_pk_mul_f32 v[82:83], v[204:205], v[82:83] op_sel:[1,0]
	v_pk_fma_f32 v[4:5], v[72:73], v[168:169], v[4:5]
	v_pk_fma_f32 v[6:7], v[74:75], v[170:171], v[6:7]
	v_pk_fma_f32 v[0:1], v[80:81], v[172:173], v[0:1]
	v_pk_fma_f32 v[2:3], v[82:83], v[174:175], v[2:3]
	v_cvt_pk_f16_f32 v4, v4, v5
	v_cvt_pk_f16_f32 v5, v6, v7
	v_cvt_pk_f16_f32 v6, v0, v1
	v_cvt_pk_f16_f32 v7, v2, v3
	ds_write_b128 v235, v[4:7] offset:64
	v_fma_mix_f32 v244, v4, 1.0, v244 op_sel_hi:[1,0,0]
	v_fma_mix_f32 v245, v4, v4, v245 op_sel_hi:[1,1,0]
	v_fma_mix_f32 v244, v4, 1.0, v244 op_sel:[1,0,0] op_sel_hi:[1,0,0]
	v_fma_mix_f32 v245, v4, v4, v245 op_sel:[1,1,0] op_sel_hi:[1,1,0]
	v_fma_mix_f32 v244, v5, 1.0, v244 op_sel_hi:[1,0,0]
	v_fma_mix_f32 v245, v5, v5, v245 op_sel_hi:[1,1,0]
	v_fma_mix_f32 v244, v5, 1.0, v244 op_sel:[1,0,0] op_sel_hi:[1,0,0]
	v_fma_mix_f32 v245, v5, v5, v245 op_sel:[1,1,0] op_sel_hi:[1,1,0]
	v_fma_mix_f32 v244, v6, 1.0, v244 op_sel_hi:[1,0,0]
	v_fma_mix_f32 v245, v6, v6, v245 op_sel_hi:[1,1,0]
	v_fma_mix_f32 v244, v6, 1.0, v244 op_sel:[1,0,0] op_sel_hi:[1,0,0]
	v_fma_mix_f32 v245, v6, v6, v245 op_sel:[1,1,0] op_sel_hi:[1,1,0]
	v_fma_mix_f32 v244, v7, 1.0, v244 op_sel_hi:[1,0,0]
	v_fma_mix_f32 v245, v7, v7, v245 op_sel_hi:[1,1,0]
	v_fma_mix_f32 v244, v7, 1.0, v244 op_sel:[1,0,0] op_sel_hi:[1,0,0]
	v_fma_mix_f32 v245, v7, v7, v245 op_sel:[1,1,0] op_sel_hi:[1,1,0]
	ds_read_b128 v[108:111], v236
	ds_read_b128 v[100:103], v236 offset:1152
	s_waitcnt lgkmcnt(0)
	v_add_u32_e32 v83, 0x42000, v224
	buffer_store_dwordx4 v[108:111], v83, s[24:27], 0 offen nt
	v_add_u32_e32 v82, 0x45000, v224
	buffer_store_dwordx4 v[100:103], v82, s[24:27], 0 offen nt
	v_xor_b32_e32 v225, 16, v234
	v_lshlrev_b32_e32 v225, 2, v225
	v_xor_b32_e32 v246, 32, v234
	v_lshlrev_b32_e32 v246, 2, v246
	ds_bpermute_b32 v92, v225, v206
	ds_bpermute_b32 v93, v225, v207
	ds_bpermute_b32 v94, v225, v140
	ds_bpermute_b32 v95, v225, v141
	ds_bpermute_b32 v120, v225, v142
	ds_bpermute_b32 v121, v225, v143
	ds_bpermute_b32 v122, v225, v216
	ds_bpermute_b32 v123, v225, v217
	s_waitcnt lgkmcnt(0)
	v_pk_add_f32 v[206:207], v[206:207], v[92:93]
	v_pk_add_f32 v[140:141], v[140:141], v[94:95]
	v_pk_add_f32 v[142:143], v[142:143], v[120:121]
	v_pk_add_f32 v[216:217], v[216:217], v[122:123]
	ds_bpermute_b32 v92, v225, v218
	ds_bpermute_b32 v93, v225, v219
	ds_bpermute_b32 v94, v225, v208
	ds_bpermute_b32 v95, v225, v209
	ds_bpermute_b32 v120, v225, v210
	ds_bpermute_b32 v121, v225, v211
	ds_bpermute_b32 v122, v225, v244
	ds_bpermute_b32 v123, v225, v245
	s_waitcnt lgkmcnt(0)
	v_pk_add_f32 v[218:219], v[218:219], v[92:93]
	v_pk_add_f32 v[208:209], v[208:209], v[94:95]
	v_pk_add_f32 v[210:211], v[210:211], v[120:121]
	v_pk_add_f32 v[244:245], v[244:245], v[122:123]
	ds_bpermute_b32 v92, v246, v206
	ds_bpermute_b32 v93, v246, v207
	ds_bpermute_b32 v94, v246, v140
	ds_bpermute_b32 v95, v246, v141
	ds_bpermute_b32 v120, v246, v142
	ds_bpermute_b32 v121, v246, v143
	ds_bpermute_b32 v122, v246, v216
	ds_bpermute_b32 v123, v246, v217
	s_waitcnt lgkmcnt(0)
	v_pk_add_f32 v[206:207], v[206:207], v[92:93]
	v_pk_add_f32 v[140:141], v[140:141], v[94:95]
	v_pk_add_f32 v[142:143], v[142:143], v[120:121]
	v_pk_add_f32 v[216:217], v[216:217], v[122:123]
	ds_bpermute_b32 v92, v246, v218
	ds_bpermute_b32 v93, v246, v219
	ds_bpermute_b32 v94, v246, v208
	ds_bpermute_b32 v95, v246, v209
	ds_bpermute_b32 v120, v246, v210
	ds_bpermute_b32 v121, v246, v211
	ds_bpermute_b32 v122, v246, v244
	ds_bpermute_b32 v123, v246, v245
	s_waitcnt lgkmcnt(0)
	v_pk_add_f32 v[218:219], v[218:219], v[92:93]
	v_pk_add_f32 v[208:209], v[208:209], v[94:95]
	v_pk_add_f32 v[210:211], v[210:211], v[120:121]
	v_pk_add_f32 v[244:245], v[244:245], v[122:123]
	s_mov_b64 exec, 0xffff
	global_store_dwordx2 v190, v[206:207], s[100:101] offset:0
	global_store_dwordx2 v190, v[140:141], s[100:101] offset:128
	global_store_dwordx2 v190, v[142:143], s[100:101] offset:256
	global_store_dwordx2 v190, v[216:217], s[100:101] offset:384
	global_store_dwordx2 v190, v[218:219], s[100:101] offset:1024
	global_store_dwordx2 v190, v[208:209], s[100:101] offset:1152
	global_store_dwordx2 v190, v[210:211], s[100:101] offset:1280
	global_store_dwordx2 v190, v[244:245], s[100:101] offset:1408
	s_mov_b64 exec, -1
	s_mov_b32 s83, s81
	s_mov_b32 s84, s82
	s_mov_b64 s[40:41], s[0:1]
	s_mov_b64 s[38:39], s[8:9]
	s_mov_b64 vcc, s[6:7]
	s_cbranch_vccz .LBB8_12
	s_waitcnt vmcnt(0)
	s_cmpk_gt_u32 s44, 0xff
	s_cbranch_scc1 .LBB8_31
	s_barrier

.LBB8_32:
	s_endpgm
	s_endpgm
	s_endpgm
	s_endpgm
	s_endpgm
	s_endpgm
	s_endpgm
	s_endpgm
	s_endpgm
	s_endpgm
	s_endpgm
	s_endpgm
	s_endpgm
	s_endpgm
	s_endpgm
	s_endpgm
	s_endpgm
	s_endpgm
	s_endpgm
	s_endpgm
	s_endpgm
	s_endpgm
	s_endpgm
	s_endpgm
	s_endpgm
	s_endpgm

.LBB9_27:
	ds_read_b128 v[128:131], v172
	ds_read_b128 v[132:135], v172 offset:1024
	ds_read_b128 v[136:139], v172 offset:2048
	ds_read_b128 v[140:143], v172 offset:3072
	s_add_u32 s30, s28, 0xfffd0080
	s_addc_u32 s31, s29, -1
	s_cmp_eq_u32 s73, 8
	s_cselect_b32 s35, s9, s31
	s_cselect_b32 s34, s8, s30
	s_cselect_b32 s31, s1, s72
	s_cselect_b32 s30, s0, s71
	s_add_i32 m0, s43, 0xc000
	ds_read_b128 v[158:161], v173
	ds_read_b128 v[162:165], v173 offset:1024
	ds_read_b128 v[178:181], v173 offset:2048
	ds_read_b128 v[182:185], v173 offset:3072
	ds_read_b128 v[186:189], v173 offset:4096
	ds_read_b128 v[190:193], v173 offset:5120
	ds_read_b128 v[194:197], v173 offset:6144
	ds_read_b128 v[198:201], v173 offset:7168
	global_load_lds_dwordx4 v152, s[28:29]
	s_add_i32 m0, s43, 0xe000
	s_nop 0
	global_load_lds_dwordx4 v154, s[28:29]
	s_waitcnt lgkmcnt(8)
	s_barrier
	s_waitcnt lgkmcnt(0)
	s_waitcnt lgkmcnt(0)
	v_mfma_f32_16x16x32_f16 v[124:127], v[128:131], v[158:161], v[124:127]
	v_mfma_f32_16x16x32_f16 v[120:123], v[136:139], v[158:161], v[120:123]
	v_mfma_f32_16x16x32_f16 v[108:111], v[128:131], v[178:181], v[108:111]
	v_mfma_f32_16x16x32_f16 v[104:107], v[136:139], v[178:181], v[104:107]
	v_mfma_f32_16x16x32_f16 v[96:99], v[128:131], v[186:189], v[96:99]
	v_mfma_f32_16x16x32_f16 v[88:91], v[136:139], v[186:189], v[88:91]
	v_mfma_f32_16x16x32_f16 v[80:83], v[128:131], v[194:197], v[80:83]
	v_mfma_f32_16x16x32_f16 v[72:75], v[136:139], v[194:197], v[72:75]
	v_mfma_f32_16x16x32_f16 v[124:127], v[132:135], v[162:165], v[124:127]
	v_mfma_f32_16x16x32_f16 v[120:123], v[140:143], v[162:165], v[120:123]
	v_mfma_f32_16x16x32_f16 v[108:111], v[132:135], v[182:185], v[108:111]
	v_mfma_f32_16x16x32_f16 v[104:107], v[140:143], v[182:185], v[104:107]
	v_mfma_f32_16x16x32_f16 v[96:99], v[132:135], v[190:193], v[96:99]
	v_mfma_f32_16x16x32_f16 v[88:91], v[140:143], v[190:193], v[88:91]
	v_mfma_f32_16x16x32_f16 v[80:83], v[132:135], v[198:201], v[80:83]
	v_mfma_f32_16x16x32_f16 v[72:75], v[140:143], v[198:201], v[72:75]
	s_barrier
	s_add_i32 s74, s65, s42
	s_add_u32 s78, s30, 0x80
	s_addc_u32 s79, s31, 0
	s_mov_b32 m0, s74
	ds_read_b128 v[202:205], v174
	ds_read_b128 v[206:209], v174 offset:1024
	ds_read_b128 v[210:213], v174 offset:2048
	ds_read_b128 v[214:217], v174 offset:3072
	global_load_lds_dwordx4 v146, s[30:31]
	s_add_i32 m0, s74, 0x2000
	s_nop 0
	global_load_lds_dwordx4 v150, s[30:31]
	s_barrier
	s_waitcnt lgkmcnt(0)
	s_waitcnt lgkmcnt(0)
	v_mfma_f32_16x16x32_f16 v[116:119], v[202:205], v[158:161], v[116:119]
	v_mfma_f32_16x16x32_f16 v[112:115], v[210:213], v[158:161], v[112:115]
	v_mfma_f32_16x16x32_f16 v[100:103], v[202:205], v[178:181], v[100:103]
	v_mfma_f32_16x16x32_f16 v[92:95], v[210:213], v[178:181], v[92:95]
	v_mfma_f32_16x16x32_f16 v[84:87], v[202:205], v[186:189], v[84:87]
	v_mfma_f32_16x16x32_f16 v[76:79], v[210:213], v[186:189], v[76:79]
	v_mfma_f32_16x16x32_f16 v[68:71], v[202:205], v[194:197], v[68:71]
	v_mfma_f32_16x16x32_f16 v[64:67], v[210:213], v[194:197], v[64:67]
	v_mfma_f32_16x16x32_f16 v[116:119], v[206:209], v[162:165], v[116:119]
	v_mfma_f32_16x16x32_f16 v[112:115], v[214:217], v[162:165], v[112:115]
	v_mfma_f32_16x16x32_f16 v[100:103], v[206:209], v[182:185], v[100:103]
	v_mfma_f32_16x16x32_f16 v[92:95], v[214:217], v[182:185], v[92:95]
	v_mfma_f32_16x16x32_f16 v[84:87], v[206:209], v[190:193], v[84:87]
	v_mfma_f32_16x16x32_f16 v[76:79], v[214:217], v[190:193], v[76:79]
	v_mfma_f32_16x16x32_f16 v[68:71], v[206:209], v[198:201], v[68:71]
	v_mfma_f32_16x16x32_f16 v[64:67], v[214:217], v[198:201], v[64:67]
	s_mov_b32 m0, s43
	s_add_u32 s80, s34, 0x80
	s_addc_u32 s81, s35, 0
	s_barrier
	ds_read_b128 v[158:161], v173 offset:16384
	ds_read_b128 v[162:165], v173 offset:17408
	ds_read_b128 v[178:181], v173 offset:18432
	ds_read_b128 v[182:185], v173 offset:19456
	ds_read_b128 v[186:189], v173 offset:20480
	ds_read_b128 v[190:193], v173 offset:21504
	ds_read_b128 v[194:197], v173 offset:22528
	ds_read_b128 v[198:201], v173 offset:23552
	global_load_lds_dwordx4 v144, s[34:35]
	s_mov_b32 m0, s44
	s_nop 0
	global_load_lds_dwordx4 v148, s[34:35]
	s_barrier
	s_waitcnt lgkmcnt(0)
	s_waitcnt lgkmcnt(0)
	v_mfma_f32_16x16x32_f16 v[60:63], v[128:131], v[158:161], v[60:63]
	v_mfma_f32_16x16x32_f16 v[56:59], v[136:139], v[158:161], v[56:59]
	v_mfma_f32_16x16x32_f16 v[48:51], v[128:131], v[178:181], v[48:51]
	v_mfma_f32_16x16x32_f16 v[40:43], v[136:139], v[178:181], v[40:43]
	v_mfma_f32_16x16x32_f16 v[32:35], v[128:131], v[186:189], v[32:35]
	v_mfma_f32_16x16x32_f16 v[24:27], v[136:139], v[186:189], v[24:27]
	v_mfma_f32_16x16x32_f16 v[16:19], v[128:131], v[194:197], v[16:19]
	v_mfma_f32_16x16x32_f16 v[8:11], v[136:139], v[194:197], v[8:11]
	v_mfma_f32_16x16x32_f16 v[60:63], v[132:135], v[162:165], v[60:63]
	v_mfma_f32_16x16x32_f16 v[56:59], v[140:143], v[162:165], v[56:59]
	v_mfma_f32_16x16x32_f16 v[48:51], v[132:135], v[182:185], v[48:51]
	v_mfma_f32_16x16x32_f16 v[40:43], v[140:143], v[182:185], v[40:43]
	v_mfma_f32_16x16x32_f16 v[32:35], v[132:135], v[190:193], v[32:35]
	v_mfma_f32_16x16x32_f16 v[24:27], v[140:143], v[190:193], v[24:27]
	v_mfma_f32_16x16x32_f16 v[16:19], v[132:135], v[198:201], v[16:19]
	v_mfma_f32_16x16x32_f16 v[8:11], v[140:143], v[198:201], v[8:11]
	s_barrier
	s_add_u32 s74, s30, 0xc000
	s_addc_u32 s75, s31, 0
	s_add_i32 s76, s66, s42
	s_mov_b32 m0, s76
	s_nop 0
	global_load_lds_dwordx4 v146, s[74:75]
	s_add_i32 m0, s76, 0x2000
	s_nop 0
	global_load_lds_dwordx4 v150, s[74:75]
	s_waitcnt vmcnt(6)
	s_barrier
	v_mfma_f32_16x16x32_f16 v[52:55], v[202:205], v[158:161], v[52:55]
	v_mfma_f32_16x16x32_f16 v[44:47], v[210:213], v[158:161], v[44:47]
	v_mfma_f32_16x16x32_f16 v[36:39], v[202:205], v[178:181], v[36:39]
	v_mfma_f32_16x16x32_f16 v[28:31], v[210:213], v[178:181], v[28:31]
	v_mfma_f32_16x16x32_f16 v[20:23], v[202:205], v[186:189], v[20:23]
	v_mfma_f32_16x16x32_f16 v[12:15], v[210:213], v[186:189], v[12:15]
	v_mfma_f32_16x16x32_f16 v[4:7], v[202:205], v[194:197], v[4:7]
	v_mfma_f32_16x16x32_f16 v[0:3], v[210:213], v[194:197], v[0:3]
	v_mfma_f32_16x16x32_f16 v[52:55], v[206:209], v[162:165], v[52:55]
	v_mfma_f32_16x16x32_f16 v[44:47], v[214:217], v[162:165], v[44:47]
	v_mfma_f32_16x16x32_f16 v[36:39], v[206:209], v[182:185], v[36:39]
	v_mfma_f32_16x16x32_f16 v[28:31], v[214:217], v[182:185], v[28:31]
	v_mfma_f32_16x16x32_f16 v[20:23], v[206:209], v[190:193], v[20:23]
	v_mfma_f32_16x16x32_f16 v[12:15], v[214:217], v[190:193], v[12:15]
	v_mfma_f32_16x16x32_f16 v[4:7], v[206:209], v[198:201], v[4:7]
	v_mfma_f32_16x16x32_f16 v[0:3], v[214:217], v[198:201], v[0:3]
	s_add_i32 s74, 0, 0x18000
	v_add_u32_e32 v140, s74, v168
	s_barrier
	ds_read_b128 v[128:131], v140
	ds_read_b128 v[132:135], v140 offset:1024
	ds_read_b128 v[136:139], v140 offset:2048
	ds_read_b128 v[140:143], v140 offset:3072
	s_add_u32 s34, s34, 0x30000
	s_addc_u32 s35, s35, 0
	s_mov_b32 m0, s45
	ds_read_b128 v[158:161], v173 offset:32768
	ds_read_b128 v[162:165], v173 offset:33792
	ds_read_b128 v[178:181], v173 offset:34816
	ds_read_b128 v[182:185], v173 offset:35840
	ds_read_b128 v[186:189], v173 offset:36864
	ds_read_b128 v[190:193], v173 offset:37888
	ds_read_b128 v[194:197], v173 offset:38912
	ds_read_b128 v[198:201], v173 offset:39936
	global_load_lds_dwordx4 v144, s[34:35]
	s_mov_b32 m0, s46
	s_nop 0
	global_load_lds_dwordx4 v148, s[34:35]
	s_waitcnt lgkmcnt(8)
	s_barrier
	s_waitcnt lgkmcnt(0)
	s_waitcnt lgkmcnt(0)
	v_mfma_f32_16x16x32_f16 v[124:127], v[128:131], v[158:161], v[124:127]
	v_mfma_f32_16x16x32_f16 v[120:123], v[136:139], v[158:161], v[120:123]
	v_mfma_f32_16x16x32_f16 v[108:111], v[128:131], v[178:181], v[108:111]
	v_mfma_f32_16x16x32_f16 v[104:107], v[136:139], v[178:181], v[104:107]
	v_mfma_f32_16x16x32_f16 v[96:99], v[128:131], v[186:189], v[96:99]
	v_mfma_f32_16x16x32_f16 v[88:91], v[136:139], v[186:189], v[88:91]
	v_mfma_f32_16x16x32_f16 v[80:83], v[128:131], v[194:197], v[80:83]
	v_mfma_f32_16x16x32_f16 v[72:75], v[136:139], v[194:197], v[72:75]
	v_mfma_f32_16x16x32_f16 v[124:127], v[132:135], v[162:165], v[124:127]
	v_mfma_f32_16x16x32_f16 v[120:123], v[140:143], v[162:165], v[120:123]
	v_mfma_f32_16x16x32_f16 v[108:111], v[132:135], v[182:185], v[108:111]
	v_mfma_f32_16x16x32_f16 v[104:107], v[140:143], v[182:185], v[104:107]
	v_mfma_f32_16x16x32_f16 v[96:99], v[132:135], v[190:193], v[96:99]
	v_mfma_f32_16x16x32_f16 v[88:91], v[140:143], v[190:193], v[88:91]
	v_mfma_f32_16x16x32_f16 v[80:83], v[132:135], v[198:201], v[80:83]
	v_mfma_f32_16x16x32_f16 v[72:75], v[140:143], v[198:201], v[72:75]
	s_barrier
	s_add_i32 s34, 0, 0x1c000
	s_add_i32 s35, s74, s42
	v_add_u32_e32 v177, s34, v168
	s_mov_b32 m0, s35
	ds_read_b128 v[202:205], v177
	ds_read_b128 v[206:209], v177 offset:1024
	ds_read_b128 v[210:213], v177 offset:2048
	ds_read_b128 v[214:217], v177 offset:3072
	global_load_lds_dwordx4 v146, s[78:79]
	s_add_i32 m0, s35, 0x2000
	s_nop 0
	global_load_lds_dwordx4 v150, s[78:79]
	s_barrier
	s_waitcnt lgkmcnt(0)
	s_waitcnt lgkmcnt(0)
	v_mfma_f32_16x16x32_f16 v[116:119], v[202:205], v[158:161], v[116:119]
	v_mfma_f32_16x16x32_f16 v[112:115], v[210:213], v[158:161], v[112:115]
	v_mfma_f32_16x16x32_f16 v[100:103], v[202:205], v[178:181], v[100:103]
	v_mfma_f32_16x16x32_f16 v[92:95], v[210:213], v[178:181], v[92:95]
	v_mfma_f32_16x16x32_f16 v[84:87], v[202:205], v[186:189], v[84:87]
	v_mfma_f32_16x16x32_f16 v[76:79], v[210:213], v[186:189], v[76:79]
	v_mfma_f32_16x16x32_f16 v[68:71], v[202:205], v[194:197], v[68:71]
	v_mfma_f32_16x16x32_f16 v[64:67], v[210:213], v[194:197], v[64:67]
	v_mfma_f32_16x16x32_f16 v[116:119], v[206:209], v[162:165], v[116:119]
	v_mfma_f32_16x16x32_f16 v[112:115], v[214:217], v[162:165], v[112:115]
	v_mfma_f32_16x16x32_f16 v[100:103], v[206:209], v[182:185], v[100:103]
	v_mfma_f32_16x16x32_f16 v[92:95], v[214:217], v[182:185], v[92:95]
	v_mfma_f32_16x16x32_f16 v[84:87], v[206:209], v[190:193], v[84:87]
	v_mfma_f32_16x16x32_f16 v[76:79], v[214:217], v[190:193], v[76:79]
	v_mfma_f32_16x16x32_f16 v[68:71], v[206:209], v[198:201], v[68:71]
	v_mfma_f32_16x16x32_f16 v[64:67], v[214:217], v[198:201], v[64:67]
	s_mov_b32 m0, s49
	s_barrier
	ds_read_b128 v[158:161], v173 offset:49152
	ds_read_b128 v[162:165], v173 offset:50176
	ds_read_b128 v[178:181], v173 offset:51200
	ds_read_b128 v[182:185], v173 offset:52224
	ds_read_b128 v[186:189], v173 offset:53248
	ds_read_b128 v[190:193], v173 offset:54272
	ds_read_b128 v[194:197], v173 offset:55296
	ds_read_b128 v[198:201], v173 offset:56320
	global_load_lds_dwordx4 v144, s[80:81]
	s_mov_b32 m0, s50
	s_nop 0
	global_load_lds_dwordx4 v148, s[80:81]
	s_barrier
	s_waitcnt lgkmcnt(0)
	s_waitcnt lgkmcnt(0)
	v_mfma_f32_16x16x32_f16 v[60:63], v[128:131], v[158:161], v[60:63]
	v_mfma_f32_16x16x32_f16 v[56:59], v[136:139], v[158:161], v[56:59]
	v_mfma_f32_16x16x32_f16 v[48:51], v[128:131], v[178:181], v[48:51]
	v_mfma_f32_16x16x32_f16 v[40:43], v[136:139], v[178:181], v[40:43]
	v_mfma_f32_16x16x32_f16 v[32:35], v[128:131], v[186:189], v[32:35]
	v_mfma_f32_16x16x32_f16 v[24:27], v[136:139], v[186:189], v[24:27]
	v_mfma_f32_16x16x32_f16 v[16:19], v[128:131], v[194:197], v[16:19]
	v_mfma_f32_16x16x32_f16 v[8:11], v[136:139], v[194:197], v[8:11]
	v_mfma_f32_16x16x32_f16 v[60:63], v[132:135], v[162:165], v[60:63]
	v_mfma_f32_16x16x32_f16 v[56:59], v[140:143], v[162:165], v[56:59]
	v_mfma_f32_16x16x32_f16 v[48:51], v[132:135], v[182:185], v[48:51]
	v_mfma_f32_16x16x32_f16 v[40:43], v[140:143], v[182:185], v[40:43]
	v_mfma_f32_16x16x32_f16 v[32:35], v[132:135], v[190:193], v[32:35]
	v_mfma_f32_16x16x32_f16 v[24:27], v[140:143], v[190:193], v[24:27]
	v_mfma_f32_16x16x32_f16 v[16:19], v[132:135], v[198:201], v[16:19]
	v_mfma_f32_16x16x32_f16 v[8:11], v[140:143], v[198:201], v[8:11]
	s_barrier
	s_add_u32 s30, s30, 0xc080
	s_addc_u32 s31, s31, 0
	s_add_i32 s34, s34, s42
	s_mov_b32 m0, s34
	s_nop 0
	global_load_lds_dwordx4 v146, s[30:31]
	s_add_i32 m0, s34, 0x2000
	s_nop 0
	global_load_lds_dwordx4 v150, s[30:31]
	s_waitcnt vmcnt(6)
	s_barrier
	v_mfma_f32_16x16x32_f16 v[52:55], v[202:205], v[158:161], v[52:55]
	v_mfma_f32_16x16x32_f16 v[44:47], v[210:213], v[158:161], v[44:47]
	v_mfma_f32_16x16x32_f16 v[36:39], v[202:205], v[178:181], v[36:39]
	v_mfma_f32_16x16x32_f16 v[28:31], v[210:213], v[178:181], v[28:31]
	v_mfma_f32_16x16x32_f16 v[20:23], v[202:205], v[186:189], v[20:23]
	v_mfma_f32_16x16x32_f16 v[12:15], v[210:213], v[186:189], v[12:15]
	v_mfma_f32_16x16x32_f16 v[4:7], v[202:205], v[194:197], v[4:7]
	v_mfma_f32_16x16x32_f16 v[0:3], v[210:213], v[194:197], v[0:3]
	v_mfma_f32_16x16x32_f16 v[52:55], v[206:209], v[162:165], v[52:55]
	v_mfma_f32_16x16x32_f16 v[44:47], v[214:217], v[162:165], v[44:47]
	v_mfma_f32_16x16x32_f16 v[36:39], v[206:209], v[182:185], v[36:39]
	v_mfma_f32_16x16x32_f16 v[28:31], v[214:217], v[182:185], v[28:31]
	v_mfma_f32_16x16x32_f16 v[20:23], v[206:209], v[190:193], v[20:23]
	v_mfma_f32_16x16x32_f16 v[12:15], v[214:217], v[190:193], v[12:15]
	v_mfma_f32_16x16x32_f16 v[4:7], v[206:209], v[198:201], v[4:7]
	v_mfma_f32_16x16x32_f16 v[0:3], v[214:217], v[198:201], v[0:3]
	s_add_i32 s73, s73, 2
	s_add_u32 s28, s28, 0x100
	s_addc_u32 s29, s29, 0
	s_add_u32 s71, s71, 0x100
	s_addc_u32 s72, s72, 0
	s_cmp_gt_u32 s73, 9
	s_barrier
	s_cbranch_scc0 .LBB9_27
	s_lshl_b32 s28, s70, 8
	s_add_i32 s28, s28, s48
	s_lshl_b32 s29, s68, 8
	s_or_b32 s29, s29, s51
	s_waitcnt vmcnt(6)
	v_pk_fma_f32 v[126:127], v[126:127], v[226:227], v[236:237] op_sel_hi:[1,0,1]
	v_pk_fma_f32 v[124:125], v[124:125], v[226:227], v[234:235] op_sel_hi:[1,0,1]
	v_pk_fma_f32 v[122:123], v[122:123], v[226:227], v[240:241] op_sel_hi:[1,0,1]
	v_pk_fma_f32 v[120:121], v[120:121], v[226:227], v[238:239] op_sel_hi:[1,0,1]
	v_cvt_pk_f16_f32 v124, v124, v125
	v_cvt_pk_f16_f32 v125, v126, v127
	v_cvt_pk_f16_f32 v126, v120, v121
	v_cvt_pk_f16_f32 v123, v122, v123
	v_pk_fma_f32 v[118:119], v[118:119], v[226:227], v[244:245] op_sel_hi:[1,0,1]
	v_pk_fma_f32 v[116:117], v[116:117], v[226:227], v[242:243] op_sel_hi:[1,0,1]
	v_pk_fma_f32 v[114:115], v[114:115], v[226:227], v[248:249] op_sel_hi:[1,0,1]
	v_pk_fma_f32 v[112:113], v[112:113], v[226:227], v[246:247] op_sel_hi:[1,0,1]
	v_pk_max_f16 v120, v124, 0
	v_pk_max_f16 v121, v125, 0
	v_pk_max_f16 v122, v126, 0
	v_pk_max_f16 v123, v123, 0
	v_cvt_pk_f16_f32 v116, v116, v117
	v_cvt_pk_f16_f32 v117, v118, v119
	v_cvt_pk_f16_f32 v118, v112, v113
	v_cvt_pk_f16_f32 v115, v114, v115
	v_pk_fma_f32 v[110:111], v[110:111], v[226:227], v[236:237] op_sel:[0,1,0]
	v_pk_fma_f32 v[108:109], v[108:109], v[226:227], v[234:235] op_sel:[0,1,0]
	v_pk_fma_f32 v[106:107], v[106:107], v[226:227], v[240:241] op_sel:[0,1,0]
	v_pk_fma_f32 v[104:105], v[104:105], v[226:227], v[238:239] op_sel:[0,1,0]
	v_pk_fma_f32 v[102:103], v[102:103], v[226:227], v[244:245] op_sel:[0,1,0]
	v_pk_fma_f32 v[100:101], v[100:101], v[226:227], v[242:243] op_sel:[0,1,0]
	v_pk_fma_f32 v[94:95], v[94:95], v[226:227], v[248:249] op_sel:[0,1,0]
	v_pk_fma_f32 v[92:93], v[92:93], v[226:227], v[246:247] op_sel:[0,1,0]
	ds_write_b128 v175, v[120:123]
	v_or_b32_e32 v120, s28, v169
	v_pk_max_f16 v112, v116, 0
	v_pk_max_f16 v113, v117, 0
	v_pk_max_f16 v114, v118, 0
	v_pk_max_f16 v115, v115, 0
	v_cvt_pk_f16_f32 v108, v108, v109
	v_cvt_pk_f16_f32 v109, v110, v111
	v_cvt_pk_f16_f32 v110, v104, v105
	v_cvt_pk_f16_f32 v107, v106, v107
	v_cvt_pk_f16_f32 v100, v100, v101
	v_cvt_pk_f16_f32 v101, v102, v103
	v_cvt_pk_f16_f32 v102, v92, v93
	v_cvt_pk_f16_f32 v95, v94, v95
	ds_write_b128 v175, v[112:115] offset:64
	v_mul_lo_u32 v116, v120, s10
	v_pk_max_f16 v104, v108, 0
	v_pk_max_f16 v105, v109, 0
	v_pk_max_f16 v106, v110, 0
	v_pk_max_f16 v107, v107, 0
	v_pk_max_f16 v92, v100, 0
	v_pk_max_f16 v93, v101, 0
	v_pk_max_f16 v94, v102, 0
	v_pk_max_f16 v95, v95, 0
	ds_read_b128 v[112:115], v176
	v_add_u32_e32 v120, s29, v116
	ds_read_b128 v[116:119], v176 offset:1152
	ds_write_b128 v175, v[104:107]
	ds_write_b128 v175, v[92:95] offset:64
	ds_read_b128 v[92:95], v176
	ds_read_b128 v[100:103], v176 offset:1152
	v_lshlrev_b32_e32 v121, 1, v120
	v_add_u32_e32 v122, v121, v170
	v_add_u32_e32 v104, s55, v121
	s_waitcnt lgkmcnt(0)
	buffer_store_dwordx4 v[112:115], v122, s[20:23], 0 offen nt
	v_add_u32_e32 v105, v104, v170
	v_pk_fma_f32 v[90:91], v[90:91], v[228:229], v[240:241] op_sel_hi:[1,0,1]
	v_add_u32_e32 v112, v121, v171
	buffer_store_dwordx4 v[116:119], v112, s[20:23], 0 offen nt
	buffer_store_dwordx4 v[92:95], v105, s[20:23], 0 offen nt
	v_pk_fma_f32 v[88:89], v[88:89], v[228:229], v[238:239] op_sel_hi:[1,0,1]
	v_pk_fma_f32 v[86:87], v[86:87], v[228:229], v[244:245] op_sel_hi:[1,0,1]
	v_pk_fma_f32 v[92:93], v[98:99], v[228:229], v[236:237] op_sel_hi:[1,0,1]
	v_pk_fma_f32 v[94:95], v[96:97], v[228:229], v[234:235] op_sel_hi:[1,0,1]
	v_pk_fma_f32 v[84:85], v[84:85], v[228:229], v[242:243] op_sel_hi:[1,0,1]
	v_pk_fma_f32 v[78:79], v[78:79], v[228:229], v[248:249] op_sel_hi:[1,0,1]
	v_pk_fma_f32 v[76:77], v[76:77], v[228:229], v[246:247] op_sel_hi:[1,0,1]
	v_cvt_pk_f16_f32 v94, v94, v95
	v_cvt_pk_f16_f32 v92, v92, v93
	v_cvt_pk_f16_f32 v93, v88, v89
	v_cvt_pk_f16_f32 v91, v90, v91
	v_cvt_pk_f16_f32 v84, v84, v85
	v_cvt_pk_f16_f32 v85, v86, v87
	v_cvt_pk_f16_f32 v86, v76, v77
	v_cvt_pk_f16_f32 v79, v78, v79
	v_pk_max_f16 v88, v94, 0
	v_pk_max_f16 v89, v92, 0
	v_pk_max_f16 v90, v93, 0
	v_pk_max_f16 v91, v91, 0
	v_pk_max_f16 v76, v84, 0
	v_pk_max_f16 v77, v85, 0
	v_pk_max_f16 v78, v86, 0
	v_pk_max_f16 v79, v79, 0
	ds_write_b128 v175, v[88:91]
	ds_write_b128 v175, v[76:79] offset:64
	ds_read_b128 v[76:79], v176
	ds_read_b128 v[84:87], v176 offset:1152
	v_add_u32_e32 v88, s55, v104
	v_add_u32_e32 v105, v104, v171
	v_add_u32_e32 v89, v88, v170
	buffer_store_dwordx4 v[100:103], v105, s[20:23], 0 offen nt
	s_waitcnt lgkmcnt(1)
	buffer_store_dwordx4 v[76:79], v89, s[20:23], 0 offen nt
	v_pk_fma_f32 v[74:75], v[74:75], v[228:229], v[240:241] op_sel:[0,1,0]
	v_pk_fma_f32 v[72:73], v[72:73], v[228:229], v[238:239] op_sel:[0,1,0]
	v_add_u32_e32 v76, v88, v171
	s_waitcnt lgkmcnt(0)
	buffer_store_dwordx4 v[84:87], v76, s[20:23], 0 offen nt
	v_pk_fma_f32 v[76:77], v[82:83], v[228:229], v[236:237] op_sel:[0,1,0]
	v_pk_fma_f32 v[78:79], v[80:81], v[228:229], v[234:235] op_sel:[0,1,0]
	v_pk_fma_f32 v[70:71], v[70:71], v[228:229], v[244:245] op_sel:[0,1,0]
	v_pk_fma_f32 v[68:69], v[68:69], v[228:229], v[242:243] op_sel:[0,1,0]
	v_pk_fma_f32 v[66:67], v[66:67], v[228:229], v[248:249] op_sel:[0,1,0]
	v_pk_fma_f32 v[64:65], v[64:65], v[228:229], v[246:247] op_sel:[0,1,0]
	v_cvt_pk_f16_f32 v78, v78, v79
	v_cvt_pk_f16_f32 v76, v76, v77
	v_cvt_pk_f16_f32 v77, v72, v73
	v_cvt_pk_f16_f32 v75, v74, v75
	v_cvt_pk_f16_f32 v68, v68, v69
	v_cvt_pk_f16_f32 v69, v70, v71
	v_cvt_pk_f16_f32 v70, v64, v65
	v_cvt_pk_f16_f32 v67, v66, v67
	v_pk_fma_f32 v[62:63], v[62:63], v[230:231], v[236:237] op_sel_hi:[1,0,1]
	v_pk_fma_f32 v[60:61], v[60:61], v[230:231], v[234:235] op_sel_hi:[1,0,1]
	v_pk_fma_f32 v[58:59], v[58:59], v[230:231], v[240:241] op_sel_hi:[1,0,1]
	v_pk_fma_f32 v[56:57], v[56:57], v[230:231], v[238:239] op_sel_hi:[1,0,1]
	v_pk_fma_f32 v[54:55], v[54:55], v[230:231], v[244:245] op_sel_hi:[1,0,1]
	v_pk_fma_f32 v[52:53], v[52:53], v[230:231], v[242:243] op_sel_hi:[1,0,1]
	v_pk_fma_f32 v[46:47], v[46:47], v[230:231], v[248:249] op_sel_hi:[1,0,1]
	v_pk_fma_f32 v[44:45], v[44:45], v[230:231], v[246:247] op_sel_hi:[1,0,1]
	v_pk_max_f16 v72, v78, 0
	v_pk_max_f16 v73, v76, 0
	v_pk_max_f16 v74, v77, 0
	v_pk_max_f16 v75, v75, 0
	v_pk_max_f16 v64, v68, 0
	v_pk_max_f16 v65, v69, 0
	v_pk_max_f16 v66, v70, 0
	v_pk_max_f16 v67, v67, 0
	v_cvt_pk_f16_f32 v60, v60, v61
	v_cvt_pk_f16_f32 v61, v62, v63
	v_cvt_pk_f16_f32 v62, v56, v57
	v_cvt_pk_f16_f32 v59, v58, v59
	v_cvt_pk_f16_f32 v52, v52, v53
	v_cvt_pk_f16_f32 v53, v54, v55
	v_cvt_pk_f16_f32 v54, v44, v45
	v_cvt_pk_f16_f32 v47, v46, v47
	ds_write_b128 v175, v[72:75]
	ds_write_b128 v175, v[64:67] offset:64
	v_pk_max_f16 v56, v60, 0
	v_pk_max_f16 v57, v61, 0
	v_pk_max_f16 v58, v62, 0
	v_pk_max_f16 v59, v59, 0
	v_pk_max_f16 v44, v52, 0
	v_pk_max_f16 v45, v53, 0
	v_pk_max_f16 v46, v54, 0
	v_pk_max_f16 v47, v47, 0
	ds_read_b128 v[64:67], v176
	ds_read_b128 v[68:71], v176 offset:1152
	ds_write_b128 v175, v[56:59]
	ds_write_b128 v175, v[44:47] offset:64
	ds_read_b128 v[44:47], v176
	ds_read_b128 v[52:55], v176 offset:1152
	v_add_u32_e32 v72, s56, v120
	v_lshlrev_b32_e32 v73, 1, v72
	v_add_u32_e32 v74, v73, v170
	v_add_u32_e32 v56, s62, v88
	s_waitcnt lgkmcnt(5)
	buffer_store_dwordx4 v[64:67], v74, s[20:23], 0 offen nt
	v_add_u32_e32 v57, v56, v170
	v_pk_fma_f32 v[42:43], v[42:43], v[230:231], v[240:241] op_sel:[0,1,0]
	v_add_u32_e32 v64, v73, v171
	s_waitcnt lgkmcnt(4)
	buffer_store_dwordx4 v[68:71], v64, s[20:23], 0 offen nt
	s_waitcnt lgkmcnt(1)
	buffer_store_dwordx4 v[44:47], v57, s[20:23], 0 offen nt
	v_pk_fma_f32 v[40:41], v[40:41], v[230:231], v[238:239] op_sel:[0,1,0]
	v_pk_fma_f32 v[38:39], v[38:39], v[230:231], v[244:245] op_sel:[0,1,0]
	v_add_u32_e32 v44, v56, v171
	s_waitcnt lgkmcnt(0)
	buffer_store_dwordx4 v[52:55], v44, s[20:23], 0 offen nt
	v_pk_fma_f32 v[44:45], v[50:51], v[230:231], v[236:237] op_sel:[0,1,0]
	v_pk_fma_f32 v[46:47], v[48:49], v[230:231], v[234:235] op_sel:[0,1,0]
	v_pk_fma_f32 v[36:37], v[36:37], v[230:231], v[242:243] op_sel:[0,1,0]
	v_pk_fma_f32 v[30:31], v[30:31], v[230:231], v[248:249] op_sel:[0,1,0]
	v_pk_fma_f32 v[28:29], v[28:29], v[230:231], v[246:247] op_sel:[0,1,0]
	v_cvt_pk_f16_f32 v46, v46, v47
	v_cvt_pk_f16_f32 v44, v44, v45
	v_cvt_pk_f16_f32 v45, v40, v41
	v_cvt_pk_f16_f32 v43, v42, v43
	v_cvt_pk_f16_f32 v36, v36, v37
	v_cvt_pk_f16_f32 v37, v38, v39
	v_cvt_pk_f16_f32 v38, v28, v29
	v_cvt_pk_f16_f32 v31, v30, v31
	v_pk_max_f16 v40, v46, 0
	v_pk_max_f16 v41, v44, 0
	v_pk_max_f16 v42, v45, 0
	v_pk_max_f16 v43, v43, 0
	v_pk_max_f16 v28, v36, 0
	v_pk_max_f16 v29, v37, 0
	v_pk_max_f16 v30, v38, 0
	v_pk_max_f16 v31, v31, 0
	ds_write_b128 v175, v[40:43]
	ds_write_b128 v175, v[28:31] offset:64
	ds_read_b128 v[28:31], v176
	ds_read_b128 v[36:39], v176 offset:1152
	v_add_u32_e32 v40, s63, v72
	v_lshlrev_b32_e32 v41, 1, v40
	v_add_u32_e32 v42, v41, v170
	s_waitcnt lgkmcnt(1)
	buffer_store_dwordx4 v[28:31], v42, s[20:23], 0 offen nt
	v_pk_fma_f32 v[26:27], v[26:27], v[232:233], v[240:241] op_sel_hi:[1,0,1]
	v_pk_fma_f32 v[24:25], v[24:25], v[232:233], v[238:239] op_sel_hi:[1,0,1]
	v_add_u32_e32 v28, v41, v171
	s_waitcnt lgkmcnt(0)
	buffer_store_dwordx4 v[36:39], v28, s[20:23], 0 offen nt
	v_pk_fma_f32 v[28:29], v[34:35], v[232:233], v[236:237] op_sel_hi:[1,0,1]
	v_pk_fma_f32 v[30:31], v[32:33], v[232:233], v[234:235] op_sel_hi:[1,0,1]
	v_pk_fma_f32 v[22:23], v[22:23], v[232:233], v[244:245] op_sel_hi:[1,0,1]
	v_pk_fma_f32 v[20:21], v[20:21], v[232:233], v[242:243] op_sel_hi:[1,0,1]
	v_pk_fma_f32 v[14:15], v[14:15], v[232:233], v[248:249] op_sel_hi:[1,0,1]
	v_pk_fma_f32 v[12:13], v[12:13], v[232:233], v[246:247] op_sel_hi:[1,0,1]
	v_cvt_pk_f16_f32 v30, v30, v31
	v_cvt_pk_f16_f32 v28, v28, v29
	v_cvt_pk_f16_f32 v29, v24, v25
	v_cvt_pk_f16_f32 v27, v26, v27
	v_cvt_pk_f16_f32 v20, v20, v21
	v_cvt_pk_f16_f32 v21, v22, v23
	v_cvt_pk_f16_f32 v22, v12, v13
	v_cvt_pk_f16_f32 v15, v14, v15
	v_pk_max_f16 v24, v30, 0
	v_pk_max_f16 v25, v28, 0
	v_pk_max_f16 v26, v29, 0
	v_pk_max_f16 v27, v27, 0
	v_pk_max_f16 v12, v20, 0
	v_pk_max_f16 v13, v21, 0
	v_pk_max_f16 v14, v22, 0
	v_pk_max_f16 v15, v15, 0
	ds_write_b128 v175, v[24:27]
	ds_write_b128 v175, v[12:15] offset:64
	ds_read_b128 v[12:15], v176
	ds_read_b128 v[20:23], v176 offset:1152
	v_add_u32_e32 v24, s64, v40
	v_lshlrev_b32_e32 v25, 1, v24
	v_add_u32_e32 v26, v25, v170
	s_waitcnt lgkmcnt(1)
	buffer_store_dwordx4 v[12:15], v26, s[20:23], 0 offen nt
	v_pk_fma_f32 v[10:11], v[10:11], v[232:233], v[240:241] op_sel:[0,1,0]
	v_pk_fma_f32 v[8:9], v[8:9], v[232:233], v[238:239] op_sel:[0,1,0]
	v_pk_fma_f32 v[12:13], v[18:19], v[232:233], v[236:237] op_sel:[0,1,0]
	v_pk_fma_f32 v[14:15], v[16:17], v[232:233], v[234:235] op_sel:[0,1,0]
	v_pk_fma_f32 v[6:7], v[6:7], v[232:233], v[244:245] op_sel:[0,1,0]
	v_pk_fma_f32 v[4:5], v[4:5], v[232:233], v[242:243] op_sel:[0,1,0]
	v_pk_fma_f32 v[2:3], v[2:3], v[232:233], v[248:249] op_sel:[0,1,0]
	v_pk_fma_f32 v[0:1], v[0:1], v[232:233], v[246:247] op_sel:[0,1,0]
	v_cvt_pk_f16_f32 v14, v14, v15
	v_cvt_pk_f16_f32 v12, v12, v13
	v_cvt_pk_f16_f32 v13, v8, v9
	v_cvt_pk_f16_f32 v11, v10, v11
	v_cvt_pk_f16_f32 v4, v4, v5
	v_cvt_pk_f16_f32 v5, v6, v7
	v_cvt_pk_f16_f32 v6, v0, v1
	v_cvt_pk_f16_f32 v3, v2, v3
	v_pk_max_f16 v8, v14, 0
	v_pk_max_f16 v9, v12, 0
	v_pk_max_f16 v10, v13, 0
	v_pk_max_f16 v11, v11, 0
	v_pk_max_f16 v0, v4, 0
	v_pk_max_f16 v1, v5, 0
	v_pk_max_f16 v2, v6, 0
	v_pk_max_f16 v3, v3, 0
	ds_write_b128 v175, v[8:11]
	ds_write_b128 v175, v[0:3] offset:64
	ds_read_b128 v[0:3], v176
	ds_read_b128 v[4:7], v176 offset:1152
	v_add_lshl_u32 v8, v24, s64, 1
	v_add_u32_e32 v25, v25, v171
	v_add_u32_e32 v9, v8, v170
	s_waitcnt lgkmcnt(4)
	buffer_store_dwordx4 v[20:23], v25, s[20:23], 0 offen nt
	s_waitcnt lgkmcnt(1)
	buffer_store_dwordx4 v[0:3], v9, s[20:23], 0 offen nt
	s_mov_b32 s68, s67
	s_mov_b32 s70, s69
	v_add_u32_e32 v0, v8, v171
	s_mov_b64 s[30:31], s[0:1]
	s_mov_b64 s[28:29], s[8:9]
	s_mov_b64 vcc, s[6:7]
	s_waitcnt lgkmcnt(0)
	buffer_store_dwordx4 v[4:7], v0, s[20:23], 0 offen nt
	s_cbranch_vccz .LBB9_12
	s_waitcnt vmcnt(0)
	s_cmpk_gt_u32 s36, 0xff
	s_cbranch_scc1 .LBB9_31
	s_barrier

.LBB9_32:
	s_endpgm
	s_endpgm
	s_endpgm
	s_endpgm
	s_endpgm
	s_endpgm
	s_endpgm
	s_endpgm
	s_endpgm
	s_endpgm
	s_endpgm
	s_endpgm
	s_endpgm
	s_endpgm
	s_endpgm
	s_endpgm
	s_endpgm
	s_endpgm
	s_endpgm
	s_endpgm
	s_endpgm
	s_endpgm
	s_endpgm
	s_endpgm
	s_endpgm
	s_endpgm
	s_endpgm
	s_endpgm
	s_endpgm
	s_endpgm
	s_endpgm
	s_endpgm
	s_endpgm

	.amdhsa_kernel _Z6k_gemmIN2pg6EpiLinILi1EEELi768EEvNS0_4GemmET_
		.amdhsa_group_segment_fixed_size 0
		.amdhsa_private_segment_fixed_size 0
		.amdhsa_kernarg_size 320
		.amdhsa_user_sgpr_count 2
		.amdhsa_user_sgpr_dispatch_ptr 0
		.amdhsa_user_sgpr_queue_ptr 0
		.amdhsa_user_sgpr_kernarg_segment_ptr 1
		.amdhsa_user_sgpr_dispatch_id 0
		.amdhsa_user_sgpr_kernarg_preload_length 0
		.amdhsa_user_sgpr_kernarg_preload_offset 0
		.amdhsa_user_sgpr_private_segment_size 0
		.amdhsa_uses_dynamic_stack 0
		.amdhsa_enable_private_segment 0
		.amdhsa_system_sgpr_workgroup_id_x 1
		.amdhsa_system_sgpr_workgroup_id_y 0
		.amdhsa_system_sgpr_workgroup_id_z 0
		.amdhsa_system_sgpr_workgroup_info 0
		.amdhsa_system_vgpr_workitem_id 0
		.amdhsa_next_free_vgpr 254
		.amdhsa_next_free_sgpr 82
		.amdhsa_accum_offset 256
		.amdhsa_reserve_vcc 1
		.amdhsa_float_round_mode_32 0
		.amdhsa_float_round_mode_16_64 0
		.amdhsa_float_denorm_mode_32 3
		.amdhsa_float_denorm_mode_16_64 3
		.amdhsa_dx10_clamp 1
		.amdhsa_ieee_mode 1
		.amdhsa_fp16_overflow 0
		.amdhsa_tg_split 0
		.amdhsa_exception_fp_ieee_invalid_op 0
		.amdhsa_exception_fp_denorm_src 0
		.amdhsa_exception_fp_ieee_div_zero 0
		.amdhsa_exception_fp_ieee_overflow 0
		.amdhsa_exception_fp_ieee_underflow 0
		.amdhsa_exception_fp_ieee_inexact 0
		.amdhsa_exception_int_div_zero 0
	.end_amdhsa_kernel

.LBB10_27:
	ds_read_b128 v[72:75], v231
	ds_read_b128 v[80:83], v231 offset:1024
	ds_read_b128 v[88:91], v231 offset:2048
	ds_read_b128 v[92:95], v231 offset:3072
	s_add_u32 s40, s38, 0xfff40080
	s_addc_u32 s41, s39, -1
	s_cmp_eq_u32 s87, 44
	s_cselect_b32 s43, s9, s41
	s_cselect_b32 s42, s8, s40
	s_cselect_b32 s41, s1, s86
	s_cselect_b32 s40, s0, s85
	s_add_i32 m0, s51, 0xc000
	ds_read_b128 v[136:139], v232
	ds_read_b128 v[148:151], v232 offset:1024
	ds_read_b128 v[152:155], v232 offset:2048
	ds_read_b128 v[156:159], v232 offset:3072
	ds_read_b128 v[160:163], v232 offset:4096
	ds_read_b128 v[164:167], v232 offset:5120
	ds_read_b128 v[168:171], v232 offset:6144
	ds_read_b128 v[172:175], v232 offset:7168
	global_load_lds_dwordx4 v184, s[38:39]
	s_add_i32 m0, s51, 0xe000
	s_nop 0
	global_load_lds_dwordx4 v186, s[38:39]
	s_waitcnt lgkmcnt(8)
	s_barrier
	s_waitcnt lgkmcnt(0)
	s_waitcnt lgkmcnt(0)
	v_mfma_f32_16x16x32_f16 v[144:147], v[72:75], v[136:139], v[144:147]
	v_mfma_f32_16x16x32_f16 v[140:143], v[88:91], v[136:139], v[140:143]
	v_mfma_f32_16x16x32_f16 v[124:127], v[72:75], v[152:155], v[124:127]
	v_mfma_f32_16x16x32_f16 v[120:123], v[88:91], v[152:155], v[120:123]
	v_mfma_f32_16x16x32_f16 v[108:111], v[72:75], v[160:163], v[108:111]
	v_mfma_f32_16x16x32_f16 v[104:107], v[88:91], v[160:163], v[104:107]
	v_mfma_f32_16x16x32_f16 v[84:87], v[72:75], v[168:171], v[84:87]
	v_mfma_f32_16x16x32_f16 v[76:79], v[88:91], v[168:171], v[76:79]
	v_mfma_f32_16x16x32_f16 v[144:147], v[80:83], v[148:151], v[144:147]
	v_mfma_f32_16x16x32_f16 v[140:143], v[92:95], v[148:151], v[140:143]
	v_mfma_f32_16x16x32_f16 v[124:127], v[80:83], v[156:159], v[124:127]
	v_mfma_f32_16x16x32_f16 v[120:123], v[92:95], v[156:159], v[120:123]
	v_mfma_f32_16x16x32_f16 v[108:111], v[80:83], v[164:167], v[108:111]
	v_mfma_f32_16x16x32_f16 v[104:107], v[92:95], v[164:167], v[104:107]
	v_mfma_f32_16x16x32_f16 v[84:87], v[80:83], v[172:175], v[84:87]
	v_mfma_f32_16x16x32_f16 v[76:79], v[92:95], v[172:175], v[76:79]
	s_barrier
	s_add_i32 s88, s69, s50
	s_add_u32 s92, s40, 0x80
	s_addc_u32 s93, s41, 0
	s_mov_b32 m0, s88
	ds_read_b128 v[190:193], v233
	ds_read_b128 v[194:197], v233 offset:1024
	ds_read_b128 v[198:201], v233 offset:2048
	ds_read_b128 v[202:205], v233 offset:3072
	global_load_lds_dwordx4 v178, s[40:41]
	s_add_i32 m0, s88, 0x2000
	s_nop 0
	global_load_lds_dwordx4 v182, s[40:41]
	s_barrier
	s_waitcnt lgkmcnt(0)
	s_waitcnt lgkmcnt(0)
	v_mfma_f32_16x16x32_f16 v[132:135], v[190:193], v[136:139], v[132:135]
	v_mfma_f32_16x16x32_f16 v[128:131], v[198:201], v[136:139], v[128:131]
	v_mfma_f32_16x16x32_f16 v[116:119], v[190:193], v[152:155], v[116:119]
	v_mfma_f32_16x16x32_f16 v[112:115], v[198:201], v[152:155], v[112:115]
	v_mfma_f32_16x16x32_f16 v[100:103], v[190:193], v[160:163], v[100:103]
	v_mfma_f32_16x16x32_f16 v[96:99], v[198:201], v[160:163], v[96:99]
	v_mfma_f32_16x16x32_f16 v[68:71], v[190:193], v[168:171], v[68:71]
	v_mfma_f32_16x16x32_f16 v[64:67], v[198:201], v[168:171], v[64:67]
	v_mfma_f32_16x16x32_f16 v[132:135], v[194:197], v[148:151], v[132:135]
	v_mfma_f32_16x16x32_f16 v[128:131], v[202:205], v[148:151], v[128:131]
	v_mfma_f32_16x16x32_f16 v[116:119], v[194:197], v[156:159], v[116:119]
	v_mfma_f32_16x16x32_f16 v[112:115], v[202:205], v[156:159], v[112:115]
	v_mfma_f32_16x16x32_f16 v[100:103], v[194:197], v[164:167], v[100:103]
	v_mfma_f32_16x16x32_f16 v[96:99], v[202:205], v[164:167], v[96:99]
	v_mfma_f32_16x16x32_f16 v[68:71], v[194:197], v[172:175], v[68:71]
	v_mfma_f32_16x16x32_f16 v[64:67], v[202:205], v[172:175], v[64:67]
	s_mov_b32 m0, s51
	s_add_u32 s94, s42, 0x80
	s_addc_u32 s95, s43, 0
	s_barrier
	ds_read_b128 v[136:139], v232 offset:16384
	ds_read_b128 v[148:151], v232 offset:17408
	ds_read_b128 v[152:155], v232 offset:18432
	ds_read_b128 v[156:159], v232 offset:19456
	ds_read_b128 v[160:163], v232 offset:20480
	ds_read_b128 v[164:167], v232 offset:21504
	ds_read_b128 v[168:171], v232 offset:22528
	ds_read_b128 v[172:175], v232 offset:23552
	global_load_lds_dwordx4 v176, s[42:43]
	s_mov_b32 m0, s52
	s_nop 0
	global_load_lds_dwordx4 v180, s[42:43]
	s_barrier
	s_waitcnt lgkmcnt(0)
	s_waitcnt lgkmcnt(0)
	v_mfma_f32_16x16x32_f16 v[60:63], v[72:75], v[136:139], v[60:63]
	v_mfma_f32_16x16x32_f16 v[56:59], v[88:91], v[136:139], v[56:59]
	v_mfma_f32_16x16x32_f16 v[44:47], v[72:75], v[152:155], v[44:47]
	v_mfma_f32_16x16x32_f16 v[40:43], v[88:91], v[152:155], v[40:43]
	v_mfma_f32_16x16x32_f16 v[28:31], v[72:75], v[160:163], v[28:31]
	v_mfma_f32_16x16x32_f16 v[24:27], v[88:91], v[160:163], v[24:27]
	v_mfma_f32_16x16x32_f16 v[12:15], v[72:75], v[168:171], v[12:15]
	v_mfma_f32_16x16x32_f16 v[8:11], v[88:91], v[168:171], v[8:11]
	v_mfma_f32_16x16x32_f16 v[60:63], v[80:83], v[148:151], v[60:63]
	v_mfma_f32_16x16x32_f16 v[56:59], v[92:95], v[148:151], v[56:59]
	v_mfma_f32_16x16x32_f16 v[44:47], v[80:83], v[156:159], v[44:47]
	v_mfma_f32_16x16x32_f16 v[40:43], v[92:95], v[156:159], v[40:43]
	v_mfma_f32_16x16x32_f16 v[28:31], v[80:83], v[164:167], v[28:31]
	v_mfma_f32_16x16x32_f16 v[24:27], v[92:95], v[164:167], v[24:27]
	v_mfma_f32_16x16x32_f16 v[12:15], v[80:83], v[172:175], v[12:15]
	v_mfma_f32_16x16x32_f16 v[8:11], v[92:95], v[172:175], v[8:11]
	s_barrier
	s_add_u32 s88, s40, 0x30000
	s_addc_u32 s89, s41, 0
	s_add_i32 s90, s70, s50
	s_mov_b32 m0, s90
	s_nop 0
	global_load_lds_dwordx4 v178, s[88:89]
	s_add_i32 m0, s90, 0x2000
	s_nop 0
	global_load_lds_dwordx4 v182, s[88:89]
	s_waitcnt vmcnt(6)
	s_barrier
	v_mfma_f32_16x16x32_f16 v[52:55], v[190:193], v[136:139], v[52:55]
	v_mfma_f32_16x16x32_f16 v[48:51], v[198:201], v[136:139], v[48:51]
	v_mfma_f32_16x16x32_f16 v[36:39], v[190:193], v[152:155], v[36:39]
	v_mfma_f32_16x16x32_f16 v[32:35], v[198:201], v[152:155], v[32:35]
	v_mfma_f32_16x16x32_f16 v[20:23], v[190:193], v[160:163], v[20:23]
	v_mfma_f32_16x16x32_f16 v[16:19], v[198:201], v[160:163], v[16:19]
	v_mfma_f32_16x16x32_f16 v[4:7], v[190:193], v[168:171], v[4:7]
	v_mfma_f32_16x16x32_f16 v[0:3], v[198:201], v[168:171], v[0:3]
	v_mfma_f32_16x16x32_f16 v[52:55], v[194:197], v[148:151], v[52:55]
	v_mfma_f32_16x16x32_f16 v[48:51], v[202:205], v[148:151], v[48:51]
	v_mfma_f32_16x16x32_f16 v[36:39], v[194:197], v[156:159], v[36:39]
	v_mfma_f32_16x16x32_f16 v[32:35], v[202:205], v[156:159], v[32:35]
	v_mfma_f32_16x16x32_f16 v[20:23], v[194:197], v[164:167], v[20:23]
	v_mfma_f32_16x16x32_f16 v[16:19], v[202:205], v[164:167], v[16:19]
	v_mfma_f32_16x16x32_f16 v[4:7], v[194:197], v[172:175], v[4:7]
	v_mfma_f32_16x16x32_f16 v[0:3], v[202:205], v[172:175], v[0:3]
	s_add_i32 s88, 0, 0x18000
	v_add_u32_e32 v92, s88, v228
	s_barrier
	ds_read_b128 v[72:75], v92
	ds_read_b128 v[80:83], v92 offset:1024
	ds_read_b128 v[88:91], v92 offset:2048
	ds_read_b128 v[92:95], v92 offset:3072
	s_add_u32 s42, s42, 0xc0000
	s_addc_u32 s43, s43, 0
	s_mov_b32 m0, s53
	ds_read_b128 v[136:139], v232 offset:32768
	ds_read_b128 v[148:151], v232 offset:33792
	ds_read_b128 v[152:155], v232 offset:34816
	ds_read_b128 v[156:159], v232 offset:35840
	ds_read_b128 v[160:163], v232 offset:36864
	ds_read_b128 v[164:167], v232 offset:37888
	ds_read_b128 v[168:171], v232 offset:38912
	ds_read_b128 v[172:175], v232 offset:39936
	global_load_lds_dwordx4 v176, s[42:43]
	s_mov_b32 m0, s54
	s_nop 0
	global_load_lds_dwordx4 v180, s[42:43]
	s_waitcnt lgkmcnt(8)
	s_barrier
	s_waitcnt lgkmcnt(0)
	s_waitcnt lgkmcnt(0)
	v_mfma_f32_16x16x32_f16 v[144:147], v[72:75], v[136:139], v[144:147]
	v_mfma_f32_16x16x32_f16 v[140:143], v[88:91], v[136:139], v[140:143]
	v_mfma_f32_16x16x32_f16 v[124:127], v[72:75], v[152:155], v[124:127]
	v_mfma_f32_16x16x32_f16 v[120:123], v[88:91], v[152:155], v[120:123]
	v_mfma_f32_16x16x32_f16 v[108:111], v[72:75], v[160:163], v[108:111]
	v_mfma_f32_16x16x32_f16 v[104:107], v[88:91], v[160:163], v[104:107]
	v_mfma_f32_16x16x32_f16 v[84:87], v[72:75], v[168:171], v[84:87]
	v_mfma_f32_16x16x32_f16 v[76:79], v[88:91], v[168:171], v[76:79]
	v_mfma_f32_16x16x32_f16 v[144:147], v[80:83], v[148:151], v[144:147]
	v_mfma_f32_16x16x32_f16 v[140:143], v[92:95], v[148:151], v[140:143]
	v_mfma_f32_16x16x32_f16 v[124:127], v[80:83], v[156:159], v[124:127]
	v_mfma_f32_16x16x32_f16 v[120:123], v[92:95], v[156:159], v[120:123]
	v_mfma_f32_16x16x32_f16 v[108:111], v[80:83], v[164:167], v[108:111]
	v_mfma_f32_16x16x32_f16 v[104:107], v[92:95], v[164:167], v[104:107]
	v_mfma_f32_16x16x32_f16 v[84:87], v[80:83], v[172:175], v[84:87]
	v_mfma_f32_16x16x32_f16 v[76:79], v[92:95], v[172:175], v[76:79]
	s_barrier
	s_add_i32 s42, 0, 0x1c000
	s_add_i32 s43, s88, s50
	v_add_u32_e32 v202, s42, v228
	s_mov_b32 m0, s43
	ds_read_b128 v[190:193], v202
	ds_read_b128 v[194:197], v202 offset:1024
	ds_read_b128 v[198:201], v202 offset:2048
	ds_read_b128 v[202:205], v202 offset:3072
	global_load_lds_dwordx4 v178, s[92:93]
	s_add_i32 m0, s43, 0x2000
	s_nop 0
	global_load_lds_dwordx4 v182, s[92:93]
	s_barrier
	s_waitcnt lgkmcnt(0)
	s_waitcnt lgkmcnt(0)
	v_mfma_f32_16x16x32_f16 v[132:135], v[190:193], v[136:139], v[132:135]
	v_mfma_f32_16x16x32_f16 v[128:131], v[198:201], v[136:139], v[128:131]
	v_mfma_f32_16x16x32_f16 v[116:119], v[190:193], v[152:155], v[116:119]
	v_mfma_f32_16x16x32_f16 v[112:115], v[198:201], v[152:155], v[112:115]
	v_mfma_f32_16x16x32_f16 v[100:103], v[190:193], v[160:163], v[100:103]
	v_mfma_f32_16x16x32_f16 v[96:99], v[198:201], v[160:163], v[96:99]
	v_mfma_f32_16x16x32_f16 v[68:71], v[190:193], v[168:171], v[68:71]
	v_mfma_f32_16x16x32_f16 v[64:67], v[198:201], v[168:171], v[64:67]
	v_mfma_f32_16x16x32_f16 v[132:135], v[194:197], v[148:151], v[132:135]
	v_mfma_f32_16x16x32_f16 v[128:131], v[202:205], v[148:151], v[128:131]
	v_mfma_f32_16x16x32_f16 v[116:119], v[194:197], v[156:159], v[116:119]
	v_mfma_f32_16x16x32_f16 v[112:115], v[202:205], v[156:159], v[112:115]
	v_mfma_f32_16x16x32_f16 v[100:103], v[194:197], v[164:167], v[100:103]
	v_mfma_f32_16x16x32_f16 v[96:99], v[202:205], v[164:167], v[96:99]
	v_mfma_f32_16x16x32_f16 v[68:71], v[194:197], v[172:175], v[68:71]
	v_mfma_f32_16x16x32_f16 v[64:67], v[202:205], v[172:175], v[64:67]
	s_mov_b32 m0, s58
	s_barrier
	ds_read_b128 v[136:139], v232 offset:49152
	ds_read_b128 v[148:151], v232 offset:50176
	ds_read_b128 v[152:155], v232 offset:51200
	ds_read_b128 v[156:159], v232 offset:52224
	ds_read_b128 v[160:163], v232 offset:53248
	ds_read_b128 v[164:167], v232 offset:54272
	ds_read_b128 v[168:171], v232 offset:55296
	ds_read_b128 v[172:175], v232 offset:56320
	global_load_lds_dwordx4 v176, s[94:95]
	s_mov_b32 m0, s59
	s_nop 0
	global_load_lds_dwordx4 v180, s[94:95]
	s_barrier
	s_waitcnt lgkmcnt(0)
	s_waitcnt lgkmcnt(0)
	v_mfma_f32_16x16x32_f16 v[60:63], v[72:75], v[136:139], v[60:63]
	v_mfma_f32_16x16x32_f16 v[56:59], v[88:91], v[136:139], v[56:59]
	v_mfma_f32_16x16x32_f16 v[44:47], v[72:75], v[152:155], v[44:47]
	v_mfma_f32_16x16x32_f16 v[40:43], v[88:91], v[152:155], v[40:43]
	v_mfma_f32_16x16x32_f16 v[28:31], v[72:75], v[160:163], v[28:31]
	v_mfma_f32_16x16x32_f16 v[24:27], v[88:91], v[160:163], v[24:27]
	v_mfma_f32_16x16x32_f16 v[12:15], v[72:75], v[168:171], v[12:15]
	v_mfma_f32_16x16x32_f16 v[8:11], v[88:91], v[168:171], v[8:11]
	v_mfma_f32_16x16x32_f16 v[60:63], v[80:83], v[148:151], v[60:63]
	v_mfma_f32_16x16x32_f16 v[56:59], v[92:95], v[148:151], v[56:59]
	v_mfma_f32_16x16x32_f16 v[44:47], v[80:83], v[156:159], v[44:47]
	v_mfma_f32_16x16x32_f16 v[40:43], v[92:95], v[156:159], v[40:43]
	v_mfma_f32_16x16x32_f16 v[28:31], v[80:83], v[164:167], v[28:31]
	v_mfma_f32_16x16x32_f16 v[24:27], v[92:95], v[164:167], v[24:27]
	v_mfma_f32_16x16x32_f16 v[12:15], v[80:83], v[172:175], v[12:15]
	v_mfma_f32_16x16x32_f16 v[8:11], v[92:95], v[172:175], v[8:11]
	s_barrier
	s_add_u32 s40, s40, 0x30080
	s_addc_u32 s41, s41, 0
	s_add_i32 s42, s42, s50
	s_mov_b32 m0, s42
	s_nop 0
	global_load_lds_dwordx4 v178, s[40:41]
	s_add_i32 m0, s42, 0x2000
	s_nop 0
	global_load_lds_dwordx4 v182, s[40:41]
	s_waitcnt vmcnt(6)
	s_barrier
	v_mfma_f32_16x16x32_f16 v[52:55], v[190:193], v[136:139], v[52:55]
	v_mfma_f32_16x16x32_f16 v[48:51], v[198:201], v[136:139], v[48:51]
	v_mfma_f32_16x16x32_f16 v[36:39], v[190:193], v[152:155], v[36:39]
	v_mfma_f32_16x16x32_f16 v[32:35], v[198:201], v[152:155], v[32:35]
	v_mfma_f32_16x16x32_f16 v[20:23], v[190:193], v[160:163], v[20:23]
	v_mfma_f32_16x16x32_f16 v[16:19], v[198:201], v[160:163], v[16:19]
	v_mfma_f32_16x16x32_f16 v[4:7], v[190:193], v[168:171], v[4:7]
	v_mfma_f32_16x16x32_f16 v[0:3], v[198:201], v[168:171], v[0:3]
	v_mfma_f32_16x16x32_f16 v[52:55], v[194:197], v[148:151], v[52:55]
	v_mfma_f32_16x16x32_f16 v[48:51], v[202:205], v[148:151], v[48:51]
	v_mfma_f32_16x16x32_f16 v[36:39], v[194:197], v[156:159], v[36:39]
	v_mfma_f32_16x16x32_f16 v[32:35], v[202:205], v[156:159], v[32:35]
	v_mfma_f32_16x16x32_f16 v[20:23], v[194:197], v[164:167], v[20:23]
	v_mfma_f32_16x16x32_f16 v[16:19], v[202:205], v[164:167], v[16:19]
	v_mfma_f32_16x16x32_f16 v[4:7], v[194:197], v[172:175], v[4:7]
	v_mfma_f32_16x16x32_f16 v[0:3], v[202:205], v[172:175], v[0:3]
	s_add_i32 s87, s87, 2
	s_add_u32 s38, s38, 0x100
	s_addc_u32 s39, s39, 0
	s_add_u32 s85, s85, 0x100
	s_addc_u32 s86, s86, 0
	s_cmp_gt_u32 s87, 45
	s_barrier
	s_cbranch_scc0 .LBB10_27
	s_lshl_b32 s92, s84, 8
	s_add_i32 s92, s92, s57
	s_lshl_b32 s93, s83, 8
	s_or_b32 s93, s93, s60
	v_lshlrev_b32_e32 v237, 2, v226
	s_lshl_b32 s96, s93, 2
	s_add_u32 s94, s16, s96
	s_addc_u32 s95, s17, 0
	global_load_dwordx4 v[72:75], v237, s[94:95] offset:0
	global_load_dwordx4 v[80:83], v237, s[94:95] offset:16
	global_load_dwordx4 v[88:91], v237, s[94:95] offset:128
	global_load_dwordx4 v[92:95], v237, s[94:95] offset:144
	s_add_u32 s94, s18, s96
	s_addc_u32 s95, s19, 0
	global_load_dwordx4 v[136:139], v237, s[94:95] offset:0
	global_load_dwordx4 v[148:151], v237, s[94:95] offset:16
	global_load_dwordx4 v[152:155], v237, s[94:95] offset:128
	global_load_dwordx4 v[156:159], v237, s[94:95] offset:144
	s_add_u32 s94, s14, s96
	s_addc_u32 s95, s15, 0
	global_load_dwordx4 v[160:163], v237, s[94:95] offset:0
	global_load_dwordx4 v[164:167], v237, s[94:95] offset:16
	global_load_dwordx4 v[168:171], v237, s[94:95] offset:128
	global_load_dwordx4 v[172:175], v237, s[94:95] offset:144
	v_lshlrev_b32_e32 v190, 3, v227
	s_lshl_b32 s96, s92, 3
	s_add_u32 s94, s12, s96
	s_addc_u32 s95, s13, 0
	global_load_dwordx2 v[238:239], v190, s[94:95] offset:0
	global_load_dwordx2 v[192:193], v190, s[94:95] offset:128
	global_load_dwordx2 v[194:195], v190, s[94:95] offset:256
	global_load_dwordx2 v[196:197], v190, s[94:95] offset:384
	global_load_dwordx2 v[198:199], v190, s[94:95] offset:1024
	global_load_dwordx2 v[200:201], v190, s[94:95] offset:1152
	global_load_dwordx2 v[202:203], v190, s[94:95] offset:1280
	global_load_dwordx2 v[204:205], v190, s[94:95] offset:1408
	v_mul_u32_u24_e32 v191, 0x600, v227
	v_lshl_add_u32 v191, v226, 1, v191
	s_mul_i32 s96, s92, 0x600
	s_lshl_b32 s97, s93, 1
	s_add_u32 s96, s96, s97
	s_add_u32 s98, s10, s96
	s_addc_u32 s99, s11, 0
	s_add_u32 s94, s98, 0x0
	s_addc_u32 s95, s99, 0
	global_load_dwordx4 v[208:211], v191, s[94:95] offset:0 nt
	global_load_dwordx4 v[212:215], v191, s[94:95] offset:64 nt
	s_add_u32 s94, s98, 0x6000
	s_addc_u32 s95, s99, 0
	global_load_dwordx4 v[216:219], v191, s[94:95] offset:0 nt
	global_load_dwordx4 v[220:223], v191, s[94:95] offset:64 nt
	v_add_u32_e32 v224, s92, v229
	v_mul_u32_u24_e32 v224, 0x600, v224
	s_lshl_b32 s97, s93, 1
	v_add3_u32 v224, v224, v230, s97
	s_lshl_b32 s96, s83, 2
	s_lshr_b32 s97, s60, 6
	s_add_u32 s96, s96, s97
	s_lshl_b32 s96, s96, 19
	s_lshl_b32 s97, s92, 3
	s_add_u32 s96, s96, s97
	s_add_u32 s100, s28, s96
	s_addc_u32 s101, s29, 0
	s_waitcnt vmcnt(19)
	v_pk_add_f32 v[72:73], v[72:73], v[136:137]
	v_pk_add_f32 v[74:75], v[74:75], v[138:139]
	s_waitcnt vmcnt(18)
	v_pk_add_f32 v[80:81], v[80:81], v[148:149]
	v_pk_add_f32 v[82:83], v[82:83], v[150:151]
	s_waitcnt vmcnt(17)
	v_pk_add_f32 v[88:89], v[88:89], v[152:153]
	v_pk_add_f32 v[90:91], v[90:91], v[154:155]
	s_waitcnt vmcnt(16)
	v_pk_add_f32 v[92:93], v[92:93], v[156:157]
	v_pk_add_f32 v[94:95], v[94:95], v[158:159]
	v_pk_add_f32 v[144:145], v[144:145], v[72:73]
	v_pk_add_f32 v[146:147], v[146:147], v[74:75]
	v_pk_add_f32 v[124:125], v[124:125], v[72:73]
	v_pk_add_f32 v[126:127], v[126:127], v[74:75]
	v_pk_add_f32 v[108:109], v[108:109], v[72:73]
	v_pk_add_f32 v[110:111], v[110:111], v[74:75]
	v_pk_add_f32 v[84:85], v[84:85], v[72:73]
	v_pk_add_f32 v[86:87], v[86:87], v[74:75]
	v_pk_add_f32 v[60:61], v[60:61], v[72:73]
	v_pk_add_f32 v[62:63], v[62:63], v[74:75]
	v_pk_add_f32 v[44:45], v[44:45], v[72:73]
	v_pk_add_f32 v[46:47], v[46:47], v[74:75]
	v_pk_add_f32 v[28:29], v[28:29], v[72:73]
	v_pk_add_f32 v[30:31], v[30:31], v[74:75]
	v_pk_add_f32 v[12:13], v[12:13], v[72:73]
	v_pk_add_f32 v[14:15], v[14:15], v[74:75]
	v_pk_add_f32 v[140:141], v[140:141], v[80:81]
	v_pk_add_f32 v[142:143], v[142:143], v[82:83]
	v_pk_add_f32 v[120:121], v[120:121], v[80:81]
	v_pk_add_f32 v[122:123], v[122:123], v[82:83]
	v_pk_add_f32 v[104:105], v[104:105], v[80:81]
	v_pk_add_f32 v[106:107], v[106:107], v[82:83]
	v_pk_add_f32 v[76:77], v[76:77], v[80:81]
	v_pk_add_f32 v[78:79], v[78:79], v[82:83]
	v_pk_add_f32 v[56:57], v[56:57], v[80:81]
	v_pk_add_f32 v[58:59], v[58:59], v[82:83]
	v_pk_add_f32 v[40:41], v[40:41], v[80:81]
	v_pk_add_f32 v[42:43], v[42:43], v[82:83]
	v_pk_add_f32 v[24:25], v[24:25], v[80:81]
	v_pk_add_f32 v[26:27], v[26:27], v[82:83]
	v_pk_add_f32 v[8:9], v[8:9], v[80:81]
	v_pk_add_f32 v[10:11], v[10:11], v[82:83]
	v_pk_add_f32 v[132:133], v[132:133], v[88:89]
	v_pk_add_f32 v[134:135], v[134:135], v[90:91]
	v_pk_add_f32 v[116:117], v[116:117], v[88:89]
	v_pk_add_f32 v[118:119], v[118:119], v[90:91]
	v_pk_add_f32 v[100:101], v[100:101], v[88:89]
	v_pk_add_f32 v[102:103], v[102:103], v[90:91]
	v_pk_add_f32 v[68:69], v[68:69], v[88:89]
	v_pk_add_f32 v[70:71], v[70:71], v[90:91]
	v_pk_add_f32 v[52:53], v[52:53], v[88:89]
	v_pk_add_f32 v[54:55], v[54:55], v[90:91]
	v_pk_add_f32 v[36:37], v[36:37], v[88:89]
	v_pk_add_f32 v[38:39], v[38:39], v[90:91]
	v_pk_add_f32 v[20:21], v[20:21], v[88:89]
	v_pk_add_f32 v[22:23], v[22:23], v[90:91]
	v_pk_add_f32 v[4:5], v[4:5], v[88:89]
	v_pk_add_f32 v[6:7], v[6:7], v[90:91]
	v_pk_add_f32 v[128:129], v[128:129], v[92:93]
	v_pk_add_f32 v[130:131], v[130:131], v[94:95]
	v_pk_add_f32 v[112:113], v[112:113], v[92:93]
	v_pk_add_f32 v[114:115], v[114:115], v[94:95]
	v_pk_add_f32 v[96:97], v[96:97], v[92:93]
	v_pk_add_f32 v[98:99], v[98:99], v[94:95]
	v_pk_add_f32 v[64:65], v[64:65], v[92:93]
	v_pk_add_f32 v[66:67], v[66:67], v[94:95]
	v_pk_add_f32 v[48:49], v[48:49], v[92:93]
	v_pk_add_f32 v[50:51], v[50:51], v[94:95]
	v_pk_add_f32 v[32:33], v[32:33], v[92:93]
	v_pk_add_f32 v[34:35], v[34:35], v[94:95]
	v_pk_add_f32 v[16:17], v[16:17], v[92:93]
	v_pk_add_f32 v[18:19], v[18:19], v[94:95]
	v_pk_add_f32 v[0:1], v[0:1], v[92:93]
	v_pk_add_f32 v[2:3], v[2:3], v[94:95]
	s_add_u32 s94, s98, 0xc000
	s_addc_u32 s95, s99, 0
	global_load_dwordx4 v[240:243], v191, s[94:95] offset:0 nt
	global_load_dwordx4 v[244:247], v191, s[94:95] offset:64 nt
	s_add_u32 s94, s98, 0x12000
	s_addc_u32 s95, s99, 0
	global_load_dwordx4 v[248:251], v191, s[94:95] offset:0 nt
	global_load_dwordx4 v[252:255], v191, s[94:95] offset:64 nt
	s_add_u32 s94, s98, 0x30000
	s_addc_u32 s95, s99, 0
	global_load_dwordx4 v[136:139], v191, s[94:95] offset:0 nt
	global_load_dwordx4 v[148:151], v191, s[94:95] offset:64 nt
	s_add_u32 s94, s98, 0x36000
	s_addc_u32 s95, s99, 0
	global_load_dwordx4 v[152:155], v191, s[94:95] offset:0 nt
	global_load_dwordx4 v[156:159], v191, s[94:95] offset:64 nt
	s_waitcnt vmcnt(19)
	s_waitcnt vmcnt(11)
	v_cvt_f32_f16_e32 v72, v208
	v_cvt_f32_f16_sdwa v73, v208 dst_sel:DWORD dst_unused:UNUSED_PAD src0_sel:WORD_1
	v_cvt_f32_f16_e32 v74, v209
	v_cvt_f32_f16_sdwa v75, v209 dst_sel:DWORD dst_unused:UNUSED_PAD src0_sel:WORD_1
	v_cvt_f32_f16_e32 v80, v210
	v_cvt_f32_f16_sdwa v81, v210 dst_sel:DWORD dst_unused:UNUSED_PAD src0_sel:WORD_1
	v_cvt_f32_f16_e32 v82, v211
	v_cvt_f32_f16_sdwa v83, v211 dst_sel:DWORD dst_unused:UNUSED_PAD src0_sel:WORD_1
	v_sub_f32_e32 v72, v72, v238
	v_sub_f32_e32 v73, v73, v238
	v_sub_f32_e32 v74, v74, v238
	v_sub_f32_e32 v75, v75, v238
	v_sub_f32_e32 v80, v80, v238
	v_sub_f32_e32 v81, v81, v238
	v_sub_f32_e32 v82, v82, v238
	v_sub_f32_e32 v83, v83, v238
	v_pk_mul_f32 v[72:73], v[238:239], v[72:73] op_sel:[1,0]
	v_pk_mul_f32 v[74:75], v[238:239], v[74:75] op_sel:[1,0]
	v_pk_mul_f32 v[80:81], v[238:239], v[80:81] op_sel:[1,0]
	v_pk_mul_f32 v[82:83], v[238:239], v[82:83] op_sel:[1,0]
	v_pk_fma_f32 v[144:145], v[72:73], v[160:161], v[144:145]
	v_pk_fma_f32 v[146:147], v[74:75], v[162:163], v[146:147]
	v_pk_fma_f32 v[140:141], v[80:81], v[164:165], v[140:141]
	v_pk_fma_f32 v[142:143], v[82:83], v[166:167], v[142:143]
	v_cvt_pk_f16_f32 v144, v144, v145
	v_cvt_pk_f16_f32 v145, v146, v147
	v_cvt_pk_f16_f32 v146, v140, v141
	v_cvt_pk_f16_f32 v147, v142, v143
	ds_write_b128 v235, v[144:147]
	v_fma_mix_f32 v206, v144, 1.0, 0 op_sel_hi:[1,0,0]
	v_fma_mix_f32 v207, v144, v144, 0 op_sel_hi:[1,1,0]
	v_fma_mix_f32 v206, v144, 1.0, v206 op_sel:[1,0,0] op_sel_hi:[1,0,0]
	v_fma_mix_f32 v207, v144, v144, v207 op_sel:[1,1,0] op_sel_hi:[1,1,0]
	v_fma_mix_f32 v206, v145, 1.0, v206 op_sel_hi:[1,0,0]
	v_fma_mix_f32 v207, v145, v145, v207 op_sel_hi:[1,1,0]
	v_fma_mix_f32 v206, v145, 1.0, v206 op_sel:[1,0,0] op_sel_hi:[1,0,0]
	v_fma_mix_f32 v207, v145, v145, v207 op_sel:[1,1,0] op_sel_hi:[1,1,0]
	v_fma_mix_f32 v206, v146, 1.0, v206 op_sel_hi:[1,0,0]
	v_fma_mix_f32 v207, v146, v146, v207 op_sel_hi:[1,1,0]
	v_fma_mix_f32 v206, v146, 1.0, v206 op_sel:[1,0,0] op_sel_hi:[1,0,0]
	v_fma_mix_f32 v207, v146, v146, v207 op_sel:[1,1,0] op_sel_hi:[1,1,0]
	v_fma_mix_f32 v206, v147, 1.0, v206 op_sel_hi:[1,0,0]
	v_fma_mix_f32 v207, v147, v147, v207 op_sel_hi:[1,1,0]
	v_fma_mix_f32 v206, v147, 1.0, v206 op_sel:[1,0,0] op_sel_hi:[1,0,0]
	v_fma_mix_f32 v207, v147, v147, v207 op_sel:[1,1,0] op_sel_hi:[1,1,0]
	s_waitcnt vmcnt(10)
	v_cvt_f32_f16_e32 v72, v212
	v_cvt_f32_f16_sdwa v73, v212 dst_sel:DWORD dst_unused:UNUSED_PAD src0_sel:WORD_1
	v_cvt_f32_f16_e32 v74, v213
	v_cvt_f32_f16_sdwa v75, v213 dst_sel:DWORD dst_unused:UNUSED_PAD src0_sel:WORD_1
	v_cvt_f32_f16_e32 v80, v214
	v_cvt_f32_f16_sdwa v81, v214 dst_sel:DWORD dst_unused:UNUSED_PAD src0_sel:WORD_1
	v_cvt_f32_f16_e32 v82, v215
	v_cvt_f32_f16_sdwa v83, v215 dst_sel:DWORD dst_unused:UNUSED_PAD src0_sel:WORD_1
	v_sub_f32_e32 v72, v72, v238
	v_sub_f32_e32 v73, v73, v238
	v_sub_f32_e32 v74, v74, v238
	v_sub_f32_e32 v75, v75, v238
	v_sub_f32_e32 v80, v80, v238
	v_sub_f32_e32 v81, v81, v238
	v_sub_f32_e32 v82, v82, v238
	v_sub_f32_e32 v83, v83, v238
	v_pk_mul_f32 v[72:73], v[238:239], v[72:73] op_sel:[1,0]
	v_pk_mul_f32 v[74:75], v[238:239], v[74:75] op_sel:[1,0]
	v_pk_mul_f32 v[80:81], v[238:239], v[80:81] op_sel:[1,0]
	v_pk_mul_f32 v[82:83], v[238:239], v[82:83] op_sel:[1,0]
	v_pk_fma_f32 v[132:133], v[72:73], v[168:169], v[132:133]
	v_pk_fma_f32 v[134:135], v[74:75], v[170:171], v[134:135]
	v_pk_fma_f32 v[128:129], v[80:81], v[172:173], v[128:129]
	v_pk_fma_f32 v[130:131], v[82:83], v[174:175], v[130:131]
	v_cvt_pk_f16_f32 v132, v132, v133
	v_cvt_pk_f16_f32 v133, v134, v135
	v_cvt_pk_f16_f32 v134, v128, v129
	v_cvt_pk_f16_f32 v135, v130, v131
	ds_write_b128 v235, v[132:135] offset:64
	v_fma_mix_f32 v206, v132, 1.0, v206 op_sel_hi:[1,0,0]
	v_fma_mix_f32 v207, v132, v132, v207 op_sel_hi:[1,1,0]
	v_fma_mix_f32 v206, v132, 1.0, v206 op_sel:[1,0,0] op_sel_hi:[1,0,0]
	v_fma_mix_f32 v207, v132, v132, v207 op_sel:[1,1,0] op_sel_hi:[1,1,0]
	v_fma_mix_f32 v206, v133, 1.0, v206 op_sel_hi:[1,0,0]
	v_fma_mix_f32 v207, v133, v133, v207 op_sel_hi:[1,1,0]
	v_fma_mix_f32 v206, v133, 1.0, v206 op_sel:[1,0,0] op_sel_hi:[1,0,0]
	v_fma_mix_f32 v207, v133, v133, v207 op_sel:[1,1,0] op_sel_hi:[1,1,0]
	v_fma_mix_f32 v206, v134, 1.0, v206 op_sel_hi:[1,0,0]
	v_fma_mix_f32 v207, v134, v134, v207 op_sel_hi:[1,1,0]
	v_fma_mix_f32 v206, v134, 1.0, v206 op_sel:[1,0,0] op_sel_hi:[1,0,0]
	v_fma_mix_f32 v207, v134, v134, v207 op_sel:[1,1,0] op_sel_hi:[1,1,0]
	v_fma_mix_f32 v206, v135, 1.0, v206 op_sel_hi:[1,0,0]
	v_fma_mix_f32 v207, v135, v135, v207 op_sel_hi:[1,1,0]
	v_fma_mix_f32 v206, v135, 1.0, v206 op_sel:[1,0,0] op_sel_hi:[1,0,0]
	v_fma_mix_f32 v207, v135, v135, v207 op_sel:[1,1,0] op_sel_hi:[1,1,0]
	ds_read_b128 v[88:91], v236
	ds_read_b128 v[92:95], v236 offset:1152
	s_waitcnt vmcnt(9)
	v_cvt_f32_f16_e32 v72, v216
	v_cvt_f32_f16_sdwa v73, v216 dst_sel:DWORD dst_unused:UNUSED_PAD src0_sel:WORD_1
	v_cvt_f32_f16_e32 v74, v217
	v_cvt_f32_f16_sdwa v75, v217 dst_sel:DWORD dst_unused:UNUSED_PAD src0_sel:WORD_1
	v_cvt_f32_f16_e32 v80, v218
	v_cvt_f32_f16_sdwa v81, v218 dst_sel:DWORD dst_unused:UNUSED_PAD src0_sel:WORD_1
	v_cvt_f32_f16_e32 v82, v219
	v_cvt_f32_f16_sdwa v83, v219 dst_sel:DWORD dst_unused:UNUSED_PAD src0_sel:WORD_1
	v_sub_f32_e32 v72, v72, v192
	v_sub_f32_e32 v73, v73, v192
	v_sub_f32_e32 v74, v74, v192
	v_sub_f32_e32 v75, v75, v192
	v_sub_f32_e32 v80, v80, v192
	v_sub_f32_e32 v81, v81, v192
	v_sub_f32_e32 v82, v82, v192
	v_sub_f32_e32 v83, v83, v192
	v_pk_mul_f32 v[72:73], v[192:193], v[72:73] op_sel:[1,0]
	v_pk_mul_f32 v[74:75], v[192:193], v[74:75] op_sel:[1,0]
	v_pk_mul_f32 v[80:81], v[192:193], v[80:81] op_sel:[1,0]
	v_pk_mul_f32 v[82:83], v[192:193], v[82:83] op_sel:[1,0]
	v_pk_fma_f32 v[124:125], v[72:73], v[160:161], v[124:125]
	v_pk_fma_f32 v[126:127], v[74:75], v[162:163], v[126:127]
	v_pk_fma_f32 v[120:121], v[80:81], v[164:165], v[120:121]
	v_pk_fma_f32 v[122:123], v[82:83], v[166:167], v[122:123]
	v_cvt_pk_f16_f32 v124, v124, v125
	v_cvt_pk_f16_f32 v125, v126, v127
	v_cvt_pk_f16_f32 v126, v120, v121
	v_cvt_pk_f16_f32 v127, v122, v123
	s_waitcnt lgkmcnt(0)
	buffer_store_dwordx4 v[88:91], v224, s[24:27], 0 offen nt
	v_add_u32_e32 v82, 0x3000, v224
	buffer_store_dwordx4 v[92:95], v82, s[24:27], 0 offen nt
	ds_write_b128 v235, v[124:127]
	v_fma_mix_f32 v140, v124, 1.0, 0 op_sel_hi:[1,0,0]
	v_fma_mix_f32 v141, v124, v124, 0 op_sel_hi:[1,1,0]
	v_fma_mix_f32 v140, v124, 1.0, v140 op_sel:[1,0,0] op_sel_hi:[1,0,0]
	v_fma_mix_f32 v141, v124, v124, v141 op_sel:[1,1,0] op_sel_hi:[1,1,0]
	v_fma_mix_f32 v140, v125, 1.0, v140 op_sel_hi:[1,0,0]
	v_fma_mix_f32 v141, v125, v125, v141 op_sel_hi:[1,1,0]
	v_fma_mix_f32 v140, v125, 1.0, v140 op_sel:[1,0,0] op_sel_hi:[1,0,0]
	v_fma_mix_f32 v141, v125, v125, v141 op_sel:[1,1,0] op_sel_hi:[1,1,0]
	v_fma_mix_f32 v140, v126, 1.0, v140 op_sel_hi:[1,0,0]
	v_fma_mix_f32 v141, v126, v126, v141 op_sel_hi:[1,1,0]
	v_fma_mix_f32 v140, v126, 1.0, v140 op_sel:[1,0,0] op_sel_hi:[1,0,0]
	v_fma_mix_f32 v141, v126, v126, v141 op_sel:[1,1,0] op_sel_hi:[1,1,0]
	v_fma_mix_f32 v140, v127, 1.0, v140 op_sel_hi:[1,0,0]
	v_fma_mix_f32 v141, v127, v127, v141 op_sel_hi:[1,1,0]
	v_fma_mix_f32 v140, v127, 1.0, v140 op_sel:[1,0,0] op_sel_hi:[1,0,0]
	v_fma_mix_f32 v141, v127, v127, v141 op_sel:[1,1,0] op_sel_hi:[1,1,0]
	s_waitcnt vmcnt(10)
	v_cvt_f32_f16_e32 v72, v220
	v_cvt_f32_f16_sdwa v73, v220 dst_sel:DWORD dst_unused:UNUSED_PAD src0_sel:WORD_1
	v_cvt_f32_f16_e32 v74, v221
	v_cvt_f32_f16_sdwa v75, v221 dst_sel:DWORD dst_unused:UNUSED_PAD src0_sel:WORD_1
	v_cvt_f32_f16_e32 v80, v222
	v_cvt_f32_f16_sdwa v81, v222 dst_sel:DWORD dst_unused:UNUSED_PAD src0_sel:WORD_1
	v_cvt_f32_f16_e32 v82, v223
	v_cvt_f32_f16_sdwa v83, v223 dst_sel:DWORD dst_unused:UNUSED_PAD src0_sel:WORD_1
	v_sub_f32_e32 v72, v72, v192
	v_sub_f32_e32 v73, v73, v192
	v_sub_f32_e32 v74, v74, v192
	v_sub_f32_e32 v75, v75, v192
	v_sub_f32_e32 v80, v80, v192
	v_sub_f32_e32 v81, v81, v192
	v_sub_f32_e32 v82, v82, v192
	v_sub_f32_e32 v83, v83, v192
	v_pk_mul_f32 v[72:73], v[192:193], v[72:73] op_sel:[1,0]
	v_pk_mul_f32 v[74:75], v[192:193], v[74:75] op_sel:[1,0]
	v_pk_mul_f32 v[80:81], v[192:193], v[80:81] op_sel:[1,0]
	v_pk_mul_f32 v[82:83], v[192:193], v[82:83] op_sel:[1,0]
	v_pk_fma_f32 v[116:117], v[72:73], v[168:169], v[116:117]
	v_pk_fma_f32 v[118:119], v[74:75], v[170:171], v[118:119]
	v_pk_fma_f32 v[112:113], v[80:81], v[172:173], v[112:113]
	v_pk_fma_f32 v[114:115], v[82:83], v[174:175], v[114:115]
	v_cvt_pk_f16_f32 v116, v116, v117
	v_cvt_pk_f16_f32 v117, v118, v119
	v_cvt_pk_f16_f32 v118, v112, v113
	v_cvt_pk_f16_f32 v119, v114, v115
	ds_write_b128 v235, v[116:119] offset:64
	v_fma_mix_f32 v140, v116, 1.0, v140 op_sel_hi:[1,0,0]
	v_fma_mix_f32 v141, v116, v116, v141 op_sel_hi:[1,1,0]
	v_fma_mix_f32 v140, v116, 1.0, v140 op_sel:[1,0,0] op_sel_hi:[1,0,0]
	v_fma_mix_f32 v141, v116, v116, v141 op_sel:[1,1,0] op_sel_hi:[1,1,0]
	v_fma_mix_f32 v140, v117, 1.0, v140 op_sel_hi:[1,0,0]
	v_fma_mix_f32 v141, v117, v117, v141 op_sel_hi:[1,1,0]
	v_fma_mix_f32 v140, v117, 1.0, v140 op_sel:[1,0,0] op_sel_hi:[1,0,0]
	v_fma_mix_f32 v141, v117, v117, v141 op_sel:[1,1,0] op_sel_hi:[1,1,0]
	v_fma_mix_f32 v140, v118, 1.0, v140 op_sel_hi:[1,0,0]
	v_fma_mix_f32 v141, v118, v118, v141 op_sel_hi:[1,1,0]
	v_fma_mix_f32 v140, v118, 1.0, v140 op_sel:[1,0,0] op_sel_hi:[1,0,0]
	v_fma_mix_f32 v141, v118, v118, v141 op_sel:[1,1,0] op_sel_hi:[1,1,0]
	v_fma_mix_f32 v140, v119, 1.0, v140 op_sel_hi:[1,0,0]
	v_fma_mix_f32 v141, v119, v119, v141 op_sel_hi:[1,1,0]
	v_fma_mix_f32 v140, v119, 1.0, v140 op_sel:[1,0,0] op_sel_hi:[1,0,0]
	v_fma_mix_f32 v141, v119, v119, v141 op_sel:[1,1,0] op_sel_hi:[1,1,0]
	ds_read_b128 v[208:211], v236
	ds_read_b128 v[128:131], v236 offset:1152
	s_add_u32 s94, s98, 0x3c000
	s_addc_u32 s95, s99, 0
	global_load_dwordx4 v[212:215], v191, s[94:95] offset:0 nt
	global_load_dwordx4 v[144:147], v191, s[94:95] offset:64 nt
	s_add_u32 s94, s98, 0x42000
	s_addc_u32 s95, s99, 0
	global_load_dwordx4 v[132:135], v191, s[94:95] offset:0 nt
	global_load_dwordx4 v[88:91], v191, s[94:95] offset:64 nt
	s_waitcnt vmcnt(13)
	v_cvt_f32_f16_e32 v72, v240
	v_cvt_f32_f16_sdwa v73, v240 dst_sel:DWORD dst_unused:UNUSED_PAD src0_sel:WORD_1
	v_cvt_f32_f16_e32 v74, v241
	v_cvt_f32_f16_sdwa v75, v241 dst_sel:DWORD dst_unused:UNUSED_PAD src0_sel:WORD_1
	v_cvt_f32_f16_e32 v80, v242
	v_cvt_f32_f16_sdwa v81, v242 dst_sel:DWORD dst_unused:UNUSED_PAD src0_sel:WORD_1
	v_cvt_f32_f16_e32 v82, v243
	v_cvt_f32_f16_sdwa v83, v243 dst_sel:DWORD dst_unused:UNUSED_PAD src0_sel:WORD_1
	v_sub_f32_e32 v72, v72, v194
	v_sub_f32_e32 v73, v73, v194
	v_sub_f32_e32 v74, v74, v194
	v_sub_f32_e32 v75, v75, v194
	v_sub_f32_e32 v80, v80, v194
	v_sub_f32_e32 v81, v81, v194
	v_sub_f32_e32 v82, v82, v194
	v_sub_f32_e32 v83, v83, v194
	v_pk_mul_f32 v[72:73], v[194:195], v[72:73] op_sel:[1,0]
	v_pk_mul_f32 v[74:75], v[194:195], v[74:75] op_sel:[1,0]
	v_pk_mul_f32 v[80:81], v[194:195], v[80:81] op_sel:[1,0]
	v_pk_mul_f32 v[82:83], v[194:195], v[82:83] op_sel:[1,0]
	v_pk_fma_f32 v[108:109], v[72:73], v[160:161], v[108:109]
	v_pk_fma_f32 v[110:111], v[74:75], v[162:163], v[110:111]
	v_pk_fma_f32 v[104:105], v[80:81], v[164:165], v[104:105]
	v_pk_fma_f32 v[106:107], v[82:83], v[166:167], v[106:107]
	v_cvt_pk_f16_f32 v108, v108, v109
	v_cvt_pk_f16_f32 v109, v110, v111
	v_cvt_pk_f16_f32 v110, v104, v105
	v_cvt_pk_f16_f32 v111, v106, v107
	s_waitcnt lgkmcnt(0)
	v_add_u32_e32 v83, 0x6000, v224
	buffer_store_dwordx4 v[208:211], v83, s[24:27], 0 offen nt
	v_add_u32_e32 v82, 0x9000, v224
	buffer_store_dwordx4 v[128:131], v82, s[24:27], 0 offen nt
	ds_write_b128 v235, v[108:111]
	v_fma_mix_f32 v142, v108, 1.0, 0 op_sel_hi:[1,0,0]
	v_fma_mix_f32 v143, v108, v108, 0 op_sel_hi:[1,1,0]
	v_fma_mix_f32 v142, v108, 1.0, v142 op_sel:[1,0,0] op_sel_hi:[1,0,0]
	v_fma_mix_f32 v143, v108, v108, v143 op_sel:[1,1,0] op_sel_hi:[1,1,0]
	v_fma_mix_f32 v142, v109, 1.0, v142 op_sel_hi:[1,0,0]
	v_fma_mix_f32 v143, v109, v109, v143 op_sel_hi:[1,1,0]
	v_fma_mix_f32 v142, v109, 1.0, v142 op_sel:[1,0,0] op_sel_hi:[1,0,0]
	v_fma_mix_f32 v143, v109, v109, v143 op_sel:[1,1,0] op_sel_hi:[1,1,0]
	v_fma_mix_f32 v142, v110, 1.0, v142 op_sel_hi:[1,0,0]
	v_fma_mix_f32 v143, v110, v110, v143 op_sel_hi:[1,1,0]
	v_fma_mix_f32 v142, v110, 1.0, v142 op_sel:[1,0,0] op_sel_hi:[1,0,0]
	v_fma_mix_f32 v143, v110, v110, v143 op_sel:[1,1,0] op_sel_hi:[1,1,0]
	v_fma_mix_f32 v142, v111, 1.0, v142 op_sel_hi:[1,0,0]
	v_fma_mix_f32 v143, v111, v111, v143 op_sel_hi:[1,1,0]
	v_fma_mix_f32 v142, v111, 1.0, v142 op_sel:[1,0,0] op_sel_hi:[1,0,0]
	v_fma_mix_f32 v143, v111, v111, v143 op_sel:[1,1,0] op_sel_hi:[1,1,0]
	s_waitcnt vmcnt(14)
	v_cvt_f32_f16_e32 v72, v244
	v_cvt_f32_f16_sdwa v73, v244 dst_sel:DWORD dst_unused:UNUSED_PAD src0_sel:WORD_1
	v_cvt_f32_f16_e32 v74, v245
	v_cvt_f32_f16_sdwa v75, v245 dst_sel:DWORD dst_unused:UNUSED_PAD src0_sel:WORD_1
	v_cvt_f32_f16_e32 v80, v246
	v_cvt_f32_f16_sdwa v81, v246 dst_sel:DWORD dst_unused:UNUSED_PAD src0_sel:WORD_1
	v_cvt_f32_f16_e32 v82, v247
	v_cvt_f32_f16_sdwa v83, v247 dst_sel:DWORD dst_unused:UNUSED_PAD src0_sel:WORD_1
	v_sub_f32_e32 v72, v72, v194
	v_sub_f32_e32 v73, v73, v194
	v_sub_f32_e32 v74, v74, v194
	v_sub_f32_e32 v75, v75, v194
	v_sub_f32_e32 v80, v80, v194
	v_sub_f32_e32 v81, v81, v194
	v_sub_f32_e32 v82, v82, v194
	v_sub_f32_e32 v83, v83, v194
	v_pk_mul_f32 v[72:73], v[194:195], v[72:73] op_sel:[1,0]
	v_pk_mul_f32 v[74:75], v[194:195], v[74:75] op_sel:[1,0]
	v_pk_mul_f32 v[80:81], v[194:195], v[80:81] op_sel:[1,0]
	v_pk_mul_f32 v[82:83], v[194:195], v[82:83] op_sel:[1,0]
	v_pk_fma_f32 v[100:101], v[72:73], v[168:169], v[100:101]
	v_pk_fma_f32 v[102:103], v[74:75], v[170:171], v[102:103]
	v_pk_fma_f32 v[96:97], v[80:81], v[172:173], v[96:97]
	v_pk_fma_f32 v[98:99], v[82:83], v[174:175], v[98:99]
	v_cvt_pk_f16_f32 v100, v100, v101
	v_cvt_pk_f16_f32 v101, v102, v103
	v_cvt_pk_f16_f32 v102, v96, v97
	v_cvt_pk_f16_f32 v103, v98, v99
	ds_write_b128 v235, v[100:103] offset:64
	v_fma_mix_f32 v142, v100, 1.0, v142 op_sel_hi:[1,0,0]
	v_fma_mix_f32 v143, v100, v100, v143 op_sel_hi:[1,1,0]
	v_fma_mix_f32 v142, v100, 1.0, v142 op_sel:[1,0,0] op_sel_hi:[1,0,0]
	v_fma_mix_f32 v143, v100, v100, v143 op_sel:[1,1,0] op_sel_hi:[1,1,0]
	v_fma_mix_f32 v142, v101, 1.0, v142 op_sel_hi:[1,0,0]
	v_fma_mix_f32 v143, v101, v101, v143 op_sel_hi:[1,1,0]
	v_fma_mix_f32 v142, v101, 1.0, v142 op_sel:[1,0,0] op_sel_hi:[1,0,0]
	v_fma_mix_f32 v143, v101, v101, v143 op_sel:[1,1,0] op_sel_hi:[1,1,0]
	v_fma_mix_f32 v142, v102, 1.0, v142 op_sel_hi:[1,0,0]
	v_fma_mix_f32 v143, v102, v102, v143 op_sel_hi:[1,1,0]
	v_fma_mix_f32 v142, v102, 1.0, v142 op_sel:[1,0,0] op_sel_hi:[1,0,0]
	v_fma_mix_f32 v143, v102, v102, v143 op_sel:[1,1,0] op_sel_hi:[1,1,0]
	v_fma_mix_f32 v142, v103, 1.0, v142 op_sel_hi:[1,0,0]
	v_fma_mix_f32 v143, v103, v103, v143 op_sel_hi:[1,1,0]
	v_fma_mix_f32 v142, v103, 1.0, v142 op_sel:[1,0,0] op_sel_hi:[1,0,0]
	v_fma_mix_f32 v143, v103, v103, v143 op_sel:[1,1,0] op_sel_hi:[1,1,0]
	ds_read_b128 v[92:95], v236
	ds_read_b128 v[120:123], v236 offset:1152
	s_waitcnt vmcnt(13)
	v_cvt_f32_f16_e32 v72, v248
	v_cvt_f32_f16_sdwa v73, v248 dst_sel:DWORD dst_unused:UNUSED_PAD src0_sel:WORD_1
	v_cvt_f32_f16_e32 v74, v249
	v_cvt_f32_f16_sdwa v75, v249 dst_sel:DWORD dst_unused:UNUSED_PAD src0_sel:WORD_1
	v_cvt_f32_f16_e32 v80, v250
	v_cvt_f32_f16_sdwa v81, v250 dst_sel:DWORD dst_unused:UNUSED_PAD src0_sel:WORD_1
	v_cvt_f32_f16_e32 v82, v251
	v_cvt_f32_f16_sdwa v83, v251 dst_sel:DWORD dst_unused:UNUSED_PAD src0_sel:WORD_1
	v_sub_f32_e32 v72, v72, v196
	v_sub_f32_e32 v73, v73, v196
	v_sub_f32_e32 v74, v74, v196
	v_sub_f32_e32 v75, v75, v196
	v_sub_f32_e32 v80, v80, v196
	v_sub_f32_e32 v81, v81, v196
	v_sub_f32_e32 v82, v82, v196
	v_sub_f32_e32 v83, v83, v196
	v_pk_mul_f32 v[72:73], v[196:197], v[72:73] op_sel:[1,0]
	v_pk_mul_f32 v[74:75], v[196:197], v[74:75] op_sel:[1,0]
	v_pk_mul_f32 v[80:81], v[196:197], v[80:81] op_sel:[1,0]
	v_pk_mul_f32 v[82:83], v[196:197], v[82:83] op_sel:[1,0]
	v_pk_fma_f32 v[84:85], v[72:73], v[160:161], v[84:85]
	v_pk_fma_f32 v[86:87], v[74:75], v[162:163], v[86:87]
	v_pk_fma_f32 v[76:77], v[80:81], v[164:165], v[76:77]
	v_pk_fma_f32 v[78:79], v[82:83], v[166:167], v[78:79]
	v_cvt_pk_f16_f32 v84, v84, v85
	v_cvt_pk_f16_f32 v85, v86, v87
	v_cvt_pk_f16_f32 v86, v76, v77
	v_cvt_pk_f16_f32 v87, v78, v79
	s_waitcnt lgkmcnt(0)
	v_add_u32_e32 v83, 0xc000, v224
	buffer_store_dwordx4 v[92:95], v83, s[24:27], 0 offen nt
	v_add_u32_e32 v82, 0xf000, v224
	buffer_store_dwordx4 v[120:123], v82, s[24:27], 0 offen nt
	ds_write_b128 v235, v[84:87]
	v_fma_mix_f32 v216, v84, 1.0, 0 op_sel_hi:[1,0,0]
	v_fma_mix_f32 v217, v84, v84, 0 op_sel_hi:[1,1,0]
	v_fma_mix_f32 v216, v84, 1.0, v216 op_sel:[1,0,0] op_sel_hi:[1,0,0]
	v_fma_mix_f32 v217, v84, v84, v217 op_sel:[1,1,0] op_sel_hi:[1,1,0]
	v_fma_mix_f32 v216, v85, 1.0, v216 op_sel_hi:[1,0,0]
	v_fma_mix_f32 v217, v85, v85, v217 op_sel_hi:[1,1,0]
	v_fma_mix_f32 v216, v85, 1.0, v216 op_sel:[1,0,0] op_sel_hi:[1,0,0]
	v_fma_mix_f32 v217, v85, v85, v217 op_sel:[1,1,0] op_sel_hi:[1,1,0]
	v_fma_mix_f32 v216, v86, 1.0, v216 op_sel_hi:[1,0,0]
	v_fma_mix_f32 v217, v86, v86, v217 op_sel_hi:[1,1,0]
	v_fma_mix_f32 v216, v86, 1.0, v216 op_sel:[1,0,0] op_sel_hi:[1,0,0]
	v_fma_mix_f32 v217, v86, v86, v217 op_sel:[1,1,0] op_sel_hi:[1,1,0]
	v_fma_mix_f32 v216, v87, 1.0, v216 op_sel_hi:[1,0,0]
	v_fma_mix_f32 v217, v87, v87, v217 op_sel_hi:[1,1,0]
	v_fma_mix_f32 v216, v87, 1.0, v216 op_sel:[1,0,0] op_sel_hi:[1,0,0]
	v_fma_mix_f32 v217, v87, v87, v217 op_sel:[1,1,0] op_sel_hi:[1,1,0]
	s_waitcnt vmcnt(14)
	v_cvt_f32_f16_e32 v72, v252
	v_cvt_f32_f16_sdwa v73, v252 dst_sel:DWORD dst_unused:UNUSED_PAD src0_sel:WORD_1
	v_cvt_f32_f16_e32 v74, v253
	v_cvt_f32_f16_sdwa v75, v253 dst_sel:DWORD dst_unused:UNUSED_PAD src0_sel:WORD_1
	v_cvt_f32_f16_e32 v80, v254
	v_cvt_f32_f16_sdwa v81, v254 dst_sel:DWORD dst_unused:UNUSED_PAD src0_sel:WORD_1
	v_cvt_f32_f16_e32 v82, v255
	v_cvt_f32_f16_sdwa v83, v255 dst_sel:DWORD dst_unused:UNUSED_PAD src0_sel:WORD_1
	v_sub_f32_e32 v72, v72, v196
	v_sub_f32_e32 v73, v73, v196
	v_sub_f32_e32 v74, v74, v196
	v_sub_f32_e32 v75, v75, v196
	v_sub_f32_e32 v80, v80, v196
	v_sub_f32_e32 v81, v81, v196
	v_sub_f32_e32 v82, v82, v196
	v_sub_f32_e32 v83, v83, v196
	v_pk_mul_f32 v[72:73], v[196:197], v[72:73] op_sel:[1,0]
	v_pk_mul_f32 v[74:75], v[196:197], v[74:75] op_sel:[1,0]
	v_pk_mul_f32 v[80:81], v[196:197], v[80:81] op_sel:[1,0]
	v_pk_mul_f32 v[82:83], v[196:197], v[82:83] op_sel:[1,0]
	v_pk_fma_f32 v[68:69], v[72:73], v[168:169], v[68:69]
	v_pk_fma_f32 v[70:71], v[74:75], v[170:171], v[70:71]
	v_pk_fma_f32 v[64:65], v[80:81], v[172:173], v[64:65]
	v_pk_fma_f32 v[66:67], v[82:83], v[174:175], v[66:67]
	v_cvt_pk_f16_f32 v68, v68, v69
	v_cvt_pk_f16_f32 v69, v70, v71
	v_cvt_pk_f16_f32 v70, v64, v65
	v_cvt_pk_f16_f32 v71, v66, v67
	ds_write_b128 v235, v[68:71] offset:64
	v_fma_mix_f32 v216, v68, 1.0, v216 op_sel_hi:[1,0,0]
	v_fma_mix_f32 v217, v68, v68, v217 op_sel_hi:[1,1,0]
	v_fma_mix_f32 v216, v68, 1.0, v216 op_sel:[1,0,0] op_sel_hi:[1,0,0]
	v_fma_mix_f32 v217, v68, v68, v217 op_sel:[1,1,0] op_sel_hi:[1,1,0]
	v_fma_mix_f32 v216, v69, 1.0, v216 op_sel_hi:[1,0,0]
	v_fma_mix_f32 v217, v69, v69, v217 op_sel_hi:[1,1,0]
	v_fma_mix_f32 v216, v69, 1.0, v216 op_sel:[1,0,0] op_sel_hi:[1,0,0]
	v_fma_mix_f32 v217, v69, v69, v217 op_sel:[1,1,0] op_sel_hi:[1,1,0]
	v_fma_mix_f32 v216, v70, 1.0, v216 op_sel_hi:[1,0,0]
	v_fma_mix_f32 v217, v70, v70, v217 op_sel_hi:[1,1,0]
	v_fma_mix_f32 v216, v70, 1.0, v216 op_sel:[1,0,0] op_sel_hi:[1,0,0]
	v_fma_mix_f32 v217, v70, v70, v217 op_sel:[1,1,0] op_sel_hi:[1,1,0]
	v_fma_mix_f32 v216, v71, 1.0, v216 op_sel_hi:[1,0,0]
	v_fma_mix_f32 v217, v71, v71, v217 op_sel_hi:[1,1,0]
	v_fma_mix_f32 v216, v71, 1.0, v216 op_sel:[1,0,0] op_sel_hi:[1,0,0]
	v_fma_mix_f32 v217, v71, v71, v217 op_sel:[1,1,0] op_sel_hi:[1,1,0]
	ds_read_b128 v[112:115], v236
	ds_read_b128 v[220:223], v236 offset:1152
	s_waitcnt vmcnt(13)
	v_cvt_f32_f16_e32 v72, v136
	v_cvt_f32_f16_sdwa v73, v136 dst_sel:DWORD dst_unused:UNUSED_PAD src0_sel:WORD_1
	v_cvt_f32_f16_e32 v74, v137
	v_cvt_f32_f16_sdwa v75, v137 dst_sel:DWORD dst_unused:UNUSED_PAD src0_sel:WORD_1
	v_cvt_f32_f16_e32 v80, v138
	v_cvt_f32_f16_sdwa v81, v138 dst_sel:DWORD dst_unused:UNUSED_PAD src0_sel:WORD_1
	v_cvt_f32_f16_e32 v82, v139
	v_cvt_f32_f16_sdwa v83, v139 dst_sel:DWORD dst_unused:UNUSED_PAD src0_sel:WORD_1
	v_sub_f32_e32 v72, v72, v198
	v_sub_f32_e32 v73, v73, v198
	v_sub_f32_e32 v74, v74, v198
	v_sub_f32_e32 v75, v75, v198
	v_sub_f32_e32 v80, v80, v198
	v_sub_f32_e32 v81, v81, v198
	v_sub_f32_e32 v82, v82, v198
	v_sub_f32_e32 v83, v83, v198
	v_pk_mul_f32 v[72:73], v[198:199], v[72:73] op_sel:[1,0]
	v_pk_mul_f32 v[74:75], v[198:199], v[74:75] op_sel:[1,0]
	v_pk_mul_f32 v[80:81], v[198:199], v[80:81] op_sel:[1,0]
	v_pk_mul_f32 v[82:83], v[198:199], v[82:83] op_sel:[1,0]
	v_pk_fma_f32 v[60:61], v[72:73], v[160:161], v[60:61]
	v_pk_fma_f32 v[62:63], v[74:75], v[162:163], v[62:63]
	v_pk_fma_f32 v[56:57], v[80:81], v[164:165], v[56:57]
	v_pk_fma_f32 v[58:59], v[82:83], v[166:167], v[58:59]
	v_cvt_pk_f16_f32 v60, v60, v61
	v_cvt_pk_f16_f32 v61, v62, v63
	v_cvt_pk_f16_f32 v62, v56, v57
	v_cvt_pk_f16_f32 v63, v58, v59
	s_waitcnt lgkmcnt(0)
	v_add_u32_e32 v83, 0x12000, v224
	buffer_store_dwordx4 v[112:115], v83, s[24:27], 0 offen nt
	v_add_u32_e32 v82, 0x15000, v224
	buffer_store_dwordx4 v[220:223], v82, s[24:27], 0 offen nt
	ds_write_b128 v235, v[60:63]
	v_fma_mix_f32 v218, v60, 1.0, 0 op_sel_hi:[1,0,0]
	v_fma_mix_f32 v219, v60, v60, 0 op_sel_hi:[1,1,0]
	v_fma_mix_f32 v218, v60, 1.0, v218 op_sel:[1,0,0] op_sel_hi:[1,0,0]
	v_fma_mix_f32 v219, v60, v60, v219 op_sel:[1,1,0] op_sel_hi:[1,1,0]
	v_fma_mix_f32 v218, v61, 1.0, v218 op_sel_hi:[1,0,0]
	v_fma_mix_f32 v219, v61, v61, v219 op_sel_hi:[1,1,0]
	v_fma_mix_f32 v218, v61, 1.0, v218 op_sel:[1,0,0] op_sel_hi:[1,0,0]
	v_fma_mix_f32 v219, v61, v61, v219 op_sel:[1,1,0] op_sel_hi:[1,1,0]
	v_fma_mix_f32 v218, v62, 1.0, v218 op_sel_hi:[1,0,0]
	v_fma_mix_f32 v219, v62, v62, v219 op_sel_hi:[1,1,0]
	v_fma_mix_f32 v218, v62, 1.0, v218 op_sel:[1,0,0] op_sel_hi:[1,0,0]
	v_fma_mix_f32 v219, v62, v62, v219 op_sel:[1,1,0] op_sel_hi:[1,1,0]
	v_fma_mix_f32 v218, v63, 1.0, v218 op_sel_hi:[1,0,0]
	v_fma_mix_f32 v219, v63, v63, v219 op_sel_hi:[1,1,0]
	v_fma_mix_f32 v218, v63, 1.0, v218 op_sel:[1,0,0] op_sel_hi:[1,0,0]
	v_fma_mix_f32 v219, v63, v63, v219 op_sel:[1,1,0] op_sel_hi:[1,1,0]
	s_waitcnt vmcnt(14)
	v_cvt_f32_f16_e32 v72, v148
	v_cvt_f32_f16_sdwa v73, v148 dst_sel:DWORD dst_unused:UNUSED_PAD src0_sel:WORD_1
	v_cvt_f32_f16_e32 v74, v149
	v_cvt_f32_f16_sdwa v75, v149 dst_sel:DWORD dst_unused:UNUSED_PAD src0_sel:WORD_1
	v_cvt_f32_f16_e32 v80, v150
	v_cvt_f32_f16_sdwa v81, v150 dst_sel:DWORD dst_unused:UNUSED_PAD src0_sel:WORD_1
	v_cvt_f32_f16_e32 v82, v151
	v_cvt_f32_f16_sdwa v83, v151 dst_sel:DWORD dst_unused:UNUSED_PAD src0_sel:WORD_1
	v_sub_f32_e32 v72, v72, v198
	v_sub_f32_e32 v73, v73, v198
	v_sub_f32_e32 v74, v74, v198
	v_sub_f32_e32 v75, v75, v198
	v_sub_f32_e32 v80, v80, v198
	v_sub_f32_e32 v81, v81, v198
	v_sub_f32_e32 v82, v82, v198
	v_sub_f32_e32 v83, v83, v198
	v_pk_mul_f32 v[72:73], v[198:199], v[72:73] op_sel:[1,0]
	v_pk_mul_f32 v[74:75], v[198:199], v[74:75] op_sel:[1,0]
	v_pk_mul_f32 v[80:81], v[198:199], v[80:81] op_sel:[1,0]
	v_pk_mul_f32 v[82:83], v[198:199], v[82:83] op_sel:[1,0]
	v_pk_fma_f32 v[52:53], v[72:73], v[168:169], v[52:53]
	v_pk_fma_f32 v[54:55], v[74:75], v[170:171], v[54:55]
	v_pk_fma_f32 v[48:49], v[80:81], v[172:173], v[48:49]
	v_pk_fma_f32 v[50:51], v[82:83], v[174:175], v[50:51]
	v_cvt_pk_f16_f32 v52, v52, v53
	v_cvt_pk_f16_f32 v53, v54, v55
	v_cvt_pk_f16_f32 v54, v48, v49
	v_cvt_pk_f16_f32 v55, v50, v51
	ds_write_b128 v235, v[52:55] offset:64
	v_fma_mix_f32 v218, v52, 1.0, v218 op_sel_hi:[1,0,0]
	v_fma_mix_f32 v219, v52, v52, v219 op_sel_hi:[1,1,0]
	v_fma_mix_f32 v218, v52, 1.0, v218 op_sel:[1,0,0] op_sel_hi:[1,0,0]
	v_fma_mix_f32 v219, v52, v52, v219 op_sel:[1,1,0] op_sel_hi:[1,1,0]
	v_fma_mix_f32 v218, v53, 1.0, v218 op_sel_hi:[1,0,0]
	v_fma_mix_f32 v219, v53, v53, v219 op_sel_hi:[1,1,0]
	v_fma_mix_f32 v218, v53, 1.0, v218 op_sel:[1,0,0] op_sel_hi:[1,0,0]
	v_fma_mix_f32 v219, v53, v53, v219 op_sel:[1,1,0] op_sel_hi:[1,1,0]
	v_fma_mix_f32 v218, v54, 1.0, v218 op_sel_hi:[1,0,0]
	v_fma_mix_f32 v219, v54, v54, v219 op_sel_hi:[1,1,0]
	v_fma_mix_f32 v218, v54, 1.0, v218 op_sel:[1,0,0] op_sel_hi:[1,0,0]
	v_fma_mix_f32 v219, v54, v54, v219 op_sel:[1,1,0] op_sel_hi:[1,1,0]
	v_fma_mix_f32 v218, v55, 1.0, v218 op_sel_hi:[1,0,0]
	v_fma_mix_f32 v219, v55, v55, v219 op_sel_hi:[1,1,0]
	v_fma_mix_f32 v218, v55, 1.0, v218 op_sel:[1,0,0] op_sel_hi:[1,0,0]
	v_fma_mix_f32 v219, v55, v55, v219 op_sel:[1,1,0] op_sel_hi:[1,1,0]
	ds_read_b128 v[124:127], v236
	ds_read_b128 v[116:119], v236 offset:1152
	s_waitcnt vmcnt(13)
	v_cvt_f32_f16_e32 v72, v152
	v_cvt_f32_f16_sdwa v73, v152 dst_sel:DWORD dst_unused:UNUSED_PAD src0_sel:WORD_1
	v_cvt_f32_f16_e32 v74, v153
	v_cvt_f32_f16_sdwa v75, v153 dst_sel:DWORD dst_unused:UNUSED_PAD src0_sel:WORD_1
	v_cvt_f32_f16_e32 v80, v154
	v_cvt_f32_f16_sdwa v81, v154 dst_sel:DWORD dst_unused:UNUSED_PAD src0_sel:WORD_1
	v_cvt_f32_f16_e32 v82, v155
	v_cvt_f32_f16_sdwa v83, v155 dst_sel:DWORD dst_unused:UNUSED_PAD src0_sel:WORD_1
	v_sub_f32_e32 v72, v72, v200
	v_sub_f32_e32 v73, v73, v200
	v_sub_f32_e32 v74, v74, v200
	v_sub_f32_e32 v75, v75, v200
	v_sub_f32_e32 v80, v80, v200
	v_sub_f32_e32 v81, v81, v200
	v_sub_f32_e32 v82, v82, v200
	v_sub_f32_e32 v83, v83, v200
	v_pk_mul_f32 v[72:73], v[200:201], v[72:73] op_sel:[1,0]
	v_pk_mul_f32 v[74:75], v[200:201], v[74:75] op_sel:[1,0]
	v_pk_mul_f32 v[80:81], v[200:201], v[80:81] op_sel:[1,0]
	v_pk_mul_f32 v[82:83], v[200:201], v[82:83] op_sel:[1,0]
	v_pk_fma_f32 v[44:45], v[72:73], v[160:161], v[44:45]
	v_pk_fma_f32 v[46:47], v[74:75], v[162:163], v[46:47]
	v_pk_fma_f32 v[40:41], v[80:81], v[164:165], v[40:41]
	v_pk_fma_f32 v[42:43], v[82:83], v[166:167], v[42:43]
	v_cvt_pk_f16_f32 v44, v44, v45
	v_cvt_pk_f16_f32 v45, v46, v47
	v_cvt_pk_f16_f32 v46, v40, v41
	v_cvt_pk_f16_f32 v47, v42, v43
	s_waitcnt lgkmcnt(0)
	v_add_u32_e32 v83, 0x30000, v224
	buffer_store_dwordx4 v[124:127], v83, s[24:27], 0 offen nt
	v_add_u32_e32 v82, 0x33000, v224
	buffer_store_dwordx4 v[116:119], v82, s[24:27], 0 offen nt
	ds_write_b128 v235, v[44:47]
	v_fma_mix_f32 v208, v44, 1.0, 0 op_sel_hi:[1,0,0]
	v_fma_mix_f32 v209, v44, v44, 0 op_sel_hi:[1,1,0]
	v_fma_mix_f32 v208, v44, 1.0, v208 op_sel:[1,0,0] op_sel_hi:[1,0,0]
	v_fma_mix_f32 v209, v44, v44, v209 op_sel:[1,1,0] op_sel_hi:[1,1,0]
	v_fma_mix_f32 v208, v45, 1.0, v208 op_sel_hi:[1,0,0]
	v_fma_mix_f32 v209, v45, v45, v209 op_sel_hi:[1,1,0]
	v_fma_mix_f32 v208, v45, 1.0, v208 op_sel:[1,0,0] op_sel_hi:[1,0,0]
	v_fma_mix_f32 v209, v45, v45, v209 op_sel:[1,1,0] op_sel_hi:[1,1,0]
	v_fma_mix_f32 v208, v46, 1.0, v208 op_sel_hi:[1,0,0]
	v_fma_mix_f32 v209, v46, v46, v209 op_sel_hi:[1,1,0]
	v_fma_mix_f32 v208, v46, 1.0, v208 op_sel:[1,0,0] op_sel_hi:[1,0,0]
	v_fma_mix_f32 v209, v46, v46, v209 op_sel:[1,1,0] op_sel_hi:[1,1,0]
	v_fma_mix_f32 v208, v47, 1.0, v208 op_sel_hi:[1,0,0]
	v_fma_mix_f32 v209, v47, v47, v209 op_sel_hi:[1,1,0]
	v_fma_mix_f32 v208, v47, 1.0, v208 op_sel:[1,0,0] op_sel_hi:[1,0,0]
	v_fma_mix_f32 v209, v47, v47, v209 op_sel:[1,1,0] op_sel_hi:[1,1,0]
	s_waitcnt vmcnt(14)
	v_cvt_f32_f16_e32 v72, v156
	v_cvt_f32_f16_sdwa v73, v156 dst_sel:DWORD dst_unused:UNUSED_PAD src0_sel:WORD_1
	v_cvt_f32_f16_e32 v74, v157
	v_cvt_f32_f16_sdwa v75, v157 dst_sel:DWORD dst_unused:UNUSED_PAD src0_sel:WORD_1
	v_cvt_f32_f16_e32 v80, v158
	v_cvt_f32_f16_sdwa v81, v158 dst_sel:DWORD dst_unused:UNUSED_PAD src0_sel:WORD_1
	v_cvt_f32_f16_e32 v82, v159
	v_cvt_f32_f16_sdwa v83, v159 dst_sel:DWORD dst_unused:UNUSED_PAD src0_sel:WORD_1
	v_sub_f32_e32 v72, v72, v200
	v_sub_f32_e32 v73, v73, v200
	v_sub_f32_e32 v74, v74, v200
	v_sub_f32_e32 v75, v75, v200
	v_sub_f32_e32 v80, v80, v200
	v_sub_f32_e32 v81, v81, v200
	v_sub_f32_e32 v82, v82, v200
	v_sub_f32_e32 v83, v83, v200
	v_pk_mul_f32 v[72:73], v[200:201], v[72:73] op_sel:[1,0]
	v_pk_mul_f32 v[74:75], v[200:201], v[74:75] op_sel:[1,0]
	v_pk_mul_f32 v[80:81], v[200:201], v[80:81] op_sel:[1,0]
	v_pk_mul_f32 v[82:83], v[200:201], v[82:83] op_sel:[1,0]
	v_pk_fma_f32 v[36:37], v[72:73], v[168:169], v[36:37]
	v_pk_fma_f32 v[38:39], v[74:75], v[170:171], v[38:39]
	v_pk_fma_f32 v[32:33], v[80:81], v[172:173], v[32:33]
	v_pk_fma_f32 v[34:35], v[82:83], v[174:175], v[34:35]
	v_cvt_pk_f16_f32 v36, v36, v37
	v_cvt_pk_f16_f32 v37, v38, v39
	v_cvt_pk_f16_f32 v38, v32, v33
	v_cvt_pk_f16_f32 v39, v34, v35
	ds_write_b128 v235, v[36:39] offset:64
	v_fma_mix_f32 v208, v36, 1.0, v208 op_sel_hi:[1,0,0]
	v_fma_mix_f32 v209, v36, v36, v209 op_sel_hi:[1,1,0]
	v_fma_mix_f32 v208, v36, 1.0, v208 op_sel:[1,0,0] op_sel_hi:[1,0,0]
	v_fma_mix_f32 v209, v36, v36, v209 op_sel:[1,1,0] op_sel_hi:[1,1,0]
	v_fma_mix_f32 v208, v37, 1.0, v208 op_sel_hi:[1,0,0]
	v_fma_mix_f32 v209, v37, v37, v209 op_sel_hi:[1,1,0]
	v_fma_mix_f32 v208, v37, 1.0, v208 op_sel:[1,0,0] op_sel_hi:[1,0,0]
	v_fma_mix_f32 v209, v37, v37, v209 op_sel:[1,1,0] op_sel_hi:[1,1,0]
	v_fma_mix_f32 v208, v38, 1.0, v208 op_sel_hi:[1,0,0]
	v_fma_mix_f32 v209, v38, v38, v209 op_sel_hi:[1,1,0]
	v_fma_mix_f32 v208, v38, 1.0, v208 op_sel:[1,0,0] op_sel_hi:[1,0,0]
	v_fma_mix_f32 v209, v38, v38, v209 op_sel:[1,1,0] op_sel_hi:[1,1,0]
	v_fma_mix_f32 v208, v39, 1.0, v208 op_sel_hi:[1,0,0]
	v_fma_mix_f32 v209, v39, v39, v209 op_sel_hi:[1,1,0]
	v_fma_mix_f32 v208, v39, 1.0, v208 op_sel:[1,0,0] op_sel_hi:[1,0,0]
	v_fma_mix_f32 v209, v39, v39, v209 op_sel:[1,1,0] op_sel_hi:[1,1,0]
	ds_read_b128 v[128:131], v236
	ds_read_b128 v[104:107], v236 offset:1152
	s_waitcnt vmcnt(11)
	v_cvt_f32_f16_e32 v72, v212
	v_cvt_f32_f16_sdwa v73, v212 dst_sel:DWORD dst_unused:UNUSED_PAD src0_sel:WORD_1
	v_cvt_f32_f16_e32 v74, v213
	v_cvt_f32_f16_sdwa v75, v213 dst_sel:DWORD dst_unused:UNUSED_PAD src0_sel:WORD_1
	v_cvt_f32_f16_e32 v80, v214
	v_cvt_f32_f16_sdwa v81, v214 dst_sel:DWORD dst_unused:UNUSED_PAD src0_sel:WORD_1
	v_cvt_f32_f16_e32 v82, v215
	v_cvt_f32_f16_sdwa v83, v215 dst_sel:DWORD dst_unused:UNUSED_PAD src0_sel:WORD_1
	v_sub_f32_e32 v72, v72, v202
	v_sub_f32_e32 v73, v73, v202
	v_sub_f32_e32 v74, v74, v202
	v_sub_f32_e32 v75, v75, v202
	v_sub_f32_e32 v80, v80, v202
	v_sub_f32_e32 v81, v81, v202
	v_sub_f32_e32 v82, v82, v202
	v_sub_f32_e32 v83, v83, v202
	v_pk_mul_f32 v[72:73], v[202:203], v[72:73] op_sel:[1,0]
	v_pk_mul_f32 v[74:75], v[202:203], v[74:75] op_sel:[1,0]
	v_pk_mul_f32 v[80:81], v[202:203], v[80:81] op_sel:[1,0]
	v_pk_mul_f32 v[82:83], v[202:203], v[82:83] op_sel:[1,0]
	v_pk_fma_f32 v[28:29], v[72:73], v[160:161], v[28:29]
	v_pk_fma_f32 v[30:31], v[74:75], v[162:163], v[30:31]
	v_pk_fma_f32 v[24:25], v[80:81], v[164:165], v[24:25]
	v_pk_fma_f32 v[26:27], v[82:83], v[166:167], v[26:27]
	v_cvt_pk_f16_f32 v28, v28, v29
	v_cvt_pk_f16_f32 v29, v30, v31
	v_cvt_pk_f16_f32 v30, v24, v25
	v_cvt_pk_f16_f32 v31, v26, v27
	s_waitcnt lgkmcnt(0)
	v_add_u32_e32 v83, 0x36000, v224
	buffer_store_dwordx4 v[128:131], v83, s[24:27], 0 offen nt
	v_add_u32_e32 v82, 0x39000, v224
	buffer_store_dwordx4 v[104:107], v82, s[24:27], 0 offen nt
	ds_write_b128 v235, v[28:31]
	v_fma_mix_f32 v210, v28, 1.0, 0 op_sel_hi:[1,0,0]
	v_fma_mix_f32 v211, v28, v28, 0 op_sel_hi:[1,1,0]
	v_fma_mix_f32 v210, v28, 1.0, v210 op_sel:[1,0,0] op_sel_hi:[1,0,0]
	v_fma_mix_f32 v211, v28, v28, v211 op_sel:[1,1,0] op_sel_hi:[1,1,0]
	v_fma_mix_f32 v210, v29, 1.0, v210 op_sel_hi:[1,0,0]
	v_fma_mix_f32 v211, v29, v29, v211 op_sel_hi:[1,1,0]
	v_fma_mix_f32 v210, v29, 1.0, v210 op_sel:[1,0,0] op_sel_hi:[1,0,0]
	v_fma_mix_f32 v211, v29, v29, v211 op_sel:[1,1,0] op_sel_hi:[1,1,0]
	v_fma_mix_f32 v210, v30, 1.0, v210 op_sel_hi:[1,0,0]
	v_fma_mix_f32 v211, v30, v30, v211 op_sel_hi:[1,1,0]
	v_fma_mix_f32 v210, v30, 1.0, v210 op_sel:[1,0,0] op_sel_hi:[1,0,0]
	v_fma_mix_f32 v211, v30, v30, v211 op_sel:[1,1,0] op_sel_hi:[1,1,0]
	v_fma_mix_f32 v210, v31, 1.0, v210 op_sel_hi:[1,0,0]
	v_fma_mix_f32 v211, v31, v31, v211 op_sel_hi:[1,1,0]
	v_fma_mix_f32 v210, v31, 1.0, v210 op_sel:[1,0,0] op_sel_hi:[1,0,0]
	v_fma_mix_f32 v211, v31, v31, v211 op_sel:[1,1,0] op_sel_hi:[1,1,0]
	s_waitcnt vmcnt(12)
	v_cvt_f32_f16_e32 v72, v144
	v_cvt_f32_f16_sdwa v73, v144 dst_sel:DWORD dst_unused:UNUSED_PAD src0_sel:WORD_1
	v_cvt_f32_f16_e32 v74, v145
	v_cvt_f32_f16_sdwa v75, v145 dst_sel:DWORD dst_unused:UNUSED_PAD src0_sel:WORD_1
	v_cvt_f32_f16_e32 v80, v146
	v_cvt_f32_f16_sdwa v81, v146 dst_sel:DWORD dst_unused:UNUSED_PAD src0_sel:WORD_1
	v_cvt_f32_f16_e32 v82, v147
	v_cvt_f32_f16_sdwa v83, v147 dst_sel:DWORD dst_unused:UNUSED_PAD src0_sel:WORD_1
	v_sub_f32_e32 v72, v72, v202
	v_sub_f32_e32 v73, v73, v202
	v_sub_f32_e32 v74, v74, v202
	v_sub_f32_e32 v75, v75, v202
	v_sub_f32_e32 v80, v80, v202
	v_sub_f32_e32 v81, v81, v202
	v_sub_f32_e32 v82, v82, v202
	v_sub_f32_e32 v83, v83, v202
	v_pk_mul_f32 v[72:73], v[202:203], v[72:73] op_sel:[1,0]
	v_pk_mul_f32 v[74:75], v[202:203], v[74:75] op_sel:[1,0]
	v_pk_mul_f32 v[80:81], v[202:203], v[80:81] op_sel:[1,0]
	v_pk_mul_f32 v[82:83], v[202:203], v[82:83] op_sel:[1,0]
	v_pk_fma_f32 v[20:21], v[72:73], v[168:169], v[20:21]
	v_pk_fma_f32 v[22:23], v[74:75], v[170:171], v[22:23]
	v_pk_fma_f32 v[16:17], v[80:81], v[172:173], v[16:17]
	v_pk_fma_f32 v[18:19], v[82:83], v[174:175], v[18:19]
	v_cvt_pk_f16_f32 v20, v20, v21
	v_cvt_pk_f16_f32 v21, v22, v23
	v_cvt_pk_f16_f32 v22, v16, v17
	v_cvt_pk_f16_f32 v23, v18, v19
	ds_write_b128 v235, v[20:23] offset:64
	v_fma_mix_f32 v210, v20, 1.0, v210 op_sel_hi:[1,0,0]
	v_fma_mix_f32 v211, v20, v20, v211 op_sel_hi:[1,1,0]
	v_fma_mix_f32 v210, v20, 1.0, v210 op_sel:[1,0,0] op_sel_hi:[1,0,0]
	v_fma_mix_f32 v211, v20, v20, v211 op_sel:[1,1,0] op_sel_hi:[1,1,0]
	v_fma_mix_f32 v210, v21, 1.0, v210 op_sel_hi:[1,0,0]
	v_fma_mix_f32 v211, v21, v21, v211 op_sel_hi:[1,1,0]
	v_fma_mix_f32 v210, v21, 1.0, v210 op_sel:[1,0,0] op_sel_hi:[1,0,0]
	v_fma_mix_f32 v211, v21, v21, v211 op_sel:[1,1,0] op_sel_hi:[1,1,0]
	v_fma_mix_f32 v210, v22, 1.0, v210 op_sel_hi:[1,0,0]
	v_fma_mix_f32 v211, v22, v22, v211 op_sel_hi:[1,1,0]
	v_fma_mix_f32 v210, v22, 1.0, v210 op_sel:[1,0,0] op_sel_hi:[1,0,0]
	v_fma_mix_f32 v211, v22, v22, v211 op_sel:[1,1,0] op_sel_hi:[1,1,0]
	v_fma_mix_f32 v210, v23, 1.0, v210 op_sel_hi:[1,0,0]
	v_fma_mix_f32 v211, v23, v23, v211 op_sel_hi:[1,1,0]
	v_fma_mix_f32 v210, v23, 1.0, v210 op_sel:[1,0,0] op_sel_hi:[1,0,0]
	v_fma_mix_f32 v211, v23, v23, v211 op_sel:[1,1,0] op_sel_hi:[1,1,0]
	ds_read_b128 v[240:243], v236
	ds_read_b128 v[96:99], v236 offset:1152
	s_waitcnt vmcnt(11)
	v_cvt_f32_f16_e32 v72, v132
	v_cvt_f32_f16_sdwa v73, v132 dst_sel:DWORD dst_unused:UNUSED_PAD src0_sel:WORD_1
	v_cvt_f32_f16_e32 v74, v133
	v_cvt_f32_f16_sdwa v75, v133 dst_sel:DWORD dst_unused:UNUSED_PAD src0_sel:WORD_1
	v_cvt_f32_f16_e32 v80, v134
	v_cvt_f32_f16_sdwa v81, v134 dst_sel:DWORD dst_unused:UNUSED_PAD src0_sel:WORD_1
	v_cvt_f32_f16_e32 v82, v135
	v_cvt_f32_f16_sdwa v83, v135 dst_sel:DWORD dst_unused:UNUSED_PAD src0_sel:WORD_1
	v_sub_f32_e32 v72, v72, v204
	v_sub_f32_e32 v73, v73, v204
	v_sub_f32_e32 v74, v74, v204
	v_sub_f32_e32 v75, v75, v204
	v_sub_f32_e32 v80, v80, v204
	v_sub_f32_e32 v81, v81, v204
	v_sub_f32_e32 v82, v82, v204
	v_sub_f32_e32 v83, v83, v204
	v_pk_mul_f32 v[72:73], v[204:205], v[72:73] op_sel:[1,0]
	v_pk_mul_f32 v[74:75], v[204:205], v[74:75] op_sel:[1,0]
	v_pk_mul_f32 v[80:81], v[204:205], v[80:81] op_sel:[1,0]
	v_pk_mul_f32 v[82:83], v[204:205], v[82:83] op_sel:[1,0]
	v_pk_fma_f32 v[12:13], v[72:73], v[160:161], v[12:13]
	v_pk_fma_f32 v[14:15], v[74:75], v[162:163], v[14:15]
	v_pk_fma_f32 v[8:9], v[80:81], v[164:165], v[8:9]
	v_pk_fma_f32 v[10:11], v[82:83], v[166:167], v[10:11]
	v_cvt_pk_f16_f32 v12, v12, v13
	v_cvt_pk_f16_f32 v13, v14, v15
	v_cvt_pk_f16_f32 v14, v8, v9
	v_cvt_pk_f16_f32 v15, v10, v11
	s_waitcnt lgkmcnt(0)
	v_add_u32_e32 v83, 0x3c000, v224
	buffer_store_dwordx4 v[240:243], v83, s[24:27], 0 offen nt
	v_add_u32_e32 v82, 0x3f000, v224
	buffer_store_dwordx4 v[96:99], v82, s[24:27], 0 offen nt
	ds_write_b128 v235, v[12:15]
	v_fma_mix_f32 v244, v12, 1.0, 0 op_sel_hi:[1,0,0]
	v_fma_mix_f32 v245, v12, v12, 0 op_sel_hi:[1,1,0]
	v_fma_mix_f32 v244, v12, 1.0, v244 op_sel:[1,0,0] op_sel_hi:[1,0,0]
	v_fma_mix_f32 v245, v12, v12, v245 op_sel:[1,1,0] op_sel_hi:[1,1,0]
	v_fma_mix_f32 v244, v13, 1.0, v244 op_sel_hi:[1,0,0]
	v_fma_mix_f32 v245, v13, v13, v245 op_sel_hi:[1,1,0]
	v_fma_mix_f32 v244, v13, 1.0, v244 op_sel:[1,0,0] op_sel_hi:[1,0,0]
	v_fma_mix_f32 v245, v13, v13, v245 op_sel:[1,1,0] op_sel_hi:[1,1,0]
	v_fma_mix_f32 v244, v14, 1.0, v244 op_sel_hi:[1,0,0]
	v_fma_mix_f32 v245, v14, v14, v245 op_sel_hi:[1,1,0]
	v_fma_mix_f32 v244, v14, 1.0, v244 op_sel:[1,0,0] op_sel_hi:[1,0,0]
	v_fma_mix_f32 v245, v14, v14, v245 op_sel:[1,1,0] op_sel_hi:[1,1,0]
	v_fma_mix_f32 v244, v15, 1.0, v244 op_sel_hi:[1,0,0]
	v_fma_mix_f32 v245, v15, v15, v245 op_sel_hi:[1,1,0]
	v_fma_mix_f32 v244, v15, 1.0, v244 op_sel:[1,0,0] op_sel_hi:[1,0,0]
	v_fma_mix_f32 v245, v15, v15, v245 op_sel:[1,1,0] op_sel_hi:[1,1,0]
	s_waitcnt vmcnt(12)
	v_cvt_f32_f16_e32 v72, v88
	v_cvt_f32_f16_sdwa v73, v88 dst_sel:DWORD dst_unused:UNUSED_PAD src0_sel:WORD_1
	v_cvt_f32_f16_e32 v74, v89
	v_cvt_f32_f16_sdwa v75, v89 dst_sel:DWORD dst_unused:UNUSED_PAD src0_sel:WORD_1
	v_cvt_f32_f16_e32 v80, v90
	v_cvt_f32_f16_sdwa v81, v90 dst_sel:DWORD dst_unused:UNUSED_PAD src0_sel:WORD_1
	v_cvt_f32_f16_e32 v82, v91
	v_cvt_f32_f16_sdwa v83, v91 dst_sel:DWORD dst_unused:UNUSED_PAD src0_sel:WORD_1
	v_sub_f32_e32 v72, v72, v204
	v_sub_f32_e32 v73, v73, v204
	v_sub_f32_e32 v74, v74, v204
	v_sub_f32_e32 v75, v75, v204
	v_sub_f32_e32 v80, v80, v204
	v_sub_f32_e32 v81, v81, v204
	v_sub_f32_e32 v82, v82, v204
	v_sub_f32_e32 v83, v83, v204
	v_pk_mul_f32 v[72:73], v[204:205], v[72:73] op_sel:[1,0]
	v_pk_mul_f32 v[74:75], v[204:205], v[74:75] op_sel:[1,0]
	v_pk_mul_f32 v[80:81], v[204:205], v[80:81] op_sel:[1,0]
	v_pk_mul_f32 v[82:83], v[204:205], v[82:83] op_sel:[1,0]
	v_pk_fma_f32 v[4:5], v[72:73], v[168:169], v[4:5]
	v_pk_fma_f32 v[6:7], v[74:75], v[170:171], v[6:7]
	v_pk_fma_f32 v[0:1], v[80:81], v[172:173], v[0:1]
	v_pk_fma_f32 v[2:3], v[82:83], v[174:175], v[2:3]
	v_cvt_pk_f16_f32 v4, v4, v5
	v_cvt_pk_f16_f32 v5, v6, v7
	v_cvt_pk_f16_f32 v6, v0, v1
	v_cvt_pk_f16_f32 v7, v2, v3
	ds_write_b128 v235, v[4:7] offset:64
	v_fma_mix_f32 v244, v4, 1.0, v244 op_sel_hi:[1,0,0]
	v_fma_mix_f32 v245, v4, v4, v245 op_sel_hi:[1,1,0]
	v_fma_mix_f32 v244, v4, 1.0, v244 op_sel:[1,0,0] op_sel_hi:[1,0,0]
	v_fma_mix_f32 v245, v4, v4, v245 op_sel:[1,1,0] op_sel_hi:[1,1,0]
	v_fma_mix_f32 v244, v5, 1.0, v244 op_sel_hi:[1,0,0]
	v_fma_mix_f32 v245, v5, v5, v245 op_sel_hi:[1,1,0]
	v_fma_mix_f32 v244, v5, 1.0, v244 op_sel:[1,0,0] op_sel_hi:[1,0,0]
	v_fma_mix_f32 v245, v5, v5, v245 op_sel:[1,1,0] op_sel_hi:[1,1,0]
	v_fma_mix_f32 v244, v6, 1.0, v244 op_sel_hi:[1,0,0]
	v_fma_mix_f32 v245, v6, v6, v245 op_sel_hi:[1,1,0]
	v_fma_mix_f32 v244, v6, 1.0, v244 op_sel:[1,0,0] op_sel_hi:[1,0,0]
	v_fma_mix_f32 v245, v6, v6, v245 op_sel:[1,1,0] op_sel_hi:[1,1,0]
	v_fma_mix_f32 v244, v7, 1.0, v244 op_sel_hi:[1,0,0]
	v_fma_mix_f32 v245, v7, v7, v245 op_sel_hi:[1,1,0]
	v_fma_mix_f32 v244, v7, 1.0, v244 op_sel:[1,0,0] op_sel_hi:[1,0,0]
	v_fma_mix_f32 v245, v7, v7, v245 op_sel:[1,1,0] op_sel_hi:[1,1,0]
	ds_read_b128 v[108:111], v236
	ds_read_b128 v[100:103], v236 offset:1152
	s_waitcnt lgkmcnt(0)
	v_add_u32_e32 v83, 0x42000, v224
	buffer_store_dwordx4 v[108:111], v83, s[24:27], 0 offen nt
	v_add_u32_e32 v82, 0x45000, v224
	buffer_store_dwordx4 v[100:103], v82, s[24:27], 0 offen nt
	v_xor_b32_e32 v225, 16, v234
	v_lshlrev_b32_e32 v225, 2, v225
	v_xor_b32_e32 v246, 32, v234
	v_lshlrev_b32_e32 v246, 2, v246
	ds_bpermute_b32 v92, v225, v206
	ds_bpermute_b32 v93, v225, v207
	ds_bpermute_b32 v94, v225, v140
	ds_bpermute_b32 v95, v225, v141
	ds_bpermute_b32 v120, v225, v142
	ds_bpermute_b32 v121, v225, v143
	ds_bpermute_b32 v122, v225, v216
	ds_bpermute_b32 v123, v225, v217
	s_waitcnt lgkmcnt(0)
	v_pk_add_f32 v[206:207], v[206:207], v[92:93]
	v_pk_add_f32 v[140:141], v[140:141], v[94:95]
	v_pk_add_f32 v[142:143], v[142:143], v[120:121]
	v_pk_add_f32 v[216:217], v[216:217], v[122:123]
	ds_bpermute_b32 v92, v225, v218
	ds_bpermute_b32 v93, v225, v219
	ds_bpermute_b32 v94, v225, v208
	ds_bpermute_b32 v95, v225, v209
	ds_bpermute_b32 v120, v225, v210
	ds_bpermute_b32 v121, v225, v211
	ds_bpermute_b32 v122, v225, v244
	ds_bpermute_b32 v123, v225, v245
	s_waitcnt lgkmcnt(0)
	v_pk_add_f32 v[218:219], v[218:219], v[92:93]
	v_pk_add_f32 v[208:209], v[208:209], v[94:95]
	v_pk_add_f32 v[210:211], v[210:211], v[120:121]
	v_pk_add_f32 v[244:245], v[244:245], v[122:123]
	ds_bpermute_b32 v92, v246, v206
	ds_bpermute_b32 v93, v246, v207
	ds_bpermute_b32 v94, v246, v140
	ds_bpermute_b32 v95, v246, v141
	ds_bpermute_b32 v120, v246, v142
	ds_bpermute_b32 v121, v246, v143
	ds_bpermute_b32 v122, v246, v216
	ds_bpermute_b32 v123, v246, v217
	s_waitcnt lgkmcnt(0)
	v_pk_add_f32 v[206:207], v[206:207], v[92:93]
	v_pk_add_f32 v[140:141], v[140:141], v[94:95]
	v_pk_add_f32 v[142:143], v[142:143], v[120:121]
	v_pk_add_f32 v[216:217], v[216:217], v[122:123]
	ds_bpermute_b32 v92, v246, v218
	ds_bpermute_b32 v93, v246, v219
	ds_bpermute_b32 v94, v246, v208
	ds_bpermute_b32 v95, v246, v209
	ds_bpermute_b32 v120, v246, v210
	ds_bpermute_b32 v121, v246, v211
	ds_bpermute_b32 v122, v246, v244
	ds_bpermute_b32 v123, v246, v245
	s_waitcnt lgkmcnt(0)
	v_pk_add_f32 v[218:219], v[218:219], v[92:93]
	v_pk_add_f32 v[208:209], v[208:209], v[94:95]
	v_pk_add_f32 v[210:211], v[210:211], v[120:121]
	v_pk_add_f32 v[244:245], v[244:245], v[122:123]
	s_mov_b64 exec, 0xffff
	global_store_dwordx2 v190, v[206:207], s[100:101] offset:0
	global_store_dwordx2 v190, v[140:141], s[100:101] offset:128
	global_store_dwordx2 v190, v[142:143], s[100:101] offset:256
	global_store_dwordx2 v190, v[216:217], s[100:101] offset:384
	global_store_dwordx2 v190, v[218:219], s[100:101] offset:1024
	global_store_dwordx2 v190, v[208:209], s[100:101] offset:1152
	global_store_dwordx2 v190, v[210:211], s[100:101] offset:1280
	global_store_dwordx2 v190, v[244:245], s[100:101] offset:1408
	s_mov_b64 exec, -1
	s_mov_b32 s83, s81
	s_mov_b32 s84, s82
	s_mov_b64 s[40:41], s[0:1]
	s_mov_b64 s[38:39], s[8:9]
	s_mov_b64 vcc, s[6:7]
	s_cbranch_vccz .LBB10_12
	s_waitcnt vmcnt(0)
	s_cmpk_gt_u32 s44, 0xff
	s_cbranch_scc1 .LBB10_31
	s_barrier

amdhsa.kernels:
  - .agpr_count:     16
    .args:
      - .actual_access:  read_only
        .address_space:  global
        .offset:         0
        .size:           8
        .value_kind:     global_buffer
      - .actual_access:  read_only
        .address_space:  global
        .offset:         8
        .size:           8
        .value_kind:     global_buffer
      - .actual_access:  write_only
        .address_space:  global
        .offset:         16
        .size:           8
        .value_kind:     global_buffer
    .group_segment_fixed_size: 45056
    .kernarg_segment_align: 8
    .kernarg_segment_size: 24
    .language:       OpenCL C
    .language_version:
      - 2
      - 0
    .max_flat_workgroup_size: 256
    .name:           _Z6k_attnPKDF16_PKfPDF16_
    .private_segment_fixed_size: 0
    .sgpr_count:     16
    .sgpr_spill_count: 0
    .symbol:         _Z6k_attnPKDF16_PKfPDF16_.kd
    .uniform_work_group_size: 1
    .uses_dynamic_stack: false
    .vgpr_count:     84
    .vgpr_spill_count: 0
    .wavefront_size: 64
  - .agpr_count:     0
    .args:
      - .actual_access:  read_only
        .address_space:  global
        .offset:         0
        .size:           8
        .value_kind:     global_buffer
      - .actual_access:  read_only
        .address_space:  global
        .offset:         8
        .size:           8
        .value_kind:     global_buffer
      - .actual_access:  write_only
        .address_space:  global
        .offset:         16
        .size:           8
        .value_kind:     global_buffer
      - .actual_access:  write_only
        .address_space:  global
        .offset:         24
        .size:           8
        .value_kind:     global_buffer
      - .actual_access:  write_only
        .address_space:  global
        .offset:         32
        .size:           8
        .value_kind:     global_buffer
      - .actual_access:  write_only
        .address_space:  global
        .offset:         40
        .size:           8
        .value_kind:     global_buffer
    .group_segment_fixed_size: 0
    .kernarg_segment_align: 8
    .kernarg_segment_size: 48
    .language:       OpenCL C
    .language_version:
      - 2
      - 0
    .max_flat_workgroup_size: 256
    .name:           _Z11k_prep_miscPKiPKfPfPDv2_fS3_S3_
    .private_segment_fixed_size: 0
    .sgpr_count:     16
    .sgpr_spill_count: 0
    .symbol:         _Z11k_prep_miscPKiPKfPfPDv2_fS3_S3_.kd
    .uniform_work_group_size: 1
    .uses_dynamic_stack: false
    .vgpr_count:     6
    .vgpr_spill_count: 0
    .wavefront_size: 64
  - .agpr_count:     0
    .args:
      - .actual_access:  read_only
        .address_space:  global
        .offset:         0
        .size:           8
        .value_kind:     global_buffer
      - .actual_access:  write_only
        .address_space:  global
        .offset:         8
        .size:           8
        .value_kind:     global_buffer
    .group_segment_fixed_size: 0
    .kernarg_segment_align: 8
    .kernarg_segment_size: 16
    .language:       OpenCL C
    .language_version:
      - 2
      - 0
    .max_flat_workgroup_size: 256
    .name:           _Z7k_cvt_xPKfPDF16_
    .private_segment_fixed_size: 0
    .sgpr_count:     14
    .sgpr_spill_count: 0
    .symbol:         _Z7k_cvt_xPKfPDF16_.kd
    .uniform_work_group_size: 1
    .uses_dynamic_stack: false
    .vgpr_count:     12
    .vgpr_spill_count: 0
    .wavefront_size: 64
  - .agpr_count:     0
    .args:
      - .offset:         0
        .size:           176
        .value_kind:     by_value
    .group_segment_fixed_size: 9216
    .kernarg_segment_align: 8
    .kernarg_segment_size: 176
    .language:       OpenCL C
    .language_version:
      - 2
      - 0
    .max_flat_workgroup_size: 256
    .name:           _Z8k_wtrans8PrepArgs
    .private_segment_fixed_size: 0
    .sgpr_count:     44
    .sgpr_spill_count: 0
    .symbol:         _Z8k_wtrans8PrepArgs.kd
    .uniform_work_group_size: 1
    .uses_dynamic_stack: false
    .vgpr_count:     18
    .vgpr_spill_count: 0
    .wavefront_size: 64
  - .agpr_count:     0
    .args:
      - .offset:         0
        .size:           176
        .value_kind:     by_value
      - .actual_access:  read_only
        .address_space:  global
        .offset:         176
        .size:           8
        .value_kind:     global_buffer
      - .actual_access:  read_only
        .address_space:  global
        .offset:         184
        .size:           8
        .value_kind:     global_buffer
    .group_segment_fixed_size: 2048
    .kernarg_segment_align: 8
    .kernarg_segment_size: 192
    .language:       OpenCL C
    .language_version:
      - 2
      - 0
    .max_flat_workgroup_size: 256
    .name:           _Z8k_colvec8PrepArgsPKfS1_
    .private_segment_fixed_size: 0
    .sgpr_count:     38
    .sgpr_spill_count: 0
    .symbol:         _Z8k_colvec8PrepArgsPKfS1_.kd
    .uniform_work_group_size: 1
    .uses_dynamic_stack: false
    .vgpr_count:     114
    .vgpr_spill_count: 0
    .wavefront_size: 64
  - .agpr_count:     0
    .args:
      - .actual_access:  read_only
        .address_space:  global
        .offset:         0
        .size:           8
        .value_kind:     global_buffer
      - .actual_access:  write_only
        .address_space:  global
        .offset:         8
        .size:           8
        .value_kind:     global_buffer
    .group_segment_fixed_size: 0
    .kernarg_segment_align: 8
    .kernarg_segment_size: 16
    .language:       OpenCL C
    .language_version:
      - 2
      - 0
    .max_flat_workgroup_size: 256
    .name:           _Z9k_rowstatPKDv2_fPS_
    .private_segment_fixed_size: 0
    .sgpr_count:     16
    .sgpr_spill_count: 0
    .symbol:         _Z9k_rowstatPKDv2_fPS_.kd
    .uniform_work_group_size: 1
    .uses_dynamic_stack: false
    .vgpr_count:     28
    .vgpr_spill_count: 0
    .wavefront_size: 64
  - .agpr_count:     0
    .args:
      - .actual_access:  read_only
        .address_space:  global
        .offset:         0
        .size:           8
        .value_kind:     global_buffer
      - .actual_access:  read_only
        .address_space:  global
        .offset:         8
        .size:           8
        .value_kind:     global_buffer
      - .actual_access:  read_only
        .address_space:  global
        .offset:         16
        .size:           8
        .value_kind:     global_buffer
      - .actual_access:  read_only
        .address_space:  global
        .offset:         24
        .size:           8
        .value_kind:     global_buffer
      - .actual_access:  write_only
        .address_space:  global
        .offset:         32
        .size:           8
        .value_kind:     global_buffer
    .group_segment_fixed_size: 0
    .kernarg_segment_align: 8
    .kernarg_segment_size: 40
    .language:       OpenCL C
    .language_version:
      - 2
      - 0
    .max_flat_workgroup_size: 256
    .name:           _Z10k_final_lnPKDF16_PKDv2_fPKfS5_Pf
    .private_segment_fixed_size: 0
    .sgpr_count:     19
    .sgpr_spill_count: 0
    .symbol:         _Z10k_final_lnPKDF16_PKDv2_fPKfS5_Pf.kd
    .uniform_work_group_size: 1
    .uses_dynamic_stack: false
    .vgpr_count:     19
    .vgpr_spill_count: 0
    .wavefront_size: 64
  - .agpr_count:     0
    .args:
      - .offset:         0
        .size:           32
        .value_kind:     by_value
      - .offset:         32
        .size:           32
        .value_kind:     by_value
      - .offset:         64
        .size:           4
        .value_kind:     hidden_block_count_x
      - .offset:         68
        .size:           4
        .value_kind:     hidden_block_count_y
      - .offset:         72
        .size:           4
        .value_kind:     hidden_block_count_z
      - .offset:         76
        .size:           2
        .value_kind:     hidden_group_size_x
      - .offset:         78
        .size:           2
        .value_kind:     hidden_group_size_y
      - .offset:         80
        .size:           2
        .value_kind:     hidden_group_size_z
      - .offset:         82
        .size:           2
        .value_kind:     hidden_remainder_x
      - .offset:         84
        .size:           2
        .value_kind:     hidden_remainder_y
      - .offset:         86
        .size:           2
        .value_kind:     hidden_remainder_z
      - .offset:         104
        .size:           8
        .value_kind:     hidden_global_offset_x
      - .offset:         112
        .size:           8
        .value_kind:     hidden_global_offset_y
      - .offset:         120
        .size:           8
        .value_kind:     hidden_global_offset_z
      - .offset:         128
        .size:           2
        .value_kind:     hidden_grid_dims
      - .offset:         184
        .size:           4
        .value_kind:     hidden_dynamic_lds_size
    .group_segment_fixed_size: 0
    .kernarg_segment_align: 8
    .kernarg_segment_size: 320
    .language:       OpenCL C
    .language_version:
      - 2
      - 0
    .max_flat_workgroup_size: 512
    .name:           _Z6k_gemmIN2pg6EpiLinILi0EEELi768EEvNS0_4GemmET_
    .private_segment_fixed_size: 0
    .sgpr_count:     88
    .sgpr_spill_count: 0
    .symbol:         _Z6k_gemmIN2pg6EpiLinILi0EEELi768EEvNS0_4GemmET_.kd
    .uniform_work_group_size: 1
    .uses_dynamic_stack: false
    .vgpr_count:     254
    .vgpr_spill_count: 0
    .wavefront_size: 64
  - .agpr_count:     0
    .args:
      - .offset:         0
        .size:           32
        .value_kind:     by_value
      - .offset:         32
        .size:           56
        .value_kind:     by_value
      - .offset:         88
        .size:           4
        .value_kind:     hidden_block_count_x
      - .offset:         92
        .size:           4
        .value_kind:     hidden_block_count_y
      - .offset:         96
        .size:           4
        .value_kind:     hidden_block_count_z
      - .offset:         100
        .size:           2
        .value_kind:     hidden_group_size_x
      - .offset:         102
        .size:           2
        .value_kind:     hidden_group_size_y
      - .offset:         104
        .size:           2
        .value_kind:     hidden_group_size_z
      - .offset:         106
        .size:           2
        .value_kind:     hidden_remainder_x
      - .offset:         108
        .size:           2
        .value_kind:     hidden_remainder_y
      - .offset:         110
        .size:           2
        .value_kind:     hidden_remainder_z
      - .offset:         128
        .size:           8
        .value_kind:     hidden_global_offset_x
      - .offset:         136
        .size:           8
        .value_kind:     hidden_global_offset_y
      - .offset:         144
        .size:           8
        .value_kind:     hidden_global_offset_z
      - .offset:         152
        .size:           2
        .value_kind:     hidden_grid_dims
      - .offset:         208
        .size:           4
        .value_kind:     hidden_dynamic_lds_size
    .group_segment_fixed_size: 0
    .kernarg_segment_align: 8
    .kernarg_segment_size: 344
    .language:       OpenCL C
    .language_version:
      - 2
      - 0
    .max_flat_workgroup_size: 512
    .name:           _Z6k_gemmIN2pg6EpiResELi768EEvNS0_4GemmET_
    .private_segment_fixed_size: 0
    .sgpr_count:     108
    .sgpr_spill_count: 0
    .symbol:         _Z6k_gemmIN2pg6EpiResELi768EEvNS0_4GemmET_.kd
    .uniform_work_group_size: 1
    .uses_dynamic_stack: false
    .vgpr_count:     256
    .vgpr_spill_count: 0
    .wavefront_size: 64
  - .agpr_count:     0
    .args:
      - .offset:         0
        .size:           32
        .value_kind:     by_value
      - .offset:         32
        .size:           32
        .value_kind:     by_value
      - .offset:         64
        .size:           4
        .value_kind:     hidden_block_count_x
      - .offset:         68
        .size:           4
        .value_kind:     hidden_block_count_y
      - .offset:         72
        .size:           4
        .value_kind:     hidden_block_count_z
      - .offset:         76
        .size:           2
        .value_kind:     hidden_group_size_x
      - .offset:         78
        .size:           2
        .value_kind:     hidden_group_size_y
      - .offset:         80
        .size:           2
        .value_kind:     hidden_group_size_z
      - .offset:         82
        .size:           2
        .value_kind:     hidden_remainder_x
      - .offset:         84
        .size:           2
        .value_kind:     hidden_remainder_y
      - .offset:         86
        .size:           2
        .value_kind:     hidden_remainder_z
      - .offset:         104
        .size:           8
        .value_kind:     hidden_global_offset_x
      - .offset:         112
        .size:           8
        .value_kind:     hidden_global_offset_y
      - .offset:         120
        .size:           8
        .value_kind:     hidden_global_offset_z
      - .offset:         128
        .size:           2
        .value_kind:     hidden_grid_dims
      - .offset:         184
        .size:           4
        .value_kind:     hidden_dynamic_lds_size
    .group_segment_fixed_size: 0
    .kernarg_segment_align: 8
    .kernarg_segment_size: 320
    .language:       OpenCL C
    .language_version:
      - 2
      - 0
    .max_flat_workgroup_size: 512
    .name:           _Z6k_gemmIN2pg6EpiLinILi1EEELi768EEvNS0_4GemmET_
    .private_segment_fixed_size: 0
    .sgpr_count:     88
    .sgpr_spill_count: 0
    .symbol:         _Z6k_gemmIN2pg6EpiLinILi1EEELi768EEvNS0_4GemmET_.kd
    .uniform_work_group_size: 1
    .uses_dynamic_stack: false
    .vgpr_count:     254
    .vgpr_spill_count: 0
    .wavefront_size: 64
  - .agpr_count:     0
    .args:
      - .offset:         0
        .size:           32
        .value_kind:     by_value
      - .offset:         32
        .size:           56
        .value_kind:     by_value
      - .offset:         88
        .size:           4
        .value_kind:     hidden_block_count_x
      - .offset:         92
        .size:           4
        .value_kind:     hidden_block_count_y
      - .offset:         96
        .size:           4
        .value_kind:     hidden_block_count_z
      - .offset:         100
        .size:           2
        .value_kind:     hidden_group_size_x
      - .offset:         102
        .size:           2
        .value_kind:     hidden_group_size_y
      - .offset:         104
        .size:           2
        .value_kind:     hidden_group_size_z
      - .offset:         106
        .size:           2
        .value_kind:     hidden_remainder_x
      - .offset:         108
        .size:           2
        .value_kind:     hidden_remainder_y
      - .offset:         110
        .size:           2
        .value_kind:     hidden_remainder_z
      - .offset:         128
        .size:           8
        .value_kind:     hidden_global_offset_x
      - .offset:         136
        .size:           8
        .value_kind:     hidden_global_offset_y
      - .offset:         144
        .size:           8
        .value_kind:     hidden_global_offset_z
      - .offset:         152
        .size:           2
        .value_kind:     hidden_grid_dims
      - .offset:         208
        .size:           4
        .value_kind:     hidden_dynamic_lds_size
    .group_segment_fixed_size: 0
    .kernarg_segment_align: 8
    .kernarg_segment_size: 344
    .language:       OpenCL C
    .language_version:
      - 2
      - 0
    .max_flat_workgroup_size: 512
    .name:           _Z6k_gemmIN2pg6EpiResELi3072EEvNS0_4GemmET_
    .private_segment_fixed_size: 0
    .sgpr_count:     108
    .sgpr_spill_count: 0
    .symbol:         _Z6k_gemmIN2pg6EpiResELi3072EEvNS0_4GemmET_.kd
    .uniform_work_group_size: 1
    .uses_dynamic_stack: false
    .vgpr_count:     256
    .vgpr_spill_count: 0
    .wavefront_size: 64
